# best3: accumulate chains + static prio waves 0-3 + compiler vmcnt(0) and redundant lgkmcnt(0) at compute heads dropped
# speedup vs baseline: 1.0146x; 1.0008x over previous
;     __device__ bool next(int i, Unit& u) const { const int rounds = nwg / G; if (i >= rounds) return false; return StaticOrder::next(rounds - 1 - i, u); }
;     __device__ bool next(int i, Unit& u) const { const int rounds = nwg / G; if (i >= 2 * rounds) return false; const bool ok = StaticOrder::next(i >= rounds ? i - rounds : i, u); u.z = (i >= rounds) ? 1 : 0; return ok; }
; #define PG8_TRIP_HEAD(T) const int t = (T); const bool last = (t == nt - 2); \
;             const char* a1 = cA + (size_t)(t + 1) * kstep; \
;             const char* a2 = last ? nA : cA + (size_t)(t + 2) * kstep; const char* b2 = last ? nB : cB + (size_t)(t + 2) * kstep; \
;             const char* a3 = a2 + kstep; const char* b3 = b2 + kstep; \
;             if (last && has_next) S.a_ready(nxt);
; template <class Epi, class Sched, bool ALIGN_EPI = false, bool SP2 = false>
; __device__ __forceinline__ void gemm_phase(PG8_LAS unsigned char* lds, const Gemm g, const Sched& S, const Epi& E) {
;     ...
;         const bool has_next = S.next(ui + 1, nxt);
;         const char* nA = has_next ? (const char*)S.opA(g, nxt) + (size_t)nxt.pm * tstepA : cA; const char* nB = has_next ? (const char*)S.opB(g, nxt) + (size_t)nxt.pn * tstepB : cB;
;     ...
;         if constexpr (SP2) {
;             { PG8_TRIP_HEAD(0) PG8_TRIP_SP2(asm volatile("s_waitcnt vmcnt(%0)" :: "n"(8 + Epi::NST) : "memory"), PG8_MMAZ) }
.LBB0_129:
	s_ashr_i32 s23, s22, 31
	s_lshl_b64 s[4:5], s[22:23], 20
	s_add_u32 s26, s34, s4
	s_addc_u32 s27, s35, s5
	s_add_i32 s45, 0, 0x10000
	s_add_i32 s47, 0, 0x14000
	v_add_u32_e32 v140, s45, v160
	v_add_u32_e32 v141, s47, v160
	ds_read_b128 v[4:7], v140
	ds_read_b128 v[8:11], v140 offset:1024
	ds_read_b128 v[12:15], v140 offset:2048
	ds_read_b128 v[16:19], v140 offset:3072
	ds_read_b128 v[20:23], v141
	ds_read_b128 v[24:27], v141 offset:1024
	ds_read_b128 v[28:31], v141 offset:2048
	ds_read_b128 v[32:35], v141 offset:3072
	s_and_b64 s[4:5], s[10:11], exec
	s_cselect_b32 s4, s27, s29
	s_cselect_b32 s5, s26, s28
	v_lshl_add_u64 v[184:185], s[30:31], 0, v[134:135]
	s_mov_b64 s[10:11], 0x84080
	s_add_i32 s23, s37, 0xc000
	v_lshl_add_u64 v[68:69], v[184:185], 0, s[10:11]
	s_mov_b32 m0, s23
	s_mov_b64 s[10:11], 0xc6080
	s_add_i32 s33, s37, 0xe000
	ds_read_b128 v[36:39], v163
	ds_read_b128 v[40:43], v163 offset:1024
	ds_read_b128 v[44:47], v163 offset:2048
	ds_read_b128 v[48:51], v163 offset:3072
	ds_read_b128 v[52:55], v163 offset:4096
	ds_read_b128 v[56:59], v163 offset:5120
	ds_read_b128 v[60:63], v163 offset:6144
	ds_read_b128 v[64:67], v163 offset:7168
	global_load_lds_dwordx4 v[68:69], off
	v_lshl_add_u64 v[68:69], v[184:185], 0, s[10:11]
	s_mov_b32 m0, s33
	s_nop 0
	global_load_lds_dwordx4 v[68:69], off
	s_waitcnt vmcnt(16)
	s_waitcnt lgkmcnt(0)
	s_barrier
	v_mfma_f32_16x16x32_bf16 v[88:91], v[12:15], v[52:55], 0
	v_mfma_f32_16x16x32_bf16 v[92:95], v[16:19], v[56:59], v[88:91]
	v_mfma_f32_16x16x32_bf16 v[88:91], v[4:7], v[60:63], 0
	v_mfma_f32_16x16x32_bf16 v[68:71], v[4:7], v[36:39], 0
	v_mfma_f32_16x16x32_bf16 v[72:75], v[12:15], v[36:39], 0
	v_mfma_f32_16x16x32_bf16 v[76:79], v[4:7], v[44:47], 0
	v_mfma_f32_16x16x32_bf16 v[80:83], v[12:15], v[44:47], 0
	v_mfma_f32_16x16x32_bf16 v[84:87], v[4:7], v[52:55], 0
	v_mfma_f32_16x16x32_bf16 v[96:99], v[8:11], v[64:67], v[88:91]
	v_mfma_f32_16x16x32_bf16 v[88:91], v[12:15], v[60:63], 0
	v_mfma_f32_16x16x32_bf16 v[68:71], v[8:11], v[40:43], v[68:71]
	v_mfma_f32_16x16x32_bf16 v[72:75], v[16:19], v[40:43], v[72:75]
	v_mfma_f32_16x16x32_bf16 v[76:79], v[8:11], v[48:51], v[76:79]
	v_mfma_f32_16x16x32_bf16 v[80:83], v[16:19], v[48:51], v[80:83]
	v_mfma_f32_16x16x32_bf16 v[84:87], v[8:11], v[56:59], v[84:87]
	v_mfma_f32_16x16x32_bf16 v[108:111], v[16:19], v[64:67], v[88:91]
	v_mfma_f32_16x16x32_bf16 v[88:91], v[20:23], v[36:39], 0
	v_mfma_f32_16x16x32_bf16 v[36:39], v[28:31], v[36:39], 0
	v_mfma_f32_16x16x32_bf16 v[112:115], v[24:27], v[40:43], v[88:91]
	v_mfma_f32_16x16x32_bf16 v[36:39], v[32:35], v[40:43], v[36:39]
	v_mfma_f32_16x16x32_bf16 v[40:43], v[20:23], v[44:47], 0
	v_mfma_f32_16x16x32_bf16 v[44:47], v[28:31], v[44:47], 0
	v_mfma_f32_16x16x32_bf16 v[40:43], v[24:27], v[48:51], v[40:43]
	v_mfma_f32_16x16x32_bf16 v[44:47], v[32:35], v[48:51], v[44:47]
	v_mfma_f32_16x16x32_bf16 v[48:51], v[20:23], v[52:55], 0
	v_mfma_f32_16x16x32_bf16 v[52:55], v[28:31], v[52:55], 0
	v_mfma_f32_16x16x32_bf16 v[48:51], v[24:27], v[56:59], v[48:51]
	v_mfma_f32_16x16x32_bf16 v[52:55], v[32:35], v[56:59], v[52:55]
	v_mfma_f32_16x16x32_bf16 v[56:59], v[20:23], v[60:63], 0
	v_mfma_f32_16x16x32_bf16 v[60:63], v[28:31], v[60:63], 0
	v_mfma_f32_16x16x32_bf16 v[56:59], v[24:27], v[64:67], v[56:59]
	v_mfma_f32_16x16x32_bf16 v[60:63], v[32:35], v[64:67], v[60:63]
	s_barrier
	v_lshl_add_u64 v[186:187], s[28:29], 0, v[132:133]
	s_mov_b64 s[10:11], 0x100
	s_add_i32 s45, s45, s36
	v_lshl_add_u64 v[142:143], v[186:187], 0, s[10:11]
	s_mov_b32 m0, s45
	s_mov_b64 s[48:49], 0x40100
	s_add_i32 s46, s45, 0x2000
	ds_read_b128 v[64:67], v163 offset:16384
	ds_read_b128 v[88:91], v163 offset:17408
	ds_read_b128 v[100:103], v163 offset:18432
	ds_read_b128 v[104:107], v163 offset:19456
	ds_read_b128 v[116:119], v163 offset:20480
	ds_read_b128 v[120:123], v163 offset:21504
	ds_read_b128 v[124:127], v163 offset:22528
	ds_read_b128 v[128:131], v163 offset:23552
	global_load_lds_dwordx4 v[142:143], off
	v_lshl_add_u64 v[142:143], v[186:187], 0, s[48:49]
	s_mov_b32 m0, s46
	s_mov_b64 s[48:49], 0x80100
	s_add_i32 s47, s47, s36
	global_load_lds_dwordx4 v[142:143], off
	v_lshl_add_u64 v[142:143], v[186:187], 0, s[48:49]
	s_mov_b32 m0, s47
	s_mov_b64 s[48:49], 0xc0100
	global_load_lds_dwordx4 v[142:143], off
	v_lshl_add_u64 v[142:143], v[186:187], 0, s[48:49]
	s_add_i32 s48, s47, 0x2000
	s_mov_b32 m0, s48
	s_nop 0
	global_load_lds_dwordx4 v[142:143], off
	v_lshl_add_u64 v[142:143], v[184:185], 0, s[10:11]
	s_mov_b32 m0, s37
	s_mov_b64 s[10:11], 0x42100
	global_load_lds_dwordx4 v[142:143], off
	v_lshl_add_u64 v[142:143], v[184:185], 0, s[10:11]
	s_mov_b32 m0, s38
	s_nop 0
	global_load_lds_dwordx4 v[142:143], off
	s_waitcnt vmcnt(16)
	s_waitcnt lgkmcnt(0)
	s_barrier
; #define PG8_TRIP_HEAD(T) const int t = (T); const bool last = (t == nt - 2); \
;             const char* a1 = cA + (size_t)(t + 1) * kstep; \
;             const char* a2 = last ? nA : cA + (size_t)(t + 2) * kstep; const char* b2 = last ? nB : cB + (size_t)(t + 2) * kstep; \
;             const char* a3 = a2 + kstep; const char* b3 = b2 + kstep; \
;             if (last && has_next) S.a_ready(nxt);
; template <class Epi, class Sched, bool ALIGN_EPI = false, bool SP2 = false>
; __device__ __forceinline__ void gemm_phase(PG8_LAS unsigned char* lds, const Gemm g, const Sched& S, const Epi& E) {
;     ...
;         if constexpr (SP2) {
;             { PG8_TRIP_HEAD(0) PG8_TRIP_SP2(asm volatile("s_waitcnt vmcnt(%0)" :: "n"(8 + Epi::NST) : "memory"), PG8_MMAZ) }
	v_mfma_f32_16x16x32_bf16 v[142:145], v[4:7], v[64:67], 0
	v_mfma_f32_16x16x32_bf16 v[152:155], v[4:7], v[100:103], 0
	v_mfma_f32_16x16x32_bf16 v[164:167], v[4:7], v[116:119], 0
	v_mfma_f32_16x16x32_bf16 v[4:7], v[4:7], v[124:127], 0
	v_mfma_f32_16x16x32_bf16 v[144:147], v[8:11], v[88:91], v[142:145]
	v_mfma_f32_16x16x32_bf16 v[152:155], v[8:11], v[104:107], v[152:155]
	v_mfma_f32_16x16x32_bf16 v[164:167], v[8:11], v[120:123], v[164:167]
	v_mfma_f32_16x16x32_bf16 v[4:7], v[8:11], v[128:131], v[4:7]
	v_mfma_f32_16x16x32_bf16 v[8:11], v[12:15], v[124:127], 0
	v_mfma_f32_16x16x32_bf16 v[148:151], v[12:15], v[64:67], 0
	v_mfma_f32_16x16x32_bf16 v[156:159], v[12:15], v[100:103], 0
	v_mfma_f32_16x16x32_bf16 v[168:171], v[12:15], v[116:119], 0
	v_mfma_f32_16x16x32_bf16 v[12:15], v[16:19], v[128:131], v[8:11]
	v_mfma_f32_16x16x32_bf16 v[148:151], v[16:19], v[88:91], v[148:151]
	v_mfma_f32_16x16x32_bf16 v[156:159], v[16:19], v[104:107], v[156:159]
	v_mfma_f32_16x16x32_bf16 v[168:171], v[16:19], v[120:123], v[168:171]
	v_mfma_f32_16x16x32_bf16 v[8:11], v[20:23], v[64:67], 0
	v_mfma_f32_16x16x32_bf16 v[16:19], v[24:27], v[88:91], v[8:11]
	v_mfma_f32_16x16x32_bf16 v[8:11], v[28:31], v[64:67], 0
	v_mfma_f32_16x16x32_bf16 v[172:175], v[32:35], v[88:91], v[8:11]
	v_mfma_f32_16x16x32_bf16 v[8:11], v[20:23], v[100:103], 0
	v_mfma_f32_16x16x32_bf16 v[176:179], v[24:27], v[104:107], v[8:11]
	v_mfma_f32_16x16x32_bf16 v[8:11], v[28:31], v[100:103], 0
	v_mfma_f32_16x16x32_bf16 v[194:197], v[32:35], v[104:107], v[8:11]
	v_mfma_f32_16x16x32_bf16 v[8:11], v[20:23], v[116:119], 0
	v_mfma_f32_16x16x32_bf16 v[198:201], v[24:27], v[120:123], v[8:11]
	v_mfma_f32_16x16x32_bf16 v[8:11], v[28:31], v[116:119], 0
	v_mfma_f32_16x16x32_bf16 v[202:205], v[32:35], v[120:123], v[8:11]
	v_mfma_f32_16x16x32_bf16 v[8:11], v[20:23], v[124:127], 0
	v_mfma_f32_16x16x32_bf16 v[206:209], v[24:27], v[128:131], v[8:11]
	v_mfma_f32_16x16x32_bf16 v[8:11], v[28:31], v[124:127], 0
	v_mfma_f32_16x16x32_bf16 v[220:223], v[32:35], v[128:131], v[8:11]
	s_barrier
	s_add_i32 s49, 0, 0x18000
	s_add_i32 s51, 0, 0x1c000
	v_add_u32_e32 v142, s49, v160
	v_add_u32_e32 v143, s51, v160
	s_nop 0
	ds_read_b128 v[8:11], v142
	ds_read_b128 v[28:31], v142 offset:1024
	ds_read_b128 v[32:35], v142 offset:2048
	ds_read_b128 v[64:67], v142 offset:3072
	ds_read_b128 v[224:227], v143
	ds_read_b128 v[228:231], v143 offset:1024
	ds_read_b128 v[232:235], v143 offset:2048
	ds_read_b128 v[236:239], v143 offset:3072
	s_mov_b64 s[10:11], 0x84100
	s_mov_b32 m0, s39
	v_lshl_add_u64 v[88:89], v[184:185], 0, s[10:11]
	s_mov_b64 s[10:11], 0xc6100
	ds_read_b128 v[20:23], v163 offset:32768
	ds_read_b128 v[24:27], v163 offset:33792
	ds_read_b128 v[240:243], v163 offset:34816
	ds_read_b128 v[244:247], v163 offset:35840
	ds_read_b128 v[248:251], v163 offset:36864
	ds_read_b128 v[216:219], v163 offset:37888
	ds_read_b128 v[190:193], v163 offset:38912
	ds_read_b128 v[180:183], v163 offset:39936
	global_load_lds_dwordx4 v[88:89], off
	v_lshl_add_u64 v[88:89], v[184:185], 0, s[10:11]
	s_mov_b32 m0, s40
	s_nop 0
	global_load_lds_dwordx4 v[88:89], off
	s_waitcnt vmcnt(8)
	s_waitcnt lgkmcnt(0)
	s_barrier
	v_mfma_f32_16x16x32_bf16 v[68:71], v[8:11], v[20:23], v[68:71]
	v_mfma_f32_16x16x32_bf16 v[120:123], v[28:31], v[24:27], v[68:71]
	v_mfma_f32_16x16x32_bf16 v[68:71], v[32:35], v[20:23], v[72:75]
	v_mfma_f32_16x16x32_bf16 v[116:119], v[64:67], v[24:27], v[68:71]
	v_mfma_f32_16x16x32_bf16 v[68:71], v[8:11], v[240:243], v[76:79]
	v_mfma_f32_16x16x32_bf16 v[104:107], v[28:31], v[244:247], v[68:71]
	v_mfma_f32_16x16x32_bf16 v[68:71], v[32:35], v[240:243], v[80:83]
	v_mfma_f32_16x16x32_bf16 v[100:103], v[64:67], v[244:247], v[68:71]
	v_mfma_f32_16x16x32_bf16 v[68:71], v[8:11], v[248:251], v[84:87]
	v_mfma_f32_16x16x32_bf16 v[88:91], v[28:31], v[216:219], v[68:71]
	v_mfma_f32_16x16x32_bf16 v[68:71], v[32:35], v[248:251], v[92:95]
	v_mfma_f32_16x16x32_bf16 v[84:87], v[64:67], v[216:219], v[68:71]
	v_mfma_f32_16x16x32_bf16 v[68:71], v[8:11], v[190:193], v[96:99]
	v_mfma_f32_16x16x32_bf16 v[72:75], v[28:31], v[180:183], v[68:71]
	v_mfma_f32_16x16x32_bf16 v[68:71], v[32:35], v[190:193], v[108:111]
	v_mfma_f32_16x16x32_bf16 v[68:71], v[64:67], v[180:183], v[68:71]
	v_mfma_f32_16x16x32_bf16 v[76:79], v[224:227], v[20:23], v[112:115]
	v_mfma_f32_16x16x32_bf16 v[20:23], v[232:235], v[20:23], v[36:39]
	v_mfma_f32_16x16x32_bf16 v[124:127], v[236:239], v[24:27], v[20:23]
	v_mfma_f32_16x16x32_bf16 v[20:23], v[224:227], v[240:243], v[40:43]
	v_mfma_f32_16x16x32_bf16 v[112:115], v[228:231], v[244:247], v[20:23]
	v_mfma_f32_16x16x32_bf16 v[20:23], v[232:235], v[240:243], v[44:47]
	v_mfma_f32_16x16x32_bf16 v[108:111], v[236:239], v[244:247], v[20:23]
	v_mfma_f32_16x16x32_bf16 v[20:23], v[224:227], v[248:251], v[48:51]
	v_mfma_f32_16x16x32_bf16 v[96:99], v[228:231], v[216:219], v[20:23]
	v_mfma_f32_16x16x32_bf16 v[20:23], v[232:235], v[248:251], v[52:55]
	v_mfma_f32_16x16x32_bf16 v[92:95], v[236:239], v[216:219], v[20:23]
	v_mfma_f32_16x16x32_bf16 v[20:23], v[224:227], v[190:193], v[56:59]
	v_mfma_f32_16x16x32_bf16 v[80:83], v[228:231], v[180:183], v[20:23]
	v_mfma_f32_16x16x32_bf16 v[20:23], v[232:235], v[190:193], v[60:63]
	v_mfma_f32_16x16x32_bf16 v[128:131], v[228:231], v[24:27], v[76:79]
	v_mfma_f32_16x16x32_bf16 v[76:79], v[236:239], v[180:183], v[20:23]
	s_barrier
; #define PG8_MMA(ai, bj, At, Bt) do { __builtin_amdgcn_s_setprio(1); _Pragma("unroll") for (int m = 0; m < 4; ++m) _Pragma("unroll") for (int n = 0; n < 2; ++n) _Pragma("unroll") for (int k = 0; k < 2; ++k) \
;         acc[ai][bj][m][n] = __builtin_amdgcn_mfma_f32_16x16x32_bf16(Bt[n][k], At[m][k], acc[ai][bj][m][n], 0, 0, 0); __builtin_amdgcn_s_setprio(0); } while (0)
; #define PG8_WAIT_V(n) asm volatile("s_waitcnt vmcnt(" #n ")" ::: "memory")
; #define PG8_TRIP_HEAD(T) const int t = (T); const bool last = (t == nt - 2); \
;             const char* a1 = cA + (size_t)(t + 1) * kstep; \
;             const char* a2 = last ? nA : cA + (size_t)(t + 2) * kstep; const char* b2 = last ? nB : cB + (size_t)(t + 2) * kstep; \
;             const char* a3 = a2 + kstep; const char* b3 = b2 + kstep; \
;             if (last && has_next) S.a_ready(nxt);
; template <class Epi, class Sched, bool ALIGN_EPI = false, bool SP2 = false>
; __device__ __forceinline__ void gemm_phase(PG8_LAS unsigned char* lds, const Gemm g, const Sched& S, const Epi& E) {
;     ...
;         if constexpr (SP2) {
;             { PG8_TRIP_HEAD(0) PG8_TRIP_SP2(asm volatile("s_waitcnt vmcnt(%0)" :: "n"(8 + Epi::NST) : "memory"), PG8_MMAZ) }
;             for (int tt = 2; tt < nt; tt += 2) { PG8_TRIP_HEAD(tt) PG8_TRIP_SP2(PG8_WAIT_V(8), PG8_MMA) }
	s_mov_b64 s[10:11], 0x180
	s_add_i32 s49, s49, s36
	s_nop 1
	v_lshl_add_u64 v[20:21], v[186:187], 0, s[10:11]
	s_mov_b32 m0, s49
	s_mov_b64 s[52:53], 0x40180
	s_add_i32 s50, s49, 0x2000
	ds_read_b128 v[44:47], v163 offset:49152
	ds_read_b128 v[48:51], v163 offset:50176
	ds_read_b128 v[180:183], v163 offset:51200
	ds_read_b128 v[190:193], v163 offset:52224
	ds_read_b128 v[216:219], v163 offset:53248
	ds_read_b128 v[240:243], v163 offset:54272
	ds_read_b128 v[244:247], v163 offset:55296
	ds_read_b128 v[248:251], v163 offset:56320
	global_load_lds_dwordx4 v[20:21], off
	v_lshl_add_u64 v[20:21], v[186:187], 0, s[52:53]
	s_mov_b32 m0, s50
	s_mov_b64 s[52:53], 0x80180
	s_add_i32 s51, s51, s36
	global_load_lds_dwordx4 v[20:21], off
	v_lshl_add_u64 v[20:21], v[186:187], 0, s[52:53]
	s_mov_b32 m0, s51
	s_mov_b64 s[52:53], 0xc0180
	global_load_lds_dwordx4 v[20:21], off
	v_lshl_add_u64 v[20:21], v[186:187], 0, s[52:53]
	s_add_i32 s52, s51, 0x2000
	s_mov_b32 m0, s52
	s_nop 0
	global_load_lds_dwordx4 v[20:21], off
	v_lshl_add_u64 v[20:21], v[184:185], 0, s[10:11]
	s_mov_b32 m0, s0
	s_mov_b64 s[10:11], 0x42180
	global_load_lds_dwordx4 v[20:21], off
	v_lshl_add_u64 v[20:21], v[184:185], 0, s[10:11]
	s_mov_b32 m0, s41
	s_nop 0
	global_load_lds_dwordx4 v[20:21], off
	s_waitcnt vmcnt(8)
	s_waitcnt lgkmcnt(0)
	s_barrier
	v_mfma_f32_16x16x32_bf16 v[20:23], v[8:11], v[44:47], v[144:147]
	v_mfma_f32_16x16x32_bf16 v[56:59], v[28:31], v[48:51], v[20:23]
	v_mfma_f32_16x16x32_bf16 v[20:23], v[32:35], v[44:47], v[148:151]
	v_mfma_f32_16x16x32_bf16 v[52:55], v[64:67], v[48:51], v[20:23]
	v_mfma_f32_16x16x32_bf16 v[20:23], v[8:11], v[180:183], v[152:155]
	v_mfma_f32_16x16x32_bf16 v[40:43], v[28:31], v[190:193], v[20:23]
	v_mfma_f32_16x16x32_bf16 v[20:23], v[32:35], v[180:183], v[156:159]
	v_mfma_f32_16x16x32_bf16 v[36:39], v[64:67], v[190:193], v[20:23]
	v_mfma_f32_16x16x32_bf16 v[20:23], v[8:11], v[216:219], v[164:167]
	v_mfma_f32_16x16x32_bf16 v[4:7], v[8:11], v[244:247], v[4:7]
	v_mfma_f32_16x16x32_bf16 v[24:27], v[28:31], v[240:243], v[20:23]
	v_mfma_f32_16x16x32_bf16 v[20:23], v[32:35], v[216:219], v[168:171]
	v_mfma_f32_16x16x32_bf16 v[8:11], v[28:31], v[248:251], v[4:7]
	v_mfma_f32_16x16x32_bf16 v[4:7], v[32:35], v[244:247], v[12:15]
	v_mfma_f32_16x16x32_bf16 v[20:23], v[64:67], v[240:243], v[20:23]
	v_mfma_f32_16x16x32_bf16 v[4:7], v[64:67], v[248:251], v[4:7]
	v_mfma_f32_16x16x32_bf16 v[12:15], v[224:227], v[44:47], v[16:19]
	v_mfma_f32_16x16x32_bf16 v[64:67], v[228:231], v[48:51], v[12:15]
	v_mfma_f32_16x16x32_bf16 v[12:15], v[232:235], v[44:47], v[172:175]
	v_mfma_f32_16x16x32_bf16 v[60:63], v[236:239], v[48:51], v[12:15]
	v_mfma_f32_16x16x32_bf16 v[12:15], v[224:227], v[180:183], v[176:179]
	v_mfma_f32_16x16x32_bf16 v[48:51], v[228:231], v[190:193], v[12:15]
	v_mfma_f32_16x16x32_bf16 v[12:15], v[232:235], v[180:183], v[194:197]
	v_mfma_f32_16x16x32_bf16 v[44:47], v[236:239], v[190:193], v[12:15]
	v_mfma_f32_16x16x32_bf16 v[12:15], v[224:227], v[216:219], v[198:201]
	v_mfma_f32_16x16x32_bf16 v[32:35], v[228:231], v[240:243], v[12:15]
	v_mfma_f32_16x16x32_bf16 v[12:15], v[232:235], v[216:219], v[202:205]
	v_mfma_f32_16x16x32_bf16 v[28:31], v[236:239], v[240:243], v[12:15]
	v_mfma_f32_16x16x32_bf16 v[12:15], v[224:227], v[244:247], v[206:209]
	v_mfma_f32_16x16x32_bf16 v[16:19], v[228:231], v[248:251], v[12:15]
	v_mfma_f32_16x16x32_bf16 v[12:15], v[232:235], v[244:247], v[220:223]
	v_mfma_f32_16x16x32_bf16 v[12:15], v[236:239], v[248:251], v[12:15]
	s_barrier
	s_add_u32 s10, s30, 0x84180
	s_addc_u32 s11, s31, 0
	s_add_u32 s28, s28, 0x200
	s_addc_u32 s29, s29, 0
	s_mov_b32 s30, 0
	s_mov_b64 s[60:61], 0x80000
	s_mov_b64 s[62:63], 0x80080
	s_mov_b64 s[64:65], 0xc0000
	s_mov_b64 s[66:67], 0xc0080
	s_mov_b64 s[68:69], 0xc6000
.LBB0_130:
	ds_read_b128 v[144:147], v140
	ds_read_b128 v[148:151], v140 offset:1024
	ds_read_b128 v[152:155], v140 offset:2048
	ds_read_b128 v[156:159], v140 offset:3072
	ds_read_b128 v[164:167], v141
	ds_read_b128 v[168:171], v141 offset:1024
	ds_read_b128 v[172:175], v141 offset:2048
	ds_read_b128 v[176:179], v141 offset:3072
	s_add_u32 s31, s10, 0xfff7c080
	s_addc_u32 s53, s11, -1
	s_cmp_eq_u32 s30, 28
	s_cselect_b32 s55, s25, s53
	s_cselect_b32 s54, s24, s31
	s_cselect_b32 s57, s4, s29
	s_cselect_b32 s56, s5, s28
	s_mov_b32 m0, s23
	v_lshl_add_u64 v[184:185], s[10:11], 0, v[138:139]
	ds_read_b128 v[180:183], v163
	ds_read_b128 v[190:193], v163 offset:1024
	ds_read_b128 v[194:197], v163 offset:2048
	ds_read_b128 v[198:201], v163 offset:3072
	ds_read_b128 v[202:205], v163 offset:4096
	ds_read_b128 v[206:209], v163 offset:5120
	ds_read_b128 v[216:219], v163 offset:6144
	ds_read_b128 v[220:223], v163 offset:7168
	global_load_lds_dwordx4 v[184:185], off
	v_lshl_add_u64 v[184:185], v[184:185], 0, s[96:97]
	s_mov_b32 m0, s33
	s_nop 0
	global_load_lds_dwordx4 v[184:185], off
	s_waitcnt vmcnt(8)
	s_waitcnt lgkmcnt(0)
	s_barrier
; #define PG8_MMA(ai, bj, At, Bt) do { __builtin_amdgcn_s_setprio(1); _Pragma("unroll") for (int m = 0; m < 4; ++m) _Pragma("unroll") for (int n = 0; n < 2; ++n) _Pragma("unroll") for (int k = 0; k < 2; ++k) \
;         acc[ai][bj][m][n] = __builtin_amdgcn_mfma_f32_16x16x32_bf16(Bt[n][k], At[m][k], acc[ai][bj][m][n], 0, 0, 0); __builtin_amdgcn_s_setprio(0); } while (0)
; #define PG8_WAIT_V(n) asm volatile("s_waitcnt vmcnt(" #n ")" ::: "memory")
; #define PG8_TRIP_HEAD(T) const int t = (T); const bool last = (t == nt - 2); \
;             const char* a1 = cA + (size_t)(t + 1) * kstep; \
;             const char* a2 = last ? nA : cA + (size_t)(t + 2) * kstep; const char* b2 = last ? nB : cB + (size_t)(t + 2) * kstep; \
;             const char* a3 = a2 + kstep; const char* b3 = b2 + kstep; \
;             if (last && has_next) S.a_ready(nxt);
; template <class Epi, class Sched, bool ALIGN_EPI = false, bool SP2 = false>
; __device__ __forceinline__ void gemm_phase(PG8_LAS unsigned char* lds, const Gemm g, const Sched& S, const Epi& E) {
;     ...
;         if constexpr (SP2) {
;             { PG8_TRIP_HEAD(0) PG8_TRIP_SP2(asm volatile("s_waitcnt vmcnt(%0)" :: "n"(8 + Epi::NST) : "memory"), PG8_MMAZ) }
;             for (int tt = 2; tt < nt; tt += 2) { PG8_TRIP_HEAD(tt) PG8_TRIP_SP2(PG8_WAIT_V(8), PG8_MMA) }
	v_mfma_f32_16x16x32_bf16 v[120:123], v[144:147], v[180:183], v[120:123]
	v_mfma_f32_16x16x32_bf16 v[120:123], v[148:151], v[190:193], v[120:123]
	v_mfma_f32_16x16x32_bf16 v[116:119], v[152:155], v[180:183], v[116:119]
	v_mfma_f32_16x16x32_bf16 v[116:119], v[156:159], v[190:193], v[116:119]
	v_mfma_f32_16x16x32_bf16 v[104:107], v[144:147], v[194:197], v[104:107]
	v_mfma_f32_16x16x32_bf16 v[104:107], v[148:151], v[198:201], v[104:107]
	v_mfma_f32_16x16x32_bf16 v[100:103], v[152:155], v[194:197], v[100:103]
	v_mfma_f32_16x16x32_bf16 v[100:103], v[156:159], v[198:201], v[100:103]
	v_mfma_f32_16x16x32_bf16 v[88:91], v[144:147], v[202:205], v[88:91]
	v_mfma_f32_16x16x32_bf16 v[88:91], v[148:151], v[206:209], v[88:91]
	v_mfma_f32_16x16x32_bf16 v[84:87], v[152:155], v[202:205], v[84:87]
	v_mfma_f32_16x16x32_bf16 v[84:87], v[156:159], v[206:209], v[84:87]
	v_mfma_f32_16x16x32_bf16 v[72:75], v[144:147], v[216:219], v[72:75]
	v_mfma_f32_16x16x32_bf16 v[72:75], v[148:151], v[220:223], v[72:75]
	v_mfma_f32_16x16x32_bf16 v[68:71], v[152:155], v[216:219], v[68:71]
	v_mfma_f32_16x16x32_bf16 v[68:71], v[156:159], v[220:223], v[68:71]
	v_mfma_f32_16x16x32_bf16 v[128:131], v[164:167], v[180:183], v[128:131]
	v_mfma_f32_16x16x32_bf16 v[128:131], v[168:171], v[190:193], v[128:131]
	v_mfma_f32_16x16x32_bf16 v[124:127], v[172:175], v[180:183], v[124:127]
	v_mfma_f32_16x16x32_bf16 v[124:127], v[176:179], v[190:193], v[124:127]
	v_mfma_f32_16x16x32_bf16 v[112:115], v[164:167], v[194:197], v[112:115]
	v_mfma_f32_16x16x32_bf16 v[112:115], v[168:171], v[198:201], v[112:115]
	v_mfma_f32_16x16x32_bf16 v[108:111], v[172:175], v[194:197], v[108:111]
	v_mfma_f32_16x16x32_bf16 v[108:111], v[176:179], v[198:201], v[108:111]
	v_mfma_f32_16x16x32_bf16 v[96:99], v[164:167], v[202:205], v[96:99]
	v_mfma_f32_16x16x32_bf16 v[96:99], v[168:171], v[206:209], v[96:99]
	v_mfma_f32_16x16x32_bf16 v[92:95], v[172:175], v[202:205], v[92:95]
	v_mfma_f32_16x16x32_bf16 v[92:95], v[176:179], v[206:209], v[92:95]
	v_mfma_f32_16x16x32_bf16 v[80:83], v[164:167], v[216:219], v[80:83]
	v_mfma_f32_16x16x32_bf16 v[80:83], v[168:171], v[220:223], v[80:83]
	v_mfma_f32_16x16x32_bf16 v[76:79], v[172:175], v[216:219], v[76:79]
	v_mfma_f32_16x16x32_bf16 v[76:79], v[176:179], v[220:223], v[76:79]
	s_barrier
	s_mov_b32 m0, s45
	v_lshl_add_u64 v[184:185], s[56:57], 0, v[132:133]
	ds_read_b128 v[180:183], v163 offset:16384
	ds_read_b128 v[190:193], v163 offset:17408
	ds_read_b128 v[194:197], v163 offset:18432
	ds_read_b128 v[198:201], v163 offset:19456
	ds_read_b128 v[202:205], v163 offset:20480
	ds_read_b128 v[206:209], v163 offset:21504
	ds_read_b128 v[216:219], v163 offset:22528
	ds_read_b128 v[220:223], v163 offset:23552
	global_load_lds_dwordx4 v[184:185], off
	v_lshl_add_u64 v[186:187], v[184:185], 0, s[90:91]
	s_mov_b32 m0, s46
	s_nop 0
	global_load_lds_dwordx4 v[186:187], off
	v_lshl_add_u64 v[186:187], v[184:185], 0, s[60:61]
	s_mov_b32 m0, s47
	s_nop 0
	global_load_lds_dwordx4 v[186:187], off
	v_lshl_add_u64 v[186:187], v[184:185], 0, s[64:65]
	s_mov_b32 m0, s48
	s_nop 0
	global_load_lds_dwordx4 v[186:187], off
	v_lshl_add_u64 v[186:187], s[54:55], 0, v[134:135]
	s_mov_b32 m0, s37
	v_lshl_add_u64 v[188:189], v[186:187], 0, s[96:97]
	global_load_lds_dwordx4 v[186:187], off
	s_mov_b32 m0, s38
	s_nop 0
	global_load_lds_dwordx4 v[188:189], off
	s_waitcnt vmcnt(8)
	s_waitcnt lgkmcnt(0)
	s_barrier
	v_mfma_f32_16x16x32_bf16 v[56:59], v[144:147], v[180:183], v[56:59]
	v_mfma_f32_16x16x32_bf16 v[56:59], v[148:151], v[190:193], v[56:59]
	v_mfma_f32_16x16x32_bf16 v[52:55], v[152:155], v[180:183], v[52:55]
	v_mfma_f32_16x16x32_bf16 v[52:55], v[156:159], v[190:193], v[52:55]
	v_mfma_f32_16x16x32_bf16 v[40:43], v[144:147], v[194:197], v[40:43]
	v_mfma_f32_16x16x32_bf16 v[40:43], v[148:151], v[198:201], v[40:43]
	v_mfma_f32_16x16x32_bf16 v[36:39], v[152:155], v[194:197], v[36:39]
	v_mfma_f32_16x16x32_bf16 v[36:39], v[156:159], v[198:201], v[36:39]
	v_mfma_f32_16x16x32_bf16 v[24:27], v[144:147], v[202:205], v[24:27]
	v_mfma_f32_16x16x32_bf16 v[24:27], v[148:151], v[206:209], v[24:27]
	v_mfma_f32_16x16x32_bf16 v[20:23], v[152:155], v[202:205], v[20:23]
	v_mfma_f32_16x16x32_bf16 v[20:23], v[156:159], v[206:209], v[20:23]
	v_mfma_f32_16x16x32_bf16 v[8:11], v[144:147], v[216:219], v[8:11]
	v_mfma_f32_16x16x32_bf16 v[8:11], v[148:151], v[220:223], v[8:11]
	v_mfma_f32_16x16x32_bf16 v[4:7], v[152:155], v[216:219], v[4:7]
	v_mfma_f32_16x16x32_bf16 v[4:7], v[156:159], v[220:223], v[4:7]
	v_mfma_f32_16x16x32_bf16 v[64:67], v[164:167], v[180:183], v[64:67]
	v_mfma_f32_16x16x32_bf16 v[64:67], v[168:171], v[190:193], v[64:67]
	v_mfma_f32_16x16x32_bf16 v[60:63], v[172:175], v[180:183], v[60:63]
	v_mfma_f32_16x16x32_bf16 v[60:63], v[176:179], v[190:193], v[60:63]
	v_mfma_f32_16x16x32_bf16 v[48:51], v[164:167], v[194:197], v[48:51]
	v_mfma_f32_16x16x32_bf16 v[48:51], v[168:171], v[198:201], v[48:51]
	v_mfma_f32_16x16x32_bf16 v[44:47], v[172:175], v[194:197], v[44:47]
	v_mfma_f32_16x16x32_bf16 v[44:47], v[176:179], v[198:201], v[44:47]
	v_mfma_f32_16x16x32_bf16 v[32:35], v[164:167], v[202:205], v[32:35]
	v_mfma_f32_16x16x32_bf16 v[32:35], v[168:171], v[206:209], v[32:35]
	v_mfma_f32_16x16x32_bf16 v[28:31], v[172:175], v[202:205], v[28:31]
	v_mfma_f32_16x16x32_bf16 v[28:31], v[176:179], v[206:209], v[28:31]
	v_mfma_f32_16x16x32_bf16 v[16:19], v[164:167], v[216:219], v[16:19]
	v_mfma_f32_16x16x32_bf16 v[16:19], v[168:171], v[220:223], v[16:19]
	v_mfma_f32_16x16x32_bf16 v[12:15], v[172:175], v[216:219], v[12:15]
	v_mfma_f32_16x16x32_bf16 v[12:15], v[176:179], v[220:223], v[12:15]
	s_barrier
; #define PG8_MMA(ai, bj, At, Bt) do { __builtin_amdgcn_s_setprio(1); _Pragma("unroll") for (int m = 0; m < 4; ++m) _Pragma("unroll") for (int n = 0; n < 2; ++n) _Pragma("unroll") for (int k = 0; k < 2; ++k) \
;         acc[ai][bj][m][n] = __builtin_amdgcn_mfma_f32_16x16x32_bf16(Bt[n][k], At[m][k], acc[ai][bj][m][n], 0, 0, 0); __builtin_amdgcn_s_setprio(0); } while (0)
; #define PG8_WAIT_V(n) asm volatile("s_waitcnt vmcnt(" #n ")" ::: "memory")
; #define PG8_BAR __builtin_amdgcn_s_barrier()
; #define PG8_TRIP_HEAD(T) const int t = (T); const bool last = (t == nt - 2); \
;             const char* a1 = cA + (size_t)(t + 1) * kstep; \
;             const char* a2 = last ? nA : cA + (size_t)(t + 2) * kstep; const char* b2 = last ? nB : cB + (size_t)(t + 2) * kstep; \
;             const char* a3 = a2 + kstep; const char* b3 = b2 + kstep; \
;             if (last && has_next) S.a_ready(nxt);
; template <class Epi, class Sched, bool ALIGN_EPI = false, bool SP2 = false>
; __device__ __forceinline__ void gemm_phase(PG8_LAS unsigned char* lds, const Gemm g, const Sched& S, const Epi& E) {
;     ...
;         if constexpr (SP2) {
;             { PG8_TRIP_HEAD(0) PG8_TRIP_SP2(asm volatile("s_waitcnt vmcnt(%0)" :: "n"(8 + Epi::NST) : "memory"), PG8_MMAZ) }
;             for (int tt = 2; tt < nt; tt += 2) { PG8_TRIP_HEAD(tt) PG8_TRIP_SP2(PG8_WAIT_V(8), PG8_MMA) }
;     ...
;         if constexpr (ALIGN_EPI) { if (wr == 0) PG8_BAR; }
	ds_read_b128 v[144:147], v142
	ds_read_b128 v[148:151], v142 offset:1024
	ds_read_b128 v[152:155], v142 offset:2048
	ds_read_b128 v[156:159], v142 offset:3072
	ds_read_b128 v[164:167], v143
	ds_read_b128 v[168:171], v143 offset:1024
	ds_read_b128 v[172:175], v143 offset:2048
	ds_read_b128 v[176:179], v143 offset:3072
	s_mov_b32 m0, s39
	v_lshl_add_u64 v[188:189], v[186:187], 0, s[82:83]
	ds_read_b128 v[180:183], v163 offset:32768
	ds_read_b128 v[190:193], v163 offset:33792
	ds_read_b128 v[194:197], v163 offset:34816
	ds_read_b128 v[198:201], v163 offset:35840
	ds_read_b128 v[202:205], v163 offset:36864
	ds_read_b128 v[206:209], v163 offset:37888
	ds_read_b128 v[216:219], v163 offset:38912
	ds_read_b128 v[220:223], v163 offset:39936
	global_load_lds_dwordx4 v[188:189], off
	v_lshl_add_u64 v[188:189], v[186:187], 0, s[68:69]
	s_mov_b32 m0, s40
	s_nop 0
	global_load_lds_dwordx4 v[188:189], off
	s_waitcnt vmcnt(8)
	s_waitcnt lgkmcnt(0)
	s_barrier
	v_mfma_f32_16x16x32_bf16 v[120:123], v[144:147], v[180:183], v[120:123]
	v_mfma_f32_16x16x32_bf16 v[120:123], v[148:151], v[190:193], v[120:123]
	v_mfma_f32_16x16x32_bf16 v[116:119], v[152:155], v[180:183], v[116:119]
	v_mfma_f32_16x16x32_bf16 v[116:119], v[156:159], v[190:193], v[116:119]
	v_mfma_f32_16x16x32_bf16 v[104:107], v[144:147], v[194:197], v[104:107]
	v_mfma_f32_16x16x32_bf16 v[104:107], v[148:151], v[198:201], v[104:107]
	v_mfma_f32_16x16x32_bf16 v[100:103], v[152:155], v[194:197], v[100:103]
	v_mfma_f32_16x16x32_bf16 v[100:103], v[156:159], v[198:201], v[100:103]
	v_mfma_f32_16x16x32_bf16 v[88:91], v[144:147], v[202:205], v[88:91]
	v_mfma_f32_16x16x32_bf16 v[88:91], v[148:151], v[206:209], v[88:91]
	v_mfma_f32_16x16x32_bf16 v[84:87], v[152:155], v[202:205], v[84:87]
	v_mfma_f32_16x16x32_bf16 v[84:87], v[156:159], v[206:209], v[84:87]
	v_mfma_f32_16x16x32_bf16 v[72:75], v[144:147], v[216:219], v[72:75]
	v_mfma_f32_16x16x32_bf16 v[72:75], v[148:151], v[220:223], v[72:75]
	v_mfma_f32_16x16x32_bf16 v[68:71], v[152:155], v[216:219], v[68:71]
	v_mfma_f32_16x16x32_bf16 v[68:71], v[156:159], v[220:223], v[68:71]
	v_mfma_f32_16x16x32_bf16 v[128:131], v[164:167], v[180:183], v[128:131]
	v_mfma_f32_16x16x32_bf16 v[128:131], v[168:171], v[190:193], v[128:131]
	v_mfma_f32_16x16x32_bf16 v[124:127], v[172:175], v[180:183], v[124:127]
	v_mfma_f32_16x16x32_bf16 v[124:127], v[176:179], v[190:193], v[124:127]
	v_mfma_f32_16x16x32_bf16 v[112:115], v[164:167], v[194:197], v[112:115]
	v_mfma_f32_16x16x32_bf16 v[112:115], v[168:171], v[198:201], v[112:115]
	v_mfma_f32_16x16x32_bf16 v[108:111], v[172:175], v[194:197], v[108:111]
	v_mfma_f32_16x16x32_bf16 v[108:111], v[176:179], v[198:201], v[108:111]
	v_mfma_f32_16x16x32_bf16 v[96:99], v[164:167], v[202:205], v[96:99]
	v_mfma_f32_16x16x32_bf16 v[96:99], v[168:171], v[206:209], v[96:99]
	v_mfma_f32_16x16x32_bf16 v[92:95], v[172:175], v[202:205], v[92:95]
	v_mfma_f32_16x16x32_bf16 v[92:95], v[176:179], v[206:209], v[92:95]
	v_mfma_f32_16x16x32_bf16 v[80:83], v[164:167], v[216:219], v[80:83]
	v_mfma_f32_16x16x32_bf16 v[80:83], v[168:171], v[220:223], v[80:83]
	v_mfma_f32_16x16x32_bf16 v[76:79], v[172:175], v[216:219], v[76:79]
	v_mfma_f32_16x16x32_bf16 v[76:79], v[176:179], v[220:223], v[76:79]
	s_barrier
	s_mov_b32 m0, s49
	v_lshl_add_u64 v[188:189], v[184:185], 0, s[78:79]
	ds_read_b128 v[180:183], v163 offset:49152
	ds_read_b128 v[190:193], v163 offset:50176
	ds_read_b128 v[194:197], v163 offset:51200
	ds_read_b128 v[198:201], v163 offset:52224
	ds_read_b128 v[202:205], v163 offset:53248
	ds_read_b128 v[206:209], v163 offset:54272
	ds_read_b128 v[216:219], v163 offset:55296
	ds_read_b128 v[220:223], v163 offset:56320
	global_load_lds_dwordx4 v[188:189], off
	v_lshl_add_u64 v[188:189], v[184:185], 0, s[84:85]
	s_mov_b32 m0, s50
	s_nop 0
	global_load_lds_dwordx4 v[188:189], off
	v_lshl_add_u64 v[188:189], v[184:185], 0, s[62:63]
	s_mov_b32 m0, s51
	v_lshl_add_u64 v[184:185], v[184:185], 0, s[66:67]
	global_load_lds_dwordx4 v[188:189], off
	s_mov_b32 m0, s52
	s_nop 0
	global_load_lds_dwordx4 v[184:185], off
	v_lshl_add_u64 v[184:185], v[186:187], 0, s[78:79]
	s_mov_b32 m0, s0
	s_nop 0
	global_load_lds_dwordx4 v[184:185], off
	v_lshl_add_u64 v[184:185], v[186:187], 0, s[92:93]
	s_mov_b32 m0, s41
	s_nop 0
	global_load_lds_dwordx4 v[184:185], off
	s_waitcnt vmcnt(8)
	s_waitcnt lgkmcnt(0)
	s_barrier
	v_mfma_f32_16x16x32_bf16 v[56:59], v[144:147], v[180:183], v[56:59]
	v_mfma_f32_16x16x32_bf16 v[56:59], v[148:151], v[190:193], v[56:59]
	v_mfma_f32_16x16x32_bf16 v[52:55], v[152:155], v[180:183], v[52:55]
	v_mfma_f32_16x16x32_bf16 v[52:55], v[156:159], v[190:193], v[52:55]
	v_mfma_f32_16x16x32_bf16 v[40:43], v[144:147], v[194:197], v[40:43]
	v_mfma_f32_16x16x32_bf16 v[40:43], v[148:151], v[198:201], v[40:43]
	v_mfma_f32_16x16x32_bf16 v[36:39], v[152:155], v[194:197], v[36:39]
	v_mfma_f32_16x16x32_bf16 v[36:39], v[156:159], v[198:201], v[36:39]
	v_mfma_f32_16x16x32_bf16 v[24:27], v[144:147], v[202:205], v[24:27]
	v_mfma_f32_16x16x32_bf16 v[24:27], v[148:151], v[206:209], v[24:27]
	v_mfma_f32_16x16x32_bf16 v[20:23], v[152:155], v[202:205], v[20:23]
	v_mfma_f32_16x16x32_bf16 v[20:23], v[156:159], v[206:209], v[20:23]
	v_mfma_f32_16x16x32_bf16 v[8:11], v[144:147], v[216:219], v[8:11]
	v_mfma_f32_16x16x32_bf16 v[8:11], v[148:151], v[220:223], v[8:11]
	v_mfma_f32_16x16x32_bf16 v[4:7], v[152:155], v[216:219], v[4:7]
	v_mfma_f32_16x16x32_bf16 v[4:7], v[156:159], v[220:223], v[4:7]
	v_mfma_f32_16x16x32_bf16 v[64:67], v[164:167], v[180:183], v[64:67]
	v_mfma_f32_16x16x32_bf16 v[64:67], v[168:171], v[190:193], v[64:67]
	v_mfma_f32_16x16x32_bf16 v[60:63], v[172:175], v[180:183], v[60:63]
	v_mfma_f32_16x16x32_bf16 v[60:63], v[176:179], v[190:193], v[60:63]
	v_mfma_f32_16x16x32_bf16 v[48:51], v[164:167], v[194:197], v[48:51]
	v_mfma_f32_16x16x32_bf16 v[48:51], v[168:171], v[198:201], v[48:51]
	v_mfma_f32_16x16x32_bf16 v[44:47], v[172:175], v[194:197], v[44:47]
	v_mfma_f32_16x16x32_bf16 v[44:47], v[176:179], v[198:201], v[44:47]
	v_mfma_f32_16x16x32_bf16 v[32:35], v[164:167], v[202:205], v[32:35]
	v_mfma_f32_16x16x32_bf16 v[32:35], v[168:171], v[206:209], v[32:35]
	v_mfma_f32_16x16x32_bf16 v[28:31], v[172:175], v[202:205], v[28:31]
	v_mfma_f32_16x16x32_bf16 v[28:31], v[176:179], v[206:209], v[28:31]
	v_mfma_f32_16x16x32_bf16 v[16:19], v[164:167], v[216:219], v[16:19]
	v_mfma_f32_16x16x32_bf16 v[16:19], v[168:171], v[220:223], v[16:19]
	v_mfma_f32_16x16x32_bf16 v[12:15], v[172:175], v[216:219], v[12:15]
	v_mfma_f32_16x16x32_bf16 v[12:15], v[176:179], v[220:223], v[12:15]
	s_barrier
	s_add_i32 s30, s30, 2
	s_add_u32 s10, s10, 0x100
	s_addc_u32 s11, s11, 0
	s_add_u32 s28, s28, 0x100
	s_addc_u32 s29, s29, 0
	s_cmp_gt_u32 s30, 29
	s_cbranch_scc0 .LBB0_130
	s_and_b64 vcc, exec, s[20:21]
	s_cbranch_vccz .LBB0_133
	s_barrier

;     __device__ bool next(int i, Unit& u) const { const int rounds = nwg / G; if (i >= rounds) return false; return StaticOrder::next(rounds - 1 - i, u); }
;     __device__ bool next(int i, Unit& u) const { const int rounds = nwg / G; if (i >= 2 * rounds) return false; const bool ok = StaticOrder::next(i >= rounds ? i - rounds : i, u); u.z = (i >= rounds) ? 1 : 0; return ok; }
; #define PG8_TRIP_HEAD(T) const int t = (T); const bool last = (t == nt - 2); \
;             const char* a1 = cA + (size_t)(t + 1) * kstep; \
;             const char* a2 = last ? nA : cA + (size_t)(t + 2) * kstep; const char* b2 = last ? nB : cB + (size_t)(t + 2) * kstep; \
;             const char* a3 = a2 + kstep; const char* b3 = b2 + kstep; \
;             if (last && has_next) S.a_ready(nxt);
; template <class Epi, class Sched, bool ALIGN_EPI = false, bool SP2 = false>
; __device__ __forceinline__ void gemm_phase(PG8_LAS unsigned char* lds, const Gemm g, const Sched& S, const Epi& E) {
;     ...
;         const bool has_next = S.next(ui + 1, nxt);
;         const char* nA = has_next ? (const char*)S.opA(g, nxt) + (size_t)nxt.pm * tstepA : cA; const char* nB = has_next ? (const char*)S.opB(g, nxt) + (size_t)nxt.pn * tstepB : cB;
;     ...
;         if constexpr (SP2) {
;             { PG8_TRIP_HEAD(0) PG8_TRIP_SP2(asm volatile("s_waitcnt vmcnt(%0)" :: "n"(8 + Epi::NST) : "memory"), PG8_MMAZ) }
.LBB0_232:
	s_add_i32 s5, 0, 0x10000
	s_add_i32 s42, 0, 0x14000
	v_add_u32_e32 v116, s5, v176
	v_add_u32_e32 v117, s42, v176
	ds_read_b128 v[4:7], v116
	ds_read_b128 v[8:11], v116 offset:1024
	ds_read_b128 v[12:15], v116 offset:2048
	ds_read_b128 v[16:19], v116 offset:3072
	ds_read_b128 v[20:23], v117
	ds_read_b128 v[24:27], v117 offset:1024
	ds_read_b128 v[28:31], v117 offset:2048
	ds_read_b128 v[32:35], v117 offset:3072
	v_lshl_add_u64 v[188:189], s[26:27], 0, v[160:161]
	s_mov_b64 s[62:63], 0x160080
	s_add_i32 s0, s31, 0xc000
	v_lshl_add_u64 v[68:69], v[188:189], 0, s[62:63]
	s_mov_b32 m0, s0
	s_mov_b64 s[64:65], 0x210080
	s_add_i32 s4, s31, 0xe000
	ds_read_b128 v[36:39], v178
	ds_read_b128 v[40:43], v178 offset:1024
	ds_read_b128 v[44:47], v178 offset:2048
	ds_read_b128 v[48:51], v178 offset:3072
	ds_read_b128 v[52:55], v178 offset:4096
	ds_read_b128 v[56:59], v178 offset:5120
	ds_read_b128 v[60:63], v178 offset:6144
	ds_read_b128 v[64:67], v178 offset:7168
	global_load_lds_dwordx4 v[68:69], off
	v_lshl_add_u64 v[68:69], v[188:189], 0, s[64:65]
	s_mov_b32 m0, s4
	s_nop 0
	global_load_lds_dwordx4 v[68:69], off
	s_waitcnt vmcnt(16)
	s_waitcnt lgkmcnt(0)
	s_barrier
	v_mfma_f32_16x16x32_bf16 v[92:95], v[4:7], v[60:63], 0
	v_mfma_f32_16x16x32_bf16 v[68:71], v[4:7], v[36:39], 0
	v_mfma_f32_16x16x32_bf16 v[72:75], v[12:15], v[36:39], 0
	v_mfma_f32_16x16x32_bf16 v[76:79], v[4:7], v[44:47], 0
	v_mfma_f32_16x16x32_bf16 v[80:83], v[12:15], v[44:47], 0
	v_mfma_f32_16x16x32_bf16 v[84:87], v[4:7], v[52:55], 0
	v_mfma_f32_16x16x32_bf16 v[88:91], v[12:15], v[52:55], 0
	v_mfma_f32_16x16x32_bf16 v[100:103], v[8:11], v[64:67], v[92:95]
	v_mfma_f32_16x16x32_bf16 v[92:95], v[12:15], v[60:63], 0
	v_mfma_f32_16x16x32_bf16 v[68:71], v[8:11], v[40:43], v[68:71]
	v_mfma_f32_16x16x32_bf16 v[72:75], v[16:19], v[40:43], v[72:75]
	v_mfma_f32_16x16x32_bf16 v[76:79], v[8:11], v[48:51], v[76:79]
	v_mfma_f32_16x16x32_bf16 v[80:83], v[16:19], v[48:51], v[80:83]
	v_mfma_f32_16x16x32_bf16 v[84:87], v[8:11], v[56:59], v[84:87]
	v_mfma_f32_16x16x32_bf16 v[88:91], v[16:19], v[56:59], v[88:91]
	v_mfma_f32_16x16x32_bf16 v[104:107], v[16:19], v[64:67], v[92:95]
	v_mfma_f32_16x16x32_bf16 v[92:95], v[20:23], v[36:39], 0
	v_mfma_f32_16x16x32_bf16 v[36:39], v[28:31], v[36:39], 0
	v_mfma_f32_16x16x32_bf16 v[120:123], v[24:27], v[40:43], v[92:95]
	v_mfma_f32_16x16x32_bf16 v[36:39], v[32:35], v[40:43], v[36:39]
	v_mfma_f32_16x16x32_bf16 v[40:43], v[20:23], v[44:47], 0
	v_mfma_f32_16x16x32_bf16 v[44:47], v[28:31], v[44:47], 0
	v_mfma_f32_16x16x32_bf16 v[40:43], v[24:27], v[48:51], v[40:43]
	v_mfma_f32_16x16x32_bf16 v[44:47], v[32:35], v[48:51], v[44:47]
	v_mfma_f32_16x16x32_bf16 v[48:51], v[20:23], v[52:55], 0
	v_mfma_f32_16x16x32_bf16 v[52:55], v[28:31], v[52:55], 0
	v_mfma_f32_16x16x32_bf16 v[48:51], v[24:27], v[56:59], v[48:51]
	v_mfma_f32_16x16x32_bf16 v[52:55], v[32:35], v[56:59], v[52:55]
	v_mfma_f32_16x16x32_bf16 v[56:59], v[20:23], v[60:63], 0
	v_mfma_f32_16x16x32_bf16 v[60:63], v[28:31], v[60:63], 0
	v_mfma_f32_16x16x32_bf16 v[56:59], v[24:27], v[64:67], v[56:59]
	v_mfma_f32_16x16x32_bf16 v[60:63], v[32:35], v[64:67], v[60:63]
	s_barrier
	v_lshl_add_u64 v[214:215], s[24:25], 0, v[162:163]
	s_mov_b64 s[44:45], 0x100
	s_add_i32 s5, s5, s30
	v_lshl_add_u64 v[118:119], v[214:215], 0, s[44:45]
	s_mov_b32 m0, s5
	s_mov_b64 s[46:47], 0xb0100
	s_add_i32 s33, s5, 0x2000
	ds_read_b128 v[64:67], v178 offset:16384
	ds_read_b128 v[92:95], v178 offset:17408
	ds_read_b128 v[96:99], v178 offset:18432
	ds_read_b128 v[108:111], v178 offset:19456
	ds_read_b128 v[112:115], v178 offset:20480
	ds_read_b128 v[124:127], v178 offset:21504
	ds_read_b128 v[128:131], v178 offset:22528
	ds_read_b128 v[132:135], v178 offset:23552
	global_load_lds_dwordx4 v[118:119], off
	v_lshl_add_u64 v[118:119], v[214:215], 0, s[46:47]
	s_mov_b32 m0, s33
	s_mov_b64 s[50:51], 0x160100
	s_add_i32 s42, s42, s30
	global_load_lds_dwordx4 v[118:119], off
	v_lshl_add_u64 v[118:119], v[214:215], 0, s[50:51]
	s_mov_b32 m0, s42
	s_mov_b64 s[52:53], 0x210100
	s_add_i32 s43, s42, 0x2000
	global_load_lds_dwordx4 v[118:119], off
	v_lshl_add_u64 v[118:119], v[214:215], 0, s[52:53]
	s_mov_b32 m0, s43
	s_nop 0
	global_load_lds_dwordx4 v[118:119], off
	v_lshl_add_u64 v[118:119], v[188:189], 0, s[44:45]
	s_mov_b32 m0, s31
	s_nop 0
	global_load_lds_dwordx4 v[118:119], off
	v_lshl_add_u64 v[118:119], v[188:189], 0, s[46:47]
	s_mov_b32 m0, s34
	s_nop 0
	global_load_lds_dwordx4 v[118:119], off
	s_waitcnt vmcnt(16)
	s_waitcnt lgkmcnt(0)
	s_barrier
	v_mfma_f32_16x16x32_bf16 v[136:139], v[4:7], v[64:67], 0
	v_mfma_f32_16x16x32_bf16 v[144:147], v[8:11], v[92:95], v[136:139]
	v_mfma_f32_16x16x32_bf16 v[136:139], v[12:15], v[64:67], 0
	v_mfma_f32_16x16x32_bf16 v[148:151], v[16:19], v[92:95], v[136:139]
	v_mfma_f32_16x16x32_bf16 v[136:139], v[4:7], v[96:99], 0
	v_mfma_f32_16x16x32_bf16 v[152:155], v[8:11], v[108:111], v[136:139]
	v_mfma_f32_16x16x32_bf16 v[136:139], v[12:15], v[96:99], 0
	v_mfma_f32_16x16x32_bf16 v[156:159], v[16:19], v[108:111], v[136:139]
	v_mfma_f32_16x16x32_bf16 v[136:139], v[4:7], v[112:115], 0
	v_mfma_f32_16x16x32_bf16 v[4:7], v[4:7], v[128:131], 0
	v_mfma_f32_16x16x32_bf16 v[166:169], v[8:11], v[124:127], v[136:139]
	v_mfma_f32_16x16x32_bf16 v[4:7], v[8:11], v[132:135], v[4:7]
	v_mfma_f32_16x16x32_bf16 v[8:11], v[12:15], v[128:131], 0
	v_mfma_f32_16x16x32_bf16 v[136:139], v[12:15], v[112:115], 0
	v_mfma_f32_16x16x32_bf16 v[8:11], v[16:19], v[132:135], v[8:11]
	v_mfma_f32_16x16x32_bf16 v[170:173], v[16:19], v[124:127], v[136:139]
	v_mfma_f32_16x16x32_bf16 v[12:15], v[20:23], v[64:67], 0
	v_mfma_f32_16x16x32_bf16 v[180:183], v[24:27], v[92:95], v[12:15]
	v_mfma_f32_16x16x32_bf16 v[12:15], v[28:31], v[64:67], 0
	v_mfma_f32_16x16x32_bf16 v[190:193], v[32:35], v[92:95], v[12:15]
	v_mfma_f32_16x16x32_bf16 v[12:15], v[20:23], v[96:99], 0
	v_mfma_f32_16x16x32_bf16 v[194:197], v[24:27], v[108:111], v[12:15]
	v_mfma_f32_16x16x32_bf16 v[12:15], v[28:31], v[96:99], 0
	v_mfma_f32_16x16x32_bf16 v[198:201], v[32:35], v[108:111], v[12:15]
	v_mfma_f32_16x16x32_bf16 v[12:15], v[20:23], v[112:115], 0
	v_mfma_f32_16x16x32_bf16 v[202:205], v[24:27], v[124:127], v[12:15]
	v_mfma_f32_16x16x32_bf16 v[12:15], v[28:31], v[112:115], 0
	v_mfma_f32_16x16x32_bf16 v[206:209], v[32:35], v[124:127], v[12:15]
	v_mfma_f32_16x16x32_bf16 v[12:15], v[20:23], v[128:131], 0
	v_mfma_f32_16x16x32_bf16 v[216:219], v[24:27], v[132:135], v[12:15]
	v_mfma_f32_16x16x32_bf16 v[12:15], v[28:31], v[128:131], 0
	v_mfma_f32_16x16x32_bf16 v[132:135], v[32:35], v[132:135], v[12:15]
	s_barrier
; #define PG8_MMA(ai, bj, At, Bt) do { __builtin_amdgcn_s_setprio(1); _Pragma("unroll") for (int m = 0; m < 4; ++m) _Pragma("unroll") for (int n = 0; n < 2; ++n) _Pragma("unroll") for (int k = 0; k < 2; ++k) \
;         acc[ai][bj][m][n] = __builtin_amdgcn_mfma_f32_16x16x32_bf16(Bt[n][k], At[m][k], acc[ai][bj][m][n], 0, 0, 0); __builtin_amdgcn_s_setprio(0); } while (0)
; #define PG8_WAIT_V(n) asm volatile("s_waitcnt vmcnt(" #n ")" ::: "memory")
; #define PG8_TRIP_HEAD(T) const int t = (T); const bool last = (t == nt - 2); \
;             const char* a1 = cA + (size_t)(t + 1) * kstep; \
;             const char* a2 = last ? nA : cA + (size_t)(t + 2) * kstep; const char* b2 = last ? nB : cB + (size_t)(t + 2) * kstep; \
;             const char* a3 = a2 + kstep; const char* b3 = b2 + kstep; \
;             if (last && has_next) S.a_ready(nxt);
; template <class Epi, class Sched, bool ALIGN_EPI = false, bool SP2 = false>
; __device__ __forceinline__ void gemm_phase(PG8_LAS unsigned char* lds, const Gemm g, const Sched& S, const Epi& E) {
;     ...
;         if constexpr (SP2) {
;             { PG8_TRIP_HEAD(0) PG8_TRIP_SP2(asm volatile("s_waitcnt vmcnt(%0)" :: "n"(8 + Epi::NST) : "memory"), PG8_MMAZ) }
;             for (int tt = 2; tt < nt; tt += 2) { PG8_TRIP_HEAD(tt) PG8_TRIP_SP2(PG8_WAIT_V(8), PG8_MMA) }
	s_add_i32 s44, 0, 0x18000
	s_add_i32 s48, 0, 0x1c000
	v_add_u32_e32 v118, s44, v176
	v_add_u32_e32 v119, s48, v176
	s_nop 0
	ds_read_b128 v[12:15], v118
	ds_read_b128 v[16:19], v118 offset:1024
	ds_read_b128 v[20:23], v118 offset:2048
	ds_read_b128 v[24:27], v118 offset:3072
	ds_read_b128 v[220:223], v119
	ds_read_b128 v[224:227], v119 offset:1024
	ds_read_b128 v[228:231], v119 offset:2048
	ds_read_b128 v[232:235], v119 offset:3072
	s_mov_b32 m0, s35
	v_lshl_add_u64 v[92:93], v[188:189], 0, s[50:51]
	ds_read_b128 v[28:31], v178 offset:32768
	ds_read_b128 v[32:35], v178 offset:33792
	ds_read_b128 v[64:67], v178 offset:34816
	ds_read_b128 v[236:239], v178 offset:35840
	ds_read_b128 v[240:243], v178 offset:36864
	ds_read_b128 v[244:247], v178 offset:37888
	ds_read_b128 v[248:251], v178 offset:38912
	ds_read_b128 v[184:187], v178 offset:39936
	global_load_lds_dwordx4 v[92:93], off
	v_lshl_add_u64 v[92:93], v[188:189], 0, s[52:53]
	s_mov_b32 m0, s36
	s_nop 0
	global_load_lds_dwordx4 v[92:93], off
	s_waitcnt vmcnt(8)
	s_waitcnt lgkmcnt(0)
	s_barrier
	v_mfma_f32_16x16x32_bf16 v[68:71], v[12:15], v[28:31], v[68:71]
	v_mfma_f32_16x16x32_bf16 v[140:143], v[16:19], v[32:35], v[68:71]
	v_mfma_f32_16x16x32_bf16 v[68:71], v[20:23], v[28:31], v[72:75]
	v_mfma_f32_16x16x32_bf16 v[136:139], v[24:27], v[32:35], v[68:71]
	v_mfma_f32_16x16x32_bf16 v[68:71], v[12:15], v[64:67], v[76:79]
	v_mfma_f32_16x16x32_bf16 v[112:115], v[16:19], v[236:239], v[68:71]
	v_mfma_f32_16x16x32_bf16 v[68:71], v[20:23], v[64:67], v[80:83]
	v_mfma_f32_16x16x32_bf16 v[108:111], v[24:27], v[236:239], v[68:71]
	v_mfma_f32_16x16x32_bf16 v[68:71], v[12:15], v[240:243], v[84:87]
	v_mfma_f32_16x16x32_bf16 v[96:99], v[16:19], v[244:247], v[68:71]
	v_mfma_f32_16x16x32_bf16 v[68:71], v[20:23], v[240:243], v[88:91]
	v_mfma_f32_16x16x32_bf16 v[92:95], v[24:27], v[244:247], v[68:71]
	v_mfma_f32_16x16x32_bf16 v[68:71], v[12:15], v[248:251], v[100:103]
	v_mfma_f32_16x16x32_bf16 v[80:83], v[16:19], v[184:187], v[68:71]
	v_mfma_f32_16x16x32_bf16 v[68:71], v[20:23], v[248:251], v[104:107]
	v_mfma_f32_16x16x32_bf16 v[76:79], v[24:27], v[184:187], v[68:71]
	v_mfma_f32_16x16x32_bf16 v[68:71], v[220:223], v[28:31], v[120:123]
	v_mfma_f32_16x16x32_bf16 v[28:31], v[228:231], v[28:31], v[36:39]
	v_mfma_f32_16x16x32_bf16 v[124:127], v[232:235], v[32:35], v[28:31]
	v_mfma_f32_16x16x32_bf16 v[28:31], v[220:223], v[64:67], v[40:43]
	v_mfma_f32_16x16x32_bf16 v[104:107], v[224:227], v[236:239], v[28:31]
	v_mfma_f32_16x16x32_bf16 v[28:31], v[228:231], v[64:67], v[44:47]
	v_mfma_f32_16x16x32_bf16 v[100:103], v[232:235], v[236:239], v[28:31]
	v_mfma_f32_16x16x32_bf16 v[28:31], v[220:223], v[240:243], v[48:51]
	v_mfma_f32_16x16x32_bf16 v[88:91], v[224:227], v[244:247], v[28:31]
	v_mfma_f32_16x16x32_bf16 v[28:31], v[228:231], v[240:243], v[52:55]
	v_mfma_f32_16x16x32_bf16 v[84:87], v[232:235], v[244:247], v[28:31]
	v_mfma_f32_16x16x32_bf16 v[28:31], v[220:223], v[248:251], v[56:59]
	v_mfma_f32_16x16x32_bf16 v[72:75], v[224:227], v[184:187], v[28:31]
	v_mfma_f32_16x16x32_bf16 v[28:31], v[228:231], v[248:251], v[60:63]
	v_mfma_f32_16x16x32_bf16 v[128:131], v[224:227], v[32:35], v[68:71]
	v_mfma_f32_16x16x32_bf16 v[68:71], v[232:235], v[184:187], v[28:31]
	s_barrier
	s_mov_b64 s[50:51], 0x180
	s_add_i32 s44, s44, s30
	s_nop 1
	v_lshl_add_u64 v[28:29], v[214:215], 0, s[50:51]
	s_mov_b32 m0, s44
	s_mov_b64 s[52:53], 0xb0180
	s_add_i32 s45, s44, 0x2000
	ds_read_b128 v[36:39], v178 offset:49152
	ds_read_b128 v[40:43], v178 offset:50176
	ds_read_b128 v[120:123], v178 offset:51200
	ds_read_b128 v[184:187], v178 offset:52224
	ds_read_b128 v[236:239], v178 offset:53248
	ds_read_b128 v[240:243], v178 offset:54272
	ds_read_b128 v[244:247], v178 offset:55296
	ds_read_b128 v[248:251], v178 offset:56320
	global_load_lds_dwordx4 v[28:29], off
	v_lshl_add_u64 v[28:29], v[214:215], 0, s[52:53]
	s_mov_b32 m0, s45
	s_mov_b64 s[46:47], 0x160180
	global_load_lds_dwordx4 v[28:29], off
	v_lshl_add_u64 v[28:29], v[214:215], 0, s[46:47]
	s_add_i32 s46, s48, s30
	s_mov_b32 m0, s46
	s_mov_b64 s[48:49], 0x210180
	s_add_i32 s47, s46, 0x2000
	global_load_lds_dwordx4 v[28:29], off
	v_lshl_add_u64 v[28:29], v[214:215], 0, s[48:49]
	s_mov_b32 m0, s47
	s_nop 0
	global_load_lds_dwordx4 v[28:29], off
	v_lshl_add_u64 v[28:29], v[188:189], 0, s[50:51]
	s_mov_b32 m0, s37
	s_nop 0
	global_load_lds_dwordx4 v[28:29], off
	v_lshl_add_u64 v[28:29], v[188:189], 0, s[52:53]
	s_mov_b32 m0, s38
	s_nop 0
	global_load_lds_dwordx4 v[28:29], off
	s_waitcnt vmcnt(8)
	s_waitcnt lgkmcnt(0)
	s_barrier
	v_mfma_f32_16x16x32_bf16 v[28:31], v[12:15], v[36:39], v[144:147]
	v_mfma_f32_16x16x32_bf16 v[56:59], v[16:19], v[40:43], v[28:31]
	v_mfma_f32_16x16x32_bf16 v[28:31], v[20:23], v[36:39], v[148:151]
	v_mfma_f32_16x16x32_bf16 v[52:55], v[24:27], v[40:43], v[28:31]
	v_mfma_f32_16x16x32_bf16 v[28:31], v[12:15], v[120:123], v[152:155]
	v_mfma_f32_16x16x32_bf16 v[48:51], v[16:19], v[184:187], v[28:31]
	v_mfma_f32_16x16x32_bf16 v[28:31], v[20:23], v[120:123], v[156:159]
	v_mfma_f32_16x16x32_bf16 v[44:47], v[24:27], v[184:187], v[28:31]
	v_mfma_f32_16x16x32_bf16 v[28:31], v[12:15], v[236:239], v[166:169]
	v_mfma_f32_16x16x32_bf16 v[4:7], v[12:15], v[244:247], v[4:7]
	v_mfma_f32_16x16x32_bf16 v[32:35], v[16:19], v[240:243], v[28:31]
	v_mfma_f32_16x16x32_bf16 v[28:31], v[20:23], v[236:239], v[170:173]
	v_mfma_f32_16x16x32_bf16 v[16:19], v[16:19], v[248:251], v[4:7]
	v_mfma_f32_16x16x32_bf16 v[4:7], v[20:23], v[244:247], v[8:11]
	v_mfma_f32_16x16x32_bf16 v[28:31], v[24:27], v[240:243], v[28:31]
	v_mfma_f32_16x16x32_bf16 v[12:15], v[24:27], v[248:251], v[4:7]
	v_mfma_f32_16x16x32_bf16 v[4:7], v[220:223], v[36:39], v[180:183]
	v_mfma_f32_16x16x32_bf16 v[64:67], v[224:227], v[40:43], v[4:7]
	v_mfma_f32_16x16x32_bf16 v[4:7], v[228:231], v[36:39], v[190:193]
	v_mfma_f32_16x16x32_bf16 v[60:63], v[232:235], v[40:43], v[4:7]
	v_mfma_f32_16x16x32_bf16 v[4:7], v[220:223], v[120:123], v[194:197]
	v_mfma_f32_16x16x32_bf16 v[40:43], v[224:227], v[184:187], v[4:7]
	v_mfma_f32_16x16x32_bf16 v[4:7], v[228:231], v[120:123], v[198:201]
	v_mfma_f32_16x16x32_bf16 v[36:39], v[232:235], v[184:187], v[4:7]
	v_mfma_f32_16x16x32_bf16 v[4:7], v[220:223], v[236:239], v[202:205]
	v_mfma_f32_16x16x32_bf16 v[24:27], v[224:227], v[240:243], v[4:7]
	v_mfma_f32_16x16x32_bf16 v[4:7], v[228:231], v[236:239], v[206:209]
	v_mfma_f32_16x16x32_bf16 v[20:23], v[232:235], v[240:243], v[4:7]
	v_mfma_f32_16x16x32_bf16 v[4:7], v[220:223], v[244:247], v[216:219]
	v_mfma_f32_16x16x32_bf16 v[8:11], v[224:227], v[248:251], v[4:7]
	v_mfma_f32_16x16x32_bf16 v[4:7], v[228:231], v[244:247], v[132:135]
	v_mfma_f32_16x16x32_bf16 v[4:7], v[232:235], v[248:251], v[4:7]
	s_barrier
	s_add_u32 s26, s26, 0x160180
	s_addc_u32 s27, s27, 0
	s_add_u32 s24, s24, 0x200
	s_addc_u32 s25, s25, 0
	s_mov_b32 s48, 0
	s_mov_b64 s[54:55], 0x160000
	s_mov_b64 s[56:57], 0x210000
	s_mov_b64 s[60:61], 0xb0080
; #define PG8_TRIP_HEAD(T) const int t = (T); const bool last = (t == nt - 2); \
;             const char* a1 = cA + (size_t)(t + 1) * kstep; \
;             const char* a2 = last ? nA : cA + (size_t)(t + 2) * kstep; const char* b2 = last ? nB : cB + (size_t)(t + 2) * kstep; \
;             const char* a3 = a2 + kstep; const char* b3 = b2 + kstep; \
;             if (last && has_next) S.a_ready(nxt);
; template <class Epi, class Sched, bool ALIGN_EPI = false, bool SP2 = false>
; __device__ __forceinline__ void gemm_phase(PG8_LAS unsigned char* lds, const Gemm g, const Sched& S, const Epi& E) {
;     ...
;         if constexpr (SP2) {
;             { PG8_TRIP_HEAD(0) PG8_TRIP_SP2(asm volatile("s_waitcnt vmcnt(%0)" :: "n"(8 + Epi::NST) : "memory"), PG8_MMAZ) }
.LBB0_233:
	ds_read_b128 v[120:123], v116
	ds_read_b128 v[132:135], v116 offset:1024
	ds_read_b128 v[144:147], v116 offset:2048
	ds_read_b128 v[148:151], v116 offset:3072
	ds_read_b128 v[152:155], v117
	ds_read_b128 v[156:159], v117 offset:1024
	ds_read_b128 v[166:169], v117 offset:2048
	ds_read_b128 v[170:173], v117 offset:3072
	s_add_u32 s49, s26, 0xffea0080
	s_addc_u32 s50, s27, -1
	s_cmpk_eq_i32 s48, 0x54
	s_cselect_b32 s51, s21, s50
	s_cselect_b32 s50, s20, s49
	s_cselect_b32 s53, s23, s25
	s_cselect_b32 s52, s22, s24
	s_mov_b32 m0, s0
	v_lshl_add_u64 v[188:189], s[26:27], 0, v[164:165]
	ds_read_b128 v[180:183], v178
	ds_read_b128 v[184:187], v178 offset:1024
	ds_read_b128 v[190:193], v178 offset:2048
	ds_read_b128 v[194:197], v178 offset:3072
	ds_read_b128 v[198:201], v178 offset:4096
	ds_read_b128 v[202:205], v178 offset:5120
	ds_read_b128 v[206:209], v178 offset:6144
	ds_read_b128 v[216:219], v178 offset:7168
	global_load_lds_dwordx4 v[188:189], off
	v_lshl_add_u64 v[188:189], v[188:189], 0, s[86:87]
	s_mov_b32 m0, s4
	s_nop 0
	global_load_lds_dwordx4 v[188:189], off
	s_waitcnt vmcnt(8)
	s_waitcnt lgkmcnt(0)
	s_barrier
	v_mfma_f32_16x16x32_bf16 v[140:143], v[120:123], v[180:183], v[140:143]
	v_mfma_f32_16x16x32_bf16 v[140:143], v[132:135], v[184:187], v[140:143]
	v_mfma_f32_16x16x32_bf16 v[136:139], v[144:147], v[180:183], v[136:139]
	v_mfma_f32_16x16x32_bf16 v[136:139], v[148:151], v[184:187], v[136:139]
	v_mfma_f32_16x16x32_bf16 v[112:115], v[120:123], v[190:193], v[112:115]
	v_mfma_f32_16x16x32_bf16 v[112:115], v[132:135], v[194:197], v[112:115]
	v_mfma_f32_16x16x32_bf16 v[108:111], v[144:147], v[190:193], v[108:111]
	v_mfma_f32_16x16x32_bf16 v[108:111], v[148:151], v[194:197], v[108:111]
	v_mfma_f32_16x16x32_bf16 v[96:99], v[120:123], v[198:201], v[96:99]
	v_mfma_f32_16x16x32_bf16 v[96:99], v[132:135], v[202:205], v[96:99]
	v_mfma_f32_16x16x32_bf16 v[92:95], v[144:147], v[198:201], v[92:95]
	v_mfma_f32_16x16x32_bf16 v[92:95], v[148:151], v[202:205], v[92:95]
	v_mfma_f32_16x16x32_bf16 v[80:83], v[120:123], v[206:209], v[80:83]
	v_mfma_f32_16x16x32_bf16 v[80:83], v[132:135], v[216:219], v[80:83]
	v_mfma_f32_16x16x32_bf16 v[76:79], v[144:147], v[206:209], v[76:79]
	v_mfma_f32_16x16x32_bf16 v[76:79], v[148:151], v[216:219], v[76:79]
	v_mfma_f32_16x16x32_bf16 v[128:131], v[152:155], v[180:183], v[128:131]
	v_mfma_f32_16x16x32_bf16 v[128:131], v[156:159], v[184:187], v[128:131]
	v_mfma_f32_16x16x32_bf16 v[124:127], v[166:169], v[180:183], v[124:127]
	v_mfma_f32_16x16x32_bf16 v[124:127], v[170:173], v[184:187], v[124:127]
	v_mfma_f32_16x16x32_bf16 v[104:107], v[152:155], v[190:193], v[104:107]
	v_mfma_f32_16x16x32_bf16 v[104:107], v[156:159], v[194:197], v[104:107]
	v_mfma_f32_16x16x32_bf16 v[100:103], v[166:169], v[190:193], v[100:103]
	v_mfma_f32_16x16x32_bf16 v[100:103], v[170:173], v[194:197], v[100:103]
	v_mfma_f32_16x16x32_bf16 v[88:91], v[152:155], v[198:201], v[88:91]
	v_mfma_f32_16x16x32_bf16 v[88:91], v[156:159], v[202:205], v[88:91]
	v_mfma_f32_16x16x32_bf16 v[84:87], v[166:169], v[198:201], v[84:87]
	v_mfma_f32_16x16x32_bf16 v[84:87], v[170:173], v[202:205], v[84:87]
	v_mfma_f32_16x16x32_bf16 v[72:75], v[152:155], v[206:209], v[72:75]
	v_mfma_f32_16x16x32_bf16 v[72:75], v[156:159], v[216:219], v[72:75]
	v_mfma_f32_16x16x32_bf16 v[68:71], v[166:169], v[206:209], v[68:71]
	v_mfma_f32_16x16x32_bf16 v[68:71], v[170:173], v[216:219], v[68:71]
	s_barrier
	s_mov_b32 m0, s5
	v_lshl_add_u64 v[188:189], s[52:53], 0, v[162:163]
	ds_read_b128 v[180:183], v178 offset:16384
	ds_read_b128 v[184:187], v178 offset:17408
	ds_read_b128 v[190:193], v178 offset:18432
	ds_read_b128 v[194:197], v178 offset:19456
	ds_read_b128 v[198:201], v178 offset:20480
	ds_read_b128 v[202:205], v178 offset:21504
	ds_read_b128 v[206:209], v178 offset:22528
	ds_read_b128 v[216:219], v178 offset:23552
	global_load_lds_dwordx4 v[188:189], off
	v_lshl_add_u64 v[214:215], v[188:189], 0, s[86:87]
	s_mov_b32 m0, s33
	s_nop 0
	global_load_lds_dwordx4 v[214:215], off
	v_lshl_add_u64 v[214:215], v[188:189], 0, s[54:55]
	s_mov_b32 m0, s42
	s_nop 0
	global_load_lds_dwordx4 v[214:215], off
	v_lshl_add_u64 v[214:215], v[188:189], 0, s[56:57]
	s_mov_b32 m0, s43
	s_nop 0
	global_load_lds_dwordx4 v[214:215], off
	v_lshl_add_u64 v[214:215], s[50:51], 0, v[160:161]
	s_mov_b32 m0, s31
	v_lshl_add_u64 v[220:221], v[214:215], 0, s[86:87]
	global_load_lds_dwordx4 v[214:215], off
	s_mov_b32 m0, s34
	s_nop 0
	global_load_lds_dwordx4 v[220:221], off
	s_waitcnt vmcnt(8)
	s_waitcnt lgkmcnt(0)
	s_barrier
; #define PG8_TRIP_HEAD(T) const int t = (T); const bool last = (t == nt - 2); \
;             const char* a1 = cA + (size_t)(t + 1) * kstep; \
;             const char* a2 = last ? nA : cA + (size_t)(t + 2) * kstep; const char* b2 = last ? nB : cB + (size_t)(t + 2) * kstep; \
;             const char* a3 = a2 + kstep; const char* b3 = b2 + kstep; \
;             if (last && has_next) S.a_ready(nxt);
; template <class Epi, class Sched, bool ALIGN_EPI = false, bool SP2 = false>
; __device__ __forceinline__ void gemm_phase(PG8_LAS unsigned char* lds, const Gemm g, const Sched& S, const Epi& E) {
;     ...
;         if constexpr (SP2) {
;             { PG8_TRIP_HEAD(0) PG8_TRIP_SP2(asm volatile("s_waitcnt vmcnt(%0)" :: "n"(8 + Epi::NST) : "memory"), PG8_MMAZ) }
	v_mfma_f32_16x16x32_bf16 v[56:59], v[120:123], v[180:183], v[56:59]
	v_mfma_f32_16x16x32_bf16 v[56:59], v[132:135], v[184:187], v[56:59]
	v_mfma_f32_16x16x32_bf16 v[52:55], v[144:147], v[180:183], v[52:55]
	v_mfma_f32_16x16x32_bf16 v[52:55], v[148:151], v[184:187], v[52:55]
	v_mfma_f32_16x16x32_bf16 v[48:51], v[120:123], v[190:193], v[48:51]
	v_mfma_f32_16x16x32_bf16 v[48:51], v[132:135], v[194:197], v[48:51]
	v_mfma_f32_16x16x32_bf16 v[44:47], v[144:147], v[190:193], v[44:47]
	v_mfma_f32_16x16x32_bf16 v[44:47], v[148:151], v[194:197], v[44:47]
	v_mfma_f32_16x16x32_bf16 v[32:35], v[120:123], v[198:201], v[32:35]
	v_mfma_f32_16x16x32_bf16 v[32:35], v[132:135], v[202:205], v[32:35]
	v_mfma_f32_16x16x32_bf16 v[28:31], v[144:147], v[198:201], v[28:31]
	v_mfma_f32_16x16x32_bf16 v[28:31], v[148:151], v[202:205], v[28:31]
	v_mfma_f32_16x16x32_bf16 v[16:19], v[120:123], v[206:209], v[16:19]
	v_mfma_f32_16x16x32_bf16 v[16:19], v[132:135], v[216:219], v[16:19]
	v_mfma_f32_16x16x32_bf16 v[12:15], v[144:147], v[206:209], v[12:15]
	v_mfma_f32_16x16x32_bf16 v[12:15], v[148:151], v[216:219], v[12:15]
	v_mfma_f32_16x16x32_bf16 v[64:67], v[152:155], v[180:183], v[64:67]
	v_mfma_f32_16x16x32_bf16 v[64:67], v[156:159], v[184:187], v[64:67]
	v_mfma_f32_16x16x32_bf16 v[60:63], v[166:169], v[180:183], v[60:63]
	v_mfma_f32_16x16x32_bf16 v[60:63], v[170:173], v[184:187], v[60:63]
	v_mfma_f32_16x16x32_bf16 v[40:43], v[152:155], v[190:193], v[40:43]
	v_mfma_f32_16x16x32_bf16 v[40:43], v[156:159], v[194:197], v[40:43]
	v_mfma_f32_16x16x32_bf16 v[36:39], v[166:169], v[190:193], v[36:39]
	v_mfma_f32_16x16x32_bf16 v[36:39], v[170:173], v[194:197], v[36:39]
	v_mfma_f32_16x16x32_bf16 v[24:27], v[152:155], v[198:201], v[24:27]
	v_mfma_f32_16x16x32_bf16 v[24:27], v[156:159], v[202:205], v[24:27]
	v_mfma_f32_16x16x32_bf16 v[20:23], v[166:169], v[198:201], v[20:23]
	v_mfma_f32_16x16x32_bf16 v[20:23], v[170:173], v[202:205], v[20:23]
	v_mfma_f32_16x16x32_bf16 v[8:11], v[152:155], v[206:209], v[8:11]
	v_mfma_f32_16x16x32_bf16 v[8:11], v[156:159], v[216:219], v[8:11]
	v_mfma_f32_16x16x32_bf16 v[4:7], v[166:169], v[206:209], v[4:7]
	v_mfma_f32_16x16x32_bf16 v[4:7], v[170:173], v[216:219], v[4:7]
	s_barrier
	ds_read_b128 v[120:123], v118
	ds_read_b128 v[132:135], v118 offset:1024
	ds_read_b128 v[144:147], v118 offset:2048
	ds_read_b128 v[148:151], v118 offset:3072
	ds_read_b128 v[152:155], v119
	ds_read_b128 v[156:159], v119 offset:1024
	ds_read_b128 v[166:169], v119 offset:2048
	ds_read_b128 v[170:173], v119 offset:3072
	s_mov_b32 m0, s35
	v_lshl_add_u64 v[220:221], v[214:215], 0, s[54:55]
	ds_read_b128 v[180:183], v178 offset:32768
	ds_read_b128 v[184:187], v178 offset:33792
	ds_read_b128 v[190:193], v178 offset:34816
	ds_read_b128 v[194:197], v178 offset:35840
	ds_read_b128 v[198:201], v178 offset:36864
	ds_read_b128 v[202:205], v178 offset:37888
	ds_read_b128 v[206:209], v178 offset:38912
	ds_read_b128 v[216:219], v178 offset:39936
	global_load_lds_dwordx4 v[220:221], off
	v_lshl_add_u64 v[220:221], v[214:215], 0, s[56:57]
	s_mov_b32 m0, s36
	s_nop 0
	global_load_lds_dwordx4 v[220:221], off
	s_waitcnt vmcnt(8)
	s_waitcnt lgkmcnt(0)
	s_barrier
	v_mfma_f32_16x16x32_bf16 v[140:143], v[120:123], v[180:183], v[140:143]
	v_mfma_f32_16x16x32_bf16 v[140:143], v[132:135], v[184:187], v[140:143]
	v_mfma_f32_16x16x32_bf16 v[136:139], v[144:147], v[180:183], v[136:139]
	v_mfma_f32_16x16x32_bf16 v[136:139], v[148:151], v[184:187], v[136:139]
	v_mfma_f32_16x16x32_bf16 v[112:115], v[120:123], v[190:193], v[112:115]
	v_mfma_f32_16x16x32_bf16 v[112:115], v[132:135], v[194:197], v[112:115]
	v_mfma_f32_16x16x32_bf16 v[108:111], v[144:147], v[190:193], v[108:111]
	v_mfma_f32_16x16x32_bf16 v[108:111], v[148:151], v[194:197], v[108:111]
	v_mfma_f32_16x16x32_bf16 v[96:99], v[120:123], v[198:201], v[96:99]
	v_mfma_f32_16x16x32_bf16 v[96:99], v[132:135], v[202:205], v[96:99]
	v_mfma_f32_16x16x32_bf16 v[92:95], v[144:147], v[198:201], v[92:95]
	v_mfma_f32_16x16x32_bf16 v[92:95], v[148:151], v[202:205], v[92:95]
	v_mfma_f32_16x16x32_bf16 v[80:83], v[120:123], v[206:209], v[80:83]
	v_mfma_f32_16x16x32_bf16 v[80:83], v[132:135], v[216:219], v[80:83]
	v_mfma_f32_16x16x32_bf16 v[76:79], v[144:147], v[206:209], v[76:79]
	v_mfma_f32_16x16x32_bf16 v[76:79], v[148:151], v[216:219], v[76:79]
	v_mfma_f32_16x16x32_bf16 v[128:131], v[152:155], v[180:183], v[128:131]
	v_mfma_f32_16x16x32_bf16 v[128:131], v[156:159], v[184:187], v[128:131]
	v_mfma_f32_16x16x32_bf16 v[124:127], v[166:169], v[180:183], v[124:127]
	v_mfma_f32_16x16x32_bf16 v[124:127], v[170:173], v[184:187], v[124:127]
	v_mfma_f32_16x16x32_bf16 v[104:107], v[152:155], v[190:193], v[104:107]
	v_mfma_f32_16x16x32_bf16 v[104:107], v[156:159], v[194:197], v[104:107]
	v_mfma_f32_16x16x32_bf16 v[100:103], v[166:169], v[190:193], v[100:103]
	v_mfma_f32_16x16x32_bf16 v[100:103], v[170:173], v[194:197], v[100:103]
	v_mfma_f32_16x16x32_bf16 v[88:91], v[152:155], v[198:201], v[88:91]
	v_mfma_f32_16x16x32_bf16 v[88:91], v[156:159], v[202:205], v[88:91]
	v_mfma_f32_16x16x32_bf16 v[84:87], v[166:169], v[198:201], v[84:87]
	v_mfma_f32_16x16x32_bf16 v[84:87], v[170:173], v[202:205], v[84:87]
	v_mfma_f32_16x16x32_bf16 v[72:75], v[152:155], v[206:209], v[72:75]
	v_mfma_f32_16x16x32_bf16 v[72:75], v[156:159], v[216:219], v[72:75]
	v_mfma_f32_16x16x32_bf16 v[68:71], v[166:169], v[206:209], v[68:71]
	v_mfma_f32_16x16x32_bf16 v[68:71], v[170:173], v[216:219], v[68:71]
	s_barrier
; #define PG8_MMA(ai, bj, At, Bt) do { __builtin_amdgcn_s_setprio(1); _Pragma("unroll") for (int m = 0; m < 4; ++m) _Pragma("unroll") for (int n = 0; n < 2; ++n) _Pragma("unroll") for (int k = 0; k < 2; ++k) \
;         acc[ai][bj][m][n] = __builtin_amdgcn_mfma_f32_16x16x32_bf16(Bt[n][k], At[m][k], acc[ai][bj][m][n], 0, 0, 0); __builtin_amdgcn_s_setprio(0); } while (0)
; #define PG8_WAIT_V(n) asm volatile("s_waitcnt vmcnt(" #n ")" ::: "memory")
; #define PG8_BAR __builtin_amdgcn_s_barrier()
; #define PG8_TRIP_HEAD(T) const int t = (T); const bool last = (t == nt - 2); \
;             const char* a1 = cA + (size_t)(t + 1) * kstep; \
;             const char* a2 = last ? nA : cA + (size_t)(t + 2) * kstep; const char* b2 = last ? nB : cB + (size_t)(t + 2) * kstep; \
;             const char* a3 = a2 + kstep; const char* b3 = b2 + kstep; \
;             if (last && has_next) S.a_ready(nxt);
; template <class Epi, class Sched, bool ALIGN_EPI = false, bool SP2 = false>
; __device__ __forceinline__ void gemm_phase(PG8_LAS unsigned char* lds, const Gemm g, const Sched& S, const Epi& E) {
;     ...
;         if constexpr (SP2) {
;             { PG8_TRIP_HEAD(0) PG8_TRIP_SP2(asm volatile("s_waitcnt vmcnt(%0)" :: "n"(8 + Epi::NST) : "memory"), PG8_MMAZ) }
;             for (int tt = 2; tt < nt; tt += 2) { PG8_TRIP_HEAD(tt) PG8_TRIP_SP2(PG8_WAIT_V(8), PG8_MMA) }
;     ...
;         if constexpr (ALIGN_EPI) { if (wr == 0) PG8_BAR; }
	s_mov_b32 m0, s44
	v_lshl_add_u64 v[220:221], v[188:189], 0, s[78:79]
	ds_read_b128 v[180:183], v178 offset:49152
	ds_read_b128 v[184:187], v178 offset:50176
	ds_read_b128 v[190:193], v178 offset:51200
	ds_read_b128 v[194:197], v178 offset:52224
	ds_read_b128 v[198:201], v178 offset:53248
	ds_read_b128 v[202:205], v178 offset:54272
	ds_read_b128 v[206:209], v178 offset:55296
	ds_read_b128 v[216:219], v178 offset:56320
	global_load_lds_dwordx4 v[220:221], off
	v_lshl_add_u64 v[220:221], v[188:189], 0, s[60:61]
	s_mov_b32 m0, s45
	s_nop 0
	global_load_lds_dwordx4 v[220:221], off
	v_lshl_add_u64 v[220:221], v[188:189], 0, s[62:63]
	s_mov_b32 m0, s46
	v_lshl_add_u64 v[188:189], v[188:189], 0, s[64:65]
	global_load_lds_dwordx4 v[220:221], off
	s_mov_b32 m0, s47
	s_nop 0
	global_load_lds_dwordx4 v[188:189], off
	v_lshl_add_u64 v[188:189], v[214:215], 0, s[78:79]
	s_mov_b32 m0, s37
	s_nop 0
	global_load_lds_dwordx4 v[188:189], off
	v_lshl_add_u64 v[188:189], v[214:215], 0, s[60:61]
	s_mov_b32 m0, s38
	s_nop 0
	global_load_lds_dwordx4 v[188:189], off
	s_waitcnt vmcnt(8)
	s_waitcnt lgkmcnt(0)
	s_barrier
	v_mfma_f32_16x16x32_bf16 v[56:59], v[120:123], v[180:183], v[56:59]
	v_mfma_f32_16x16x32_bf16 v[56:59], v[132:135], v[184:187], v[56:59]
	v_mfma_f32_16x16x32_bf16 v[52:55], v[144:147], v[180:183], v[52:55]
	v_mfma_f32_16x16x32_bf16 v[52:55], v[148:151], v[184:187], v[52:55]
	v_mfma_f32_16x16x32_bf16 v[48:51], v[120:123], v[190:193], v[48:51]
	v_mfma_f32_16x16x32_bf16 v[48:51], v[132:135], v[194:197], v[48:51]
	v_mfma_f32_16x16x32_bf16 v[44:47], v[144:147], v[190:193], v[44:47]
	v_mfma_f32_16x16x32_bf16 v[44:47], v[148:151], v[194:197], v[44:47]
	v_mfma_f32_16x16x32_bf16 v[32:35], v[120:123], v[198:201], v[32:35]
	v_mfma_f32_16x16x32_bf16 v[32:35], v[132:135], v[202:205], v[32:35]
	v_mfma_f32_16x16x32_bf16 v[28:31], v[144:147], v[198:201], v[28:31]
	v_mfma_f32_16x16x32_bf16 v[28:31], v[148:151], v[202:205], v[28:31]
	v_mfma_f32_16x16x32_bf16 v[16:19], v[120:123], v[206:209], v[16:19]
	v_mfma_f32_16x16x32_bf16 v[16:19], v[132:135], v[216:219], v[16:19]
	v_mfma_f32_16x16x32_bf16 v[12:15], v[144:147], v[206:209], v[12:15]
	v_mfma_f32_16x16x32_bf16 v[12:15], v[148:151], v[216:219], v[12:15]
	v_mfma_f32_16x16x32_bf16 v[64:67], v[152:155], v[180:183], v[64:67]
	v_mfma_f32_16x16x32_bf16 v[64:67], v[156:159], v[184:187], v[64:67]
	v_mfma_f32_16x16x32_bf16 v[60:63], v[166:169], v[180:183], v[60:63]
	v_mfma_f32_16x16x32_bf16 v[60:63], v[170:173], v[184:187], v[60:63]
	v_mfma_f32_16x16x32_bf16 v[40:43], v[152:155], v[190:193], v[40:43]
	v_mfma_f32_16x16x32_bf16 v[40:43], v[156:159], v[194:197], v[40:43]
	v_mfma_f32_16x16x32_bf16 v[36:39], v[166:169], v[190:193], v[36:39]
	v_mfma_f32_16x16x32_bf16 v[36:39], v[170:173], v[194:197], v[36:39]
	v_mfma_f32_16x16x32_bf16 v[24:27], v[152:155], v[198:201], v[24:27]
	v_mfma_f32_16x16x32_bf16 v[24:27], v[156:159], v[202:205], v[24:27]
	v_mfma_f32_16x16x32_bf16 v[20:23], v[166:169], v[198:201], v[20:23]
	v_mfma_f32_16x16x32_bf16 v[20:23], v[170:173], v[202:205], v[20:23]
	v_mfma_f32_16x16x32_bf16 v[8:11], v[152:155], v[206:209], v[8:11]
	v_mfma_f32_16x16x32_bf16 v[8:11], v[156:159], v[216:219], v[8:11]
	v_mfma_f32_16x16x32_bf16 v[4:7], v[166:169], v[206:209], v[4:7]
	v_mfma_f32_16x16x32_bf16 v[4:7], v[170:173], v[216:219], v[4:7]
	s_barrier
	s_add_i32 s48, s48, 2
	s_add_u32 s26, s26, 0x100
	s_addc_u32 s27, s27, 0
	s_add_u32 s24, s24, 0x100
	s_addc_u32 s25, s25, 0
	s_cmpk_gt_u32 s48, 0x55
	s_cbranch_scc0 .LBB0_233
	s_and_b64 vcc, exec, s[18:19]
	s_cbranch_vccz .LBB0_236
	s_barrier

;     __device__ bool next(int i, Unit& u) const { const int rounds = nwg / G; if (i >= rounds) return false; return StaticOrder::next(rounds - 1 - i, u); }
;     __device__ bool next(int i, Unit& u) const { const int rounds = nwg / G; if (i >= 2 * rounds) return false; const bool ok = StaticOrder::next(i >= rounds ? i - rounds : i, u); u.z = (i >= rounds) ? 1 : 0; return ok; }
; #define PG8_TRIP_HEAD(T) const int t = (T); const bool last = (t == nt - 2); \
;             const char* a1 = cA + (size_t)(t + 1) * kstep; \
;             const char* a2 = last ? nA : cA + (size_t)(t + 2) * kstep; const char* b2 = last ? nB : cB + (size_t)(t + 2) * kstep; \
;             const char* a3 = a2 + kstep; const char* b3 = b2 + kstep; \
;             if (last && has_next) S.a_ready(nxt);
; template <class Epi, class Sched, bool ALIGN_EPI = false, bool SP2 = false>
; __device__ __forceinline__ void gemm_phase(PG8_LAS unsigned char* lds, const Gemm g, const Sched& S, const Epi& E) {
;     ...
;         const bool has_next = S.next(ui + 1, nxt);
;         const char* nA = has_next ? (const char*)S.opA(g, nxt) + (size_t)nxt.pm * tstepA : cA; const char* nB = has_next ? (const char*)S.opB(g, nxt) + (size_t)nxt.pn * tstepB : cB;
;     ...
;         if constexpr (SP2) {
;             { PG8_TRIP_HEAD(0) PG8_TRIP_SP2(asm volatile("s_waitcnt vmcnt(%0)" :: "n"(8 + Epi::NST) : "memory"), PG8_MMAZ) }
.LBB0_323:
	s_ashr_i32 s23, s22, 31
	s_lshl_b64 s[4:5], s[22:23], 20
	v_readlane_b32 s26, v254, 18
	v_readlane_b32 s27, v254, 19
	s_add_u32 s26, s26, s4
	s_addc_u32 s27, s27, s5
	s_add_i32 s28, 0, 0x10000
	s_add_i32 s33, 0, 0x14000
	v_add_u32_e32 v132, s28, v197
	s_waitcnt lgkmcnt(0)
	v_add_u32_e32 v133, s33, v197
	ds_read_b128 v[4:7], v132
	ds_read_b128 v[8:11], v132 offset:1024
	ds_read_b128 v[12:15], v132 offset:2048
	ds_read_b128 v[16:19], v132 offset:3072
	ds_read_b128 v[20:23], v133
	ds_read_b128 v[24:27], v133 offset:1024
	ds_read_b128 v[28:31], v133 offset:2048
	ds_read_b128 v[32:35], v133 offset:3072
	s_and_b64 s[4:5], s[10:11], exec
	s_cselect_b32 s3, s27, s13
	s_cselect_b32 s4, s26, s12
	v_lshl_add_u64 v[194:195], s[14:15], 0, v[166:167]
	s_mov_b64 s[10:11], 0x84080
	s_add_i32 s5, s30, 0xc000
	v_lshl_add_u64 v[68:69], v[194:195], 0, s[10:11]
	s_mov_b32 m0, s5
	s_mov_b64 s[10:11], 0xc6080
	s_add_i32 s23, s30, 0xe000
	ds_read_b128 v[36:39], v200
	ds_read_b128 v[40:43], v200 offset:1024
	ds_read_b128 v[44:47], v200 offset:2048
	ds_read_b128 v[48:51], v200 offset:3072
	ds_read_b128 v[52:55], v200 offset:4096
	ds_read_b128 v[56:59], v200 offset:5120
	ds_read_b128 v[60:63], v200 offset:6144
	ds_read_b128 v[64:67], v200 offset:7168
	global_load_lds_dwordx4 v[68:69], off
	v_lshl_add_u64 v[68:69], v[194:195], 0, s[10:11]
	s_mov_b32 m0, s23
	s_nop 0
	global_load_lds_dwordx4 v[68:69], off
	s_waitcnt vmcnt(16)
	s_waitcnt lgkmcnt(0)
	s_barrier
	v_mfma_f32_16x16x32_bf16 v[88:91], v[12:15], v[52:55], 0
	v_mfma_f32_16x16x32_bf16 v[92:95], v[16:19], v[56:59], v[88:91]
	v_mfma_f32_16x16x32_bf16 v[88:91], v[4:7], v[60:63], 0
	v_mfma_f32_16x16x32_bf16 v[68:71], v[4:7], v[36:39], 0
	v_mfma_f32_16x16x32_bf16 v[72:75], v[12:15], v[36:39], 0
	v_mfma_f32_16x16x32_bf16 v[76:79], v[4:7], v[44:47], 0
	v_mfma_f32_16x16x32_bf16 v[80:83], v[12:15], v[44:47], 0
	v_mfma_f32_16x16x32_bf16 v[84:87], v[4:7], v[52:55], 0
	v_mfma_f32_16x16x32_bf16 v[96:99], v[8:11], v[64:67], v[88:91]
	v_mfma_f32_16x16x32_bf16 v[88:91], v[12:15], v[60:63], 0
	v_mfma_f32_16x16x32_bf16 v[68:71], v[8:11], v[40:43], v[68:71]
	v_mfma_f32_16x16x32_bf16 v[72:75], v[16:19], v[40:43], v[72:75]
	v_mfma_f32_16x16x32_bf16 v[76:79], v[8:11], v[48:51], v[76:79]
	v_mfma_f32_16x16x32_bf16 v[80:83], v[16:19], v[48:51], v[80:83]
	v_mfma_f32_16x16x32_bf16 v[84:87], v[8:11], v[56:59], v[84:87]
	v_mfma_f32_16x16x32_bf16 v[108:111], v[16:19], v[64:67], v[88:91]
	v_mfma_f32_16x16x32_bf16 v[88:91], v[20:23], v[36:39], 0
	v_mfma_f32_16x16x32_bf16 v[36:39], v[28:31], v[36:39], 0
	v_mfma_f32_16x16x32_bf16 v[112:115], v[24:27], v[40:43], v[88:91]
	v_mfma_f32_16x16x32_bf16 v[36:39], v[32:35], v[40:43], v[36:39]
	v_mfma_f32_16x16x32_bf16 v[40:43], v[20:23], v[44:47], 0
	v_mfma_f32_16x16x32_bf16 v[44:47], v[28:31], v[44:47], 0
	v_mfma_f32_16x16x32_bf16 v[40:43], v[24:27], v[48:51], v[40:43]
	v_mfma_f32_16x16x32_bf16 v[44:47], v[32:35], v[48:51], v[44:47]
	v_mfma_f32_16x16x32_bf16 v[48:51], v[20:23], v[52:55], 0
	v_mfma_f32_16x16x32_bf16 v[52:55], v[28:31], v[52:55], 0
	v_mfma_f32_16x16x32_bf16 v[48:51], v[24:27], v[56:59], v[48:51]
	v_mfma_f32_16x16x32_bf16 v[52:55], v[32:35], v[56:59], v[52:55]
	v_mfma_f32_16x16x32_bf16 v[56:59], v[20:23], v[60:63], 0
	v_mfma_f32_16x16x32_bf16 v[60:63], v[28:31], v[60:63], 0
	v_mfma_f32_16x16x32_bf16 v[56:59], v[24:27], v[64:67], v[56:59]
	v_mfma_f32_16x16x32_bf16 v[60:63], v[32:35], v[64:67], v[60:63]
	s_barrier
	v_lshl_add_u64 v[214:215], s[12:13], 0, v[164:165]
	s_mov_b64 s[10:11], 0x100
	s_add_i32 s28, s28, s0
	v_lshl_add_u64 v[134:135], v[214:215], 0, s[10:11]
	s_mov_b32 m0, s28
	s_mov_b64 s[46:47], 0x40100
	s_add_i32 s29, s28, 0x2000
	ds_read_b128 v[64:67], v200 offset:16384
	ds_read_b128 v[88:91], v200 offset:17408
	ds_read_b128 v[100:103], v200 offset:18432
	ds_read_b128 v[104:107], v200 offset:19456
	ds_read_b128 v[116:119], v200 offset:20480
	ds_read_b128 v[120:123], v200 offset:21504
	ds_read_b128 v[124:127], v200 offset:22528
	ds_read_b128 v[128:131], v200 offset:23552
	global_load_lds_dwordx4 v[134:135], off
	v_lshl_add_u64 v[134:135], v[214:215], 0, s[46:47]
	s_mov_b32 m0, s29
	s_mov_b64 s[46:47], 0x80100
	s_add_i32 s33, s33, s0
	global_load_lds_dwordx4 v[134:135], off
	v_lshl_add_u64 v[134:135], v[214:215], 0, s[46:47]
	s_mov_b32 m0, s33
	s_mov_b64 s[46:47], 0xc0100
	s_add_i32 s45, s33, 0x2000
	global_load_lds_dwordx4 v[134:135], off
	v_lshl_add_u64 v[134:135], v[214:215], 0, s[46:47]
	s_mov_b32 m0, s45
	s_nop 0
	global_load_lds_dwordx4 v[134:135], off
	v_lshl_add_u64 v[134:135], v[194:195], 0, s[10:11]
	s_mov_b32 m0, s30
	s_mov_b64 s[10:11], 0x42100
	global_load_lds_dwordx4 v[134:135], off
	v_lshl_add_u64 v[134:135], v[194:195], 0, s[10:11]
	s_mov_b32 m0, s31
	s_nop 0
	global_load_lds_dwordx4 v[134:135], off
	s_waitcnt vmcnt(16)
	s_waitcnt lgkmcnt(0)
	s_barrier
; #define PG8_TRIP_HEAD(T) const int t = (T); const bool last = (t == nt - 2); \
;             const char* a1 = cA + (size_t)(t + 1) * kstep; \
;             const char* a2 = last ? nA : cA + (size_t)(t + 2) * kstep; const char* b2 = last ? nB : cB + (size_t)(t + 2) * kstep; \
;             const char* a3 = a2 + kstep; const char* b3 = b2 + kstep; \
;             if (last && has_next) S.a_ready(nxt);
; template <class Epi, class Sched, bool ALIGN_EPI = false, bool SP2 = false>
; __device__ __forceinline__ void gemm_phase(PG8_LAS unsigned char* lds, const Gemm g, const Sched& S, const Epi& E) {
;     ...
;         if constexpr (SP2) {
;             { PG8_TRIP_HEAD(0) PG8_TRIP_SP2(asm volatile("s_waitcnt vmcnt(%0)" :: "n"(8 + Epi::NST) : "memory"), PG8_MMAZ) }
	v_mfma_f32_16x16x32_bf16 v[134:137], v[4:7], v[64:67], 0
	v_mfma_f32_16x16x32_bf16 v[144:147], v[4:7], v[100:103], 0
	v_mfma_f32_16x16x32_bf16 v[152:155], v[4:7], v[116:119], 0
	v_mfma_f32_16x16x32_bf16 v[4:7], v[4:7], v[124:127], 0
	v_mfma_f32_16x16x32_bf16 v[136:139], v[8:11], v[88:91], v[134:137]
	v_mfma_f32_16x16x32_bf16 v[144:147], v[8:11], v[104:107], v[144:147]
	v_mfma_f32_16x16x32_bf16 v[152:155], v[8:11], v[120:123], v[152:155]
	v_mfma_f32_16x16x32_bf16 v[4:7], v[8:11], v[128:131], v[4:7]
	v_mfma_f32_16x16x32_bf16 v[8:11], v[12:15], v[124:127], 0
	v_mfma_f32_16x16x32_bf16 v[140:143], v[12:15], v[64:67], 0
	v_mfma_f32_16x16x32_bf16 v[148:151], v[12:15], v[100:103], 0
	v_mfma_f32_16x16x32_bf16 v[156:159], v[12:15], v[116:119], 0
	v_mfma_f32_16x16x32_bf16 v[12:15], v[16:19], v[128:131], v[8:11]
	v_mfma_f32_16x16x32_bf16 v[140:143], v[16:19], v[88:91], v[140:143]
	v_mfma_f32_16x16x32_bf16 v[148:151], v[16:19], v[104:107], v[148:151]
	v_mfma_f32_16x16x32_bf16 v[156:159], v[16:19], v[120:123], v[156:159]
	v_mfma_f32_16x16x32_bf16 v[8:11], v[20:23], v[64:67], 0
	v_mfma_f32_16x16x32_bf16 v[16:19], v[24:27], v[88:91], v[8:11]
	v_mfma_f32_16x16x32_bf16 v[8:11], v[28:31], v[64:67], 0
	v_mfma_f32_16x16x32_bf16 v[160:163], v[32:35], v[88:91], v[8:11]
	v_mfma_f32_16x16x32_bf16 v[8:11], v[20:23], v[100:103], 0
	v_mfma_f32_16x16x32_bf16 v[174:177], v[24:27], v[104:107], v[8:11]
	v_mfma_f32_16x16x32_bf16 v[8:11], v[28:31], v[100:103], 0
	v_mfma_f32_16x16x32_bf16 v[178:181], v[32:35], v[104:107], v[8:11]
	v_mfma_f32_16x16x32_bf16 v[8:11], v[20:23], v[116:119], 0
	v_mfma_f32_16x16x32_bf16 v[182:185], v[24:27], v[120:123], v[8:11]
	v_mfma_f32_16x16x32_bf16 v[8:11], v[28:31], v[116:119], 0
	v_mfma_f32_16x16x32_bf16 v[190:193], v[32:35], v[120:123], v[8:11]
	v_mfma_f32_16x16x32_bf16 v[8:11], v[20:23], v[124:127], 0
	v_mfma_f32_16x16x32_bf16 v[202:205], v[24:27], v[128:131], v[8:11]
	v_mfma_f32_16x16x32_bf16 v[8:11], v[28:31], v[124:127], 0
	v_mfma_f32_16x16x32_bf16 v[206:209], v[32:35], v[128:131], v[8:11]
	s_barrier
	s_add_i32 s46, 0, 0x18000
	s_add_i32 s48, 0, 0x1c000
	v_add_u32_e32 v134, s46, v197
	v_add_u32_e32 v135, s48, v197
	s_nop 0
	ds_read_b128 v[8:11], v134
	ds_read_b128 v[28:31], v134 offset:1024
	ds_read_b128 v[32:35], v134 offset:2048
	ds_read_b128 v[64:67], v134 offset:3072
	ds_read_b128 v[216:219], v135
	ds_read_b128 v[220:223], v135 offset:1024
	ds_read_b128 v[224:227], v135 offset:2048
	ds_read_b128 v[228:231], v135 offset:3072
	s_mov_b64 s[10:11], 0x84100
	s_mov_b32 m0, s34
	v_lshl_add_u64 v[88:89], v[194:195], 0, s[10:11]
	s_mov_b64 s[10:11], 0xc6100
	ds_read_b128 v[20:23], v200 offset:32768
	ds_read_b128 v[24:27], v200 offset:33792
	ds_read_b128 v[232:235], v200 offset:34816
	ds_read_b128 v[236:239], v200 offset:35840
	ds_read_b128 v[240:243], v200 offset:36864
	ds_read_b128 v[244:247], v200 offset:37888
	ds_read_b128 v[248:251], v200 offset:38912
	ds_read_b128 v[186:189], v200 offset:39936
	global_load_lds_dwordx4 v[88:89], off
	v_lshl_add_u64 v[88:89], v[194:195], 0, s[10:11]
	s_mov_b32 m0, s35
	s_nop 0
	global_load_lds_dwordx4 v[88:89], off
	s_waitcnt vmcnt(8)
	s_waitcnt lgkmcnt(0)
	s_barrier
	v_mfma_f32_16x16x32_bf16 v[68:71], v[8:11], v[20:23], v[68:71]
	v_mfma_f32_16x16x32_bf16 v[120:123], v[28:31], v[24:27], v[68:71]
	v_mfma_f32_16x16x32_bf16 v[68:71], v[32:35], v[20:23], v[72:75]
	v_mfma_f32_16x16x32_bf16 v[116:119], v[64:67], v[24:27], v[68:71]
	v_mfma_f32_16x16x32_bf16 v[68:71], v[8:11], v[232:235], v[76:79]
	v_mfma_f32_16x16x32_bf16 v[104:107], v[28:31], v[236:239], v[68:71]
	v_mfma_f32_16x16x32_bf16 v[68:71], v[32:35], v[232:235], v[80:83]
	v_mfma_f32_16x16x32_bf16 v[100:103], v[64:67], v[236:239], v[68:71]
	v_mfma_f32_16x16x32_bf16 v[68:71], v[8:11], v[240:243], v[84:87]
	v_mfma_f32_16x16x32_bf16 v[88:91], v[28:31], v[244:247], v[68:71]
	v_mfma_f32_16x16x32_bf16 v[68:71], v[32:35], v[240:243], v[92:95]
	v_mfma_f32_16x16x32_bf16 v[84:87], v[64:67], v[244:247], v[68:71]
	v_mfma_f32_16x16x32_bf16 v[68:71], v[8:11], v[248:251], v[96:99]
	v_mfma_f32_16x16x32_bf16 v[72:75], v[28:31], v[186:189], v[68:71]
	v_mfma_f32_16x16x32_bf16 v[68:71], v[32:35], v[248:251], v[108:111]
	v_mfma_f32_16x16x32_bf16 v[68:71], v[64:67], v[186:189], v[68:71]
	v_mfma_f32_16x16x32_bf16 v[76:79], v[216:219], v[20:23], v[112:115]
	v_mfma_f32_16x16x32_bf16 v[20:23], v[224:227], v[20:23], v[36:39]
	v_mfma_f32_16x16x32_bf16 v[124:127], v[228:231], v[24:27], v[20:23]
	v_mfma_f32_16x16x32_bf16 v[20:23], v[216:219], v[232:235], v[40:43]
	v_mfma_f32_16x16x32_bf16 v[112:115], v[220:223], v[236:239], v[20:23]
	v_mfma_f32_16x16x32_bf16 v[20:23], v[224:227], v[232:235], v[44:47]
	v_mfma_f32_16x16x32_bf16 v[108:111], v[228:231], v[236:239], v[20:23]
	v_mfma_f32_16x16x32_bf16 v[20:23], v[216:219], v[240:243], v[48:51]
	v_mfma_f32_16x16x32_bf16 v[96:99], v[220:223], v[244:247], v[20:23]
	v_mfma_f32_16x16x32_bf16 v[20:23], v[224:227], v[240:243], v[52:55]
	v_mfma_f32_16x16x32_bf16 v[92:95], v[228:231], v[244:247], v[20:23]
	v_mfma_f32_16x16x32_bf16 v[20:23], v[216:219], v[248:251], v[56:59]
	v_mfma_f32_16x16x32_bf16 v[80:83], v[220:223], v[186:189], v[20:23]
	v_mfma_f32_16x16x32_bf16 v[20:23], v[224:227], v[248:251], v[60:63]
	v_mfma_f32_16x16x32_bf16 v[128:131], v[220:223], v[24:27], v[76:79]
	v_mfma_f32_16x16x32_bf16 v[76:79], v[228:231], v[186:189], v[20:23]
	s_barrier
; #define PG8_MMA(ai, bj, At, Bt) do { __builtin_amdgcn_s_setprio(1); _Pragma("unroll") for (int m = 0; m < 4; ++m) _Pragma("unroll") for (int n = 0; n < 2; ++n) _Pragma("unroll") for (int k = 0; k < 2; ++k) \
;         acc[ai][bj][m][n] = __builtin_amdgcn_mfma_f32_16x16x32_bf16(Bt[n][k], At[m][k], acc[ai][bj][m][n], 0, 0, 0); __builtin_amdgcn_s_setprio(0); } while (0)
; #define PG8_WAIT_V(n) asm volatile("s_waitcnt vmcnt(" #n ")" ::: "memory")
; #define PG8_TRIP_HEAD(T) const int t = (T); const bool last = (t == nt - 2); \
;             const char* a1 = cA + (size_t)(t + 1) * kstep; \
;             const char* a2 = last ? nA : cA + (size_t)(t + 2) * kstep; const char* b2 = last ? nB : cB + (size_t)(t + 2) * kstep; \
;             const char* a3 = a2 + kstep; const char* b3 = b2 + kstep; \
;             if (last && has_next) S.a_ready(nxt);
; template <class Epi, class Sched, bool ALIGN_EPI = false, bool SP2 = false>
; __device__ __forceinline__ void gemm_phase(PG8_LAS unsigned char* lds, const Gemm g, const Sched& S, const Epi& E) {
;     ...
;         if constexpr (SP2) {
;             { PG8_TRIP_HEAD(0) PG8_TRIP_SP2(asm volatile("s_waitcnt vmcnt(%0)" :: "n"(8 + Epi::NST) : "memory"), PG8_MMAZ) }
;             for (int tt = 2; tt < nt; tt += 2) { PG8_TRIP_HEAD(tt) PG8_TRIP_SP2(PG8_WAIT_V(8), PG8_MMA) }
	s_mov_b64 s[10:11], 0x180
	s_add_i32 s46, s46, s0
	s_nop 1
	v_lshl_add_u64 v[20:21], v[214:215], 0, s[10:11]
	s_mov_b32 m0, s46
	s_mov_b64 s[50:51], 0x40180
	s_add_i32 s47, s46, 0x2000
	ds_read_b128 v[44:47], v200 offset:49152
	ds_read_b128 v[48:51], v200 offset:50176
	ds_read_b128 v[186:189], v200 offset:51200
	ds_read_b128 v[232:235], v200 offset:52224
	ds_read_b128 v[236:239], v200 offset:53248
	ds_read_b128 v[240:243], v200 offset:54272
	ds_read_b128 v[244:247], v200 offset:55296
	ds_read_b128 v[248:251], v200 offset:56320
	global_load_lds_dwordx4 v[20:21], off
	v_lshl_add_u64 v[20:21], v[214:215], 0, s[50:51]
	s_mov_b32 m0, s47
	s_mov_b64 s[50:51], 0x80180
	s_add_i32 s48, s48, s0
	global_load_lds_dwordx4 v[20:21], off
	v_lshl_add_u64 v[20:21], v[214:215], 0, s[50:51]
	s_mov_b32 m0, s48
	s_mov_b64 s[50:51], 0xc0180
	s_add_i32 s49, s48, 0x2000
	global_load_lds_dwordx4 v[20:21], off
	v_lshl_add_u64 v[20:21], v[214:215], 0, s[50:51]
	s_mov_b32 m0, s49
	s_nop 0
	global_load_lds_dwordx4 v[20:21], off
	v_lshl_add_u64 v[20:21], v[194:195], 0, s[10:11]
	s_mov_b32 m0, s38
	s_mov_b64 s[10:11], 0x42180
	global_load_lds_dwordx4 v[20:21], off
	v_lshl_add_u64 v[20:21], v[194:195], 0, s[10:11]
	s_mov_b32 m0, s39
	s_nop 0
	global_load_lds_dwordx4 v[20:21], off
	s_waitcnt vmcnt(8)
	s_waitcnt lgkmcnt(0)
	s_barrier
	v_mfma_f32_16x16x32_bf16 v[20:23], v[8:11], v[44:47], v[136:139]
	v_mfma_f32_16x16x32_bf16 v[56:59], v[28:31], v[48:51], v[20:23]
	v_mfma_f32_16x16x32_bf16 v[20:23], v[32:35], v[44:47], v[140:143]
	v_mfma_f32_16x16x32_bf16 v[52:55], v[64:67], v[48:51], v[20:23]
	v_mfma_f32_16x16x32_bf16 v[20:23], v[8:11], v[186:189], v[144:147]
	v_mfma_f32_16x16x32_bf16 v[40:43], v[28:31], v[232:235], v[20:23]
	v_mfma_f32_16x16x32_bf16 v[20:23], v[32:35], v[186:189], v[148:151]
	v_mfma_f32_16x16x32_bf16 v[36:39], v[64:67], v[232:235], v[20:23]
	v_mfma_f32_16x16x32_bf16 v[20:23], v[8:11], v[236:239], v[152:155]
	v_mfma_f32_16x16x32_bf16 v[4:7], v[8:11], v[244:247], v[4:7]
	v_mfma_f32_16x16x32_bf16 v[24:27], v[28:31], v[240:243], v[20:23]
	v_mfma_f32_16x16x32_bf16 v[20:23], v[32:35], v[236:239], v[156:159]
	v_mfma_f32_16x16x32_bf16 v[8:11], v[28:31], v[248:251], v[4:7]
	v_mfma_f32_16x16x32_bf16 v[4:7], v[32:35], v[244:247], v[12:15]
	v_mfma_f32_16x16x32_bf16 v[20:23], v[64:67], v[240:243], v[20:23]
	v_mfma_f32_16x16x32_bf16 v[4:7], v[64:67], v[248:251], v[4:7]
	v_mfma_f32_16x16x32_bf16 v[12:15], v[216:219], v[44:47], v[16:19]
	v_mfma_f32_16x16x32_bf16 v[64:67], v[220:223], v[48:51], v[12:15]
	v_mfma_f32_16x16x32_bf16 v[12:15], v[224:227], v[44:47], v[160:163]
	v_mfma_f32_16x16x32_bf16 v[60:63], v[228:231], v[48:51], v[12:15]
	v_mfma_f32_16x16x32_bf16 v[12:15], v[216:219], v[186:189], v[174:177]
	v_mfma_f32_16x16x32_bf16 v[48:51], v[220:223], v[232:235], v[12:15]
	v_mfma_f32_16x16x32_bf16 v[12:15], v[224:227], v[186:189], v[178:181]
	v_mfma_f32_16x16x32_bf16 v[44:47], v[228:231], v[232:235], v[12:15]
	v_mfma_f32_16x16x32_bf16 v[12:15], v[216:219], v[236:239], v[182:185]
	v_mfma_f32_16x16x32_bf16 v[32:35], v[220:223], v[240:243], v[12:15]
	v_mfma_f32_16x16x32_bf16 v[12:15], v[224:227], v[236:239], v[190:193]
	v_mfma_f32_16x16x32_bf16 v[28:31], v[228:231], v[240:243], v[12:15]
	v_mfma_f32_16x16x32_bf16 v[12:15], v[216:219], v[244:247], v[202:205]
	v_mfma_f32_16x16x32_bf16 v[16:19], v[220:223], v[248:251], v[12:15]
	v_mfma_f32_16x16x32_bf16 v[12:15], v[224:227], v[244:247], v[206:209]
	v_mfma_f32_16x16x32_bf16 v[12:15], v[228:231], v[248:251], v[12:15]
	s_barrier
	s_add_u32 s10, s14, 0x84180
	s_addc_u32 s11, s15, 0
	s_add_u32 s12, s12, 0x200
	s_addc_u32 s13, s13, 0
	s_mov_b32 s14, 0
	s_mov_b64 s[54:55], 0x80000
	s_mov_b64 s[56:57], 0x80080
	s_mov_b64 s[60:61], 0xc0000
	s_mov_b64 s[62:63], 0xc0080
	s_mov_b64 s[64:65], 0xc6000
.LBB0_324:
	ds_read_b128 v[136:139], v132
	ds_read_b128 v[140:143], v132 offset:1024
	ds_read_b128 v[144:147], v132 offset:2048
	ds_read_b128 v[148:151], v132 offset:3072
	ds_read_b128 v[152:155], v133
	ds_read_b128 v[156:159], v133 offset:1024
	ds_read_b128 v[160:163], v133 offset:2048
	ds_read_b128 v[174:177], v133 offset:3072
	s_add_u32 s15, s10, 0xfff7c080
	s_addc_u32 s50, s11, -1
	s_cmp_eq_u32 s14, 28
	s_cselect_b32 s51, s25, s50
	s_cselect_b32 s50, s24, s15
	s_cselect_b32 s53, s3, s13
	s_cselect_b32 s52, s4, s12
	s_mov_b32 m0, s5
	v_lshl_add_u64 v[194:195], s[10:11], 0, v[172:173]
	ds_read_b128 v[178:181], v200
	ds_read_b128 v[182:185], v200 offset:1024
	ds_read_b128 v[186:189], v200 offset:2048
	ds_read_b128 v[190:193], v200 offset:3072
	ds_read_b128 v[202:205], v200 offset:4096
	ds_read_b128 v[206:209], v200 offset:5120
	ds_read_b128 v[216:219], v200 offset:6144
	ds_read_b128 v[220:223], v200 offset:7168
	global_load_lds_dwordx4 v[194:195], off
	v_lshl_add_u64 v[194:195], v[194:195], 0, s[96:97]
	s_mov_b32 m0, s23
	s_nop 0
	global_load_lds_dwordx4 v[194:195], off
	s_waitcnt vmcnt(8)
	s_waitcnt lgkmcnt(0)
	s_barrier
	v_mfma_f32_16x16x32_bf16 v[120:123], v[136:139], v[178:181], v[120:123]
	v_mfma_f32_16x16x32_bf16 v[120:123], v[140:143], v[182:185], v[120:123]
	v_mfma_f32_16x16x32_bf16 v[116:119], v[144:147], v[178:181], v[116:119]
	v_mfma_f32_16x16x32_bf16 v[116:119], v[148:151], v[182:185], v[116:119]
	v_mfma_f32_16x16x32_bf16 v[104:107], v[136:139], v[186:189], v[104:107]
	v_mfma_f32_16x16x32_bf16 v[104:107], v[140:143], v[190:193], v[104:107]
	v_mfma_f32_16x16x32_bf16 v[100:103], v[144:147], v[186:189], v[100:103]
	v_mfma_f32_16x16x32_bf16 v[100:103], v[148:151], v[190:193], v[100:103]
	v_mfma_f32_16x16x32_bf16 v[88:91], v[136:139], v[202:205], v[88:91]
	v_mfma_f32_16x16x32_bf16 v[88:91], v[140:143], v[206:209], v[88:91]
	v_mfma_f32_16x16x32_bf16 v[84:87], v[144:147], v[202:205], v[84:87]
	v_mfma_f32_16x16x32_bf16 v[84:87], v[148:151], v[206:209], v[84:87]
	v_mfma_f32_16x16x32_bf16 v[72:75], v[136:139], v[216:219], v[72:75]
	v_mfma_f32_16x16x32_bf16 v[72:75], v[140:143], v[220:223], v[72:75]
	v_mfma_f32_16x16x32_bf16 v[68:71], v[144:147], v[216:219], v[68:71]
	v_mfma_f32_16x16x32_bf16 v[68:71], v[148:151], v[220:223], v[68:71]
	v_mfma_f32_16x16x32_bf16 v[128:131], v[152:155], v[178:181], v[128:131]
	v_mfma_f32_16x16x32_bf16 v[128:131], v[156:159], v[182:185], v[128:131]
	v_mfma_f32_16x16x32_bf16 v[124:127], v[160:163], v[178:181], v[124:127]
	v_mfma_f32_16x16x32_bf16 v[124:127], v[174:177], v[182:185], v[124:127]
	v_mfma_f32_16x16x32_bf16 v[112:115], v[152:155], v[186:189], v[112:115]
	v_mfma_f32_16x16x32_bf16 v[112:115], v[156:159], v[190:193], v[112:115]
	v_mfma_f32_16x16x32_bf16 v[108:111], v[160:163], v[186:189], v[108:111]
	v_mfma_f32_16x16x32_bf16 v[108:111], v[174:177], v[190:193], v[108:111]
	v_mfma_f32_16x16x32_bf16 v[96:99], v[152:155], v[202:205], v[96:99]
	v_mfma_f32_16x16x32_bf16 v[96:99], v[156:159], v[206:209], v[96:99]
	v_mfma_f32_16x16x32_bf16 v[92:95], v[160:163], v[202:205], v[92:95]
	v_mfma_f32_16x16x32_bf16 v[92:95], v[174:177], v[206:209], v[92:95]
	v_mfma_f32_16x16x32_bf16 v[80:83], v[152:155], v[216:219], v[80:83]
	v_mfma_f32_16x16x32_bf16 v[80:83], v[156:159], v[220:223], v[80:83]
	v_mfma_f32_16x16x32_bf16 v[76:79], v[160:163], v[216:219], v[76:79]
	v_mfma_f32_16x16x32_bf16 v[76:79], v[174:177], v[220:223], v[76:79]
	s_barrier
	s_mov_b32 m0, s28
	v_lshl_add_u64 v[194:195], s[52:53], 0, v[164:165]
	ds_read_b128 v[178:181], v200 offset:16384
	ds_read_b128 v[182:185], v200 offset:17408
	ds_read_b128 v[186:189], v200 offset:18432
	ds_read_b128 v[190:193], v200 offset:19456
	ds_read_b128 v[202:205], v200 offset:20480
	ds_read_b128 v[206:209], v200 offset:21504
	ds_read_b128 v[216:219], v200 offset:22528
	ds_read_b128 v[220:223], v200 offset:23552
	global_load_lds_dwordx4 v[194:195], off
	v_lshl_add_u64 v[214:215], v[194:195], 0, s[90:91]
	s_mov_b32 m0, s29
	s_nop 0
	global_load_lds_dwordx4 v[214:215], off
	v_lshl_add_u64 v[214:215], v[194:195], 0, s[54:55]
	s_mov_b32 m0, s33
	s_nop 0
	global_load_lds_dwordx4 v[214:215], off
	v_lshl_add_u64 v[214:215], v[194:195], 0, s[60:61]
	s_mov_b32 m0, s45
	s_nop 0
	global_load_lds_dwordx4 v[214:215], off
	v_lshl_add_u64 v[214:215], s[50:51], 0, v[166:167]
	s_mov_b32 m0, s30
	v_lshl_add_u64 v[224:225], v[214:215], 0, s[96:97]
	global_load_lds_dwordx4 v[214:215], off
	s_mov_b32 m0, s31
	s_nop 0
	global_load_lds_dwordx4 v[224:225], off
	s_waitcnt vmcnt(8)
	s_waitcnt lgkmcnt(0)
	s_barrier
	v_mfma_f32_16x16x32_bf16 v[56:59], v[136:139], v[178:181], v[56:59]
	v_mfma_f32_16x16x32_bf16 v[56:59], v[140:143], v[182:185], v[56:59]
	v_mfma_f32_16x16x32_bf16 v[52:55], v[144:147], v[178:181], v[52:55]
	v_mfma_f32_16x16x32_bf16 v[52:55], v[148:151], v[182:185], v[52:55]
	v_mfma_f32_16x16x32_bf16 v[40:43], v[136:139], v[186:189], v[40:43]
	v_mfma_f32_16x16x32_bf16 v[40:43], v[140:143], v[190:193], v[40:43]
	v_mfma_f32_16x16x32_bf16 v[36:39], v[144:147], v[186:189], v[36:39]
	v_mfma_f32_16x16x32_bf16 v[36:39], v[148:151], v[190:193], v[36:39]
	v_mfma_f32_16x16x32_bf16 v[24:27], v[136:139], v[202:205], v[24:27]
	v_mfma_f32_16x16x32_bf16 v[24:27], v[140:143], v[206:209], v[24:27]
	v_mfma_f32_16x16x32_bf16 v[20:23], v[144:147], v[202:205], v[20:23]
	v_mfma_f32_16x16x32_bf16 v[20:23], v[148:151], v[206:209], v[20:23]
	v_mfma_f32_16x16x32_bf16 v[8:11], v[136:139], v[216:219], v[8:11]
	v_mfma_f32_16x16x32_bf16 v[8:11], v[140:143], v[220:223], v[8:11]
	v_mfma_f32_16x16x32_bf16 v[4:7], v[144:147], v[216:219], v[4:7]
	v_mfma_f32_16x16x32_bf16 v[4:7], v[148:151], v[220:223], v[4:7]
	v_mfma_f32_16x16x32_bf16 v[64:67], v[152:155], v[178:181], v[64:67]
	v_mfma_f32_16x16x32_bf16 v[64:67], v[156:159], v[182:185], v[64:67]
	v_mfma_f32_16x16x32_bf16 v[60:63], v[160:163], v[178:181], v[60:63]
	v_mfma_f32_16x16x32_bf16 v[60:63], v[174:177], v[182:185], v[60:63]
	v_mfma_f32_16x16x32_bf16 v[48:51], v[152:155], v[186:189], v[48:51]
	v_mfma_f32_16x16x32_bf16 v[48:51], v[156:159], v[190:193], v[48:51]
	v_mfma_f32_16x16x32_bf16 v[44:47], v[160:163], v[186:189], v[44:47]
	v_mfma_f32_16x16x32_bf16 v[44:47], v[174:177], v[190:193], v[44:47]
	v_mfma_f32_16x16x32_bf16 v[32:35], v[152:155], v[202:205], v[32:35]
	v_mfma_f32_16x16x32_bf16 v[32:35], v[156:159], v[206:209], v[32:35]
	v_mfma_f32_16x16x32_bf16 v[28:31], v[160:163], v[202:205], v[28:31]
	v_mfma_f32_16x16x32_bf16 v[28:31], v[174:177], v[206:209], v[28:31]
	v_mfma_f32_16x16x32_bf16 v[16:19], v[152:155], v[216:219], v[16:19]
	v_mfma_f32_16x16x32_bf16 v[16:19], v[156:159], v[220:223], v[16:19]
	v_mfma_f32_16x16x32_bf16 v[12:15], v[160:163], v[216:219], v[12:15]
	v_mfma_f32_16x16x32_bf16 v[12:15], v[174:177], v[220:223], v[12:15]
	s_barrier
; #define PG8_MMA(ai, bj, At, Bt) do { __builtin_amdgcn_s_setprio(1); _Pragma("unroll") for (int m = 0; m < 4; ++m) _Pragma("unroll") for (int n = 0; n < 2; ++n) _Pragma("unroll") for (int k = 0; k < 2; ++k) \
;         acc[ai][bj][m][n] = __builtin_amdgcn_mfma_f32_16x16x32_bf16(Bt[n][k], At[m][k], acc[ai][bj][m][n], 0, 0, 0); __builtin_amdgcn_s_setprio(0); } while (0)
; #define PG8_WAIT_V(n) asm volatile("s_waitcnt vmcnt(" #n ")" ::: "memory")
; #define PG8_TRIP_HEAD(T) const int t = (T); const bool last = (t == nt - 2); \
;             const char* a1 = cA + (size_t)(t + 1) * kstep; \
;             const char* a2 = last ? nA : cA + (size_t)(t + 2) * kstep; const char* b2 = last ? nB : cB + (size_t)(t + 2) * kstep; \
;             const char* a3 = a2 + kstep; const char* b3 = b2 + kstep; \
;             if (last && has_next) S.a_ready(nxt);
; template <class Epi, class Sched, bool ALIGN_EPI = false, bool SP2 = false>
; __device__ __forceinline__ void gemm_phase(PG8_LAS unsigned char* lds, const Gemm g, const Sched& S, const Epi& E) {
;     ...
;         if constexpr (SP2) {
;             { PG8_TRIP_HEAD(0) PG8_TRIP_SP2(asm volatile("s_waitcnt vmcnt(%0)" :: "n"(8 + Epi::NST) : "memory"), PG8_MMAZ) }
;             for (int tt = 2; tt < nt; tt += 2) { PG8_TRIP_HEAD(tt) PG8_TRIP_SP2(PG8_WAIT_V(8), PG8_MMA) }
	ds_read_b128 v[136:139], v134
	ds_read_b128 v[140:143], v134 offset:1024
	ds_read_b128 v[144:147], v134 offset:2048
	ds_read_b128 v[148:151], v134 offset:3072
	ds_read_b128 v[152:155], v135
	ds_read_b128 v[156:159], v135 offset:1024
	ds_read_b128 v[160:163], v135 offset:2048
	ds_read_b128 v[174:177], v135 offset:3072
	s_mov_b32 m0, s34
	v_lshl_add_u64 v[224:225], v[214:215], 0, s[82:83]
	ds_read_b128 v[178:181], v200 offset:32768
	ds_read_b128 v[182:185], v200 offset:33792
	ds_read_b128 v[186:189], v200 offset:34816
	ds_read_b128 v[190:193], v200 offset:35840
	ds_read_b128 v[202:205], v200 offset:36864
	ds_read_b128 v[206:209], v200 offset:37888
	ds_read_b128 v[216:219], v200 offset:38912
	ds_read_b128 v[220:223], v200 offset:39936
	global_load_lds_dwordx4 v[224:225], off
	v_lshl_add_u64 v[224:225], v[214:215], 0, s[64:65]
	s_mov_b32 m0, s35
	s_nop 0
	global_load_lds_dwordx4 v[224:225], off
	s_waitcnt vmcnt(8)
	s_waitcnt lgkmcnt(0)
	s_barrier
	v_mfma_f32_16x16x32_bf16 v[120:123], v[136:139], v[178:181], v[120:123]
	v_mfma_f32_16x16x32_bf16 v[120:123], v[140:143], v[182:185], v[120:123]
	v_mfma_f32_16x16x32_bf16 v[116:119], v[144:147], v[178:181], v[116:119]
	v_mfma_f32_16x16x32_bf16 v[116:119], v[148:151], v[182:185], v[116:119]
	v_mfma_f32_16x16x32_bf16 v[104:107], v[136:139], v[186:189], v[104:107]
	v_mfma_f32_16x16x32_bf16 v[104:107], v[140:143], v[190:193], v[104:107]
	v_mfma_f32_16x16x32_bf16 v[100:103], v[144:147], v[186:189], v[100:103]
	v_mfma_f32_16x16x32_bf16 v[100:103], v[148:151], v[190:193], v[100:103]
	v_mfma_f32_16x16x32_bf16 v[88:91], v[136:139], v[202:205], v[88:91]
	v_mfma_f32_16x16x32_bf16 v[88:91], v[140:143], v[206:209], v[88:91]
	v_mfma_f32_16x16x32_bf16 v[84:87], v[144:147], v[202:205], v[84:87]
	v_mfma_f32_16x16x32_bf16 v[84:87], v[148:151], v[206:209], v[84:87]
	v_mfma_f32_16x16x32_bf16 v[72:75], v[136:139], v[216:219], v[72:75]
	v_mfma_f32_16x16x32_bf16 v[72:75], v[140:143], v[220:223], v[72:75]
	v_mfma_f32_16x16x32_bf16 v[68:71], v[144:147], v[216:219], v[68:71]
	v_mfma_f32_16x16x32_bf16 v[68:71], v[148:151], v[220:223], v[68:71]
	v_mfma_f32_16x16x32_bf16 v[128:131], v[152:155], v[178:181], v[128:131]
	v_mfma_f32_16x16x32_bf16 v[128:131], v[156:159], v[182:185], v[128:131]
	v_mfma_f32_16x16x32_bf16 v[124:127], v[160:163], v[178:181], v[124:127]
	v_mfma_f32_16x16x32_bf16 v[124:127], v[174:177], v[182:185], v[124:127]
	v_mfma_f32_16x16x32_bf16 v[112:115], v[152:155], v[186:189], v[112:115]
	v_mfma_f32_16x16x32_bf16 v[112:115], v[156:159], v[190:193], v[112:115]
	v_mfma_f32_16x16x32_bf16 v[108:111], v[160:163], v[186:189], v[108:111]
	v_mfma_f32_16x16x32_bf16 v[108:111], v[174:177], v[190:193], v[108:111]
	v_mfma_f32_16x16x32_bf16 v[96:99], v[152:155], v[202:205], v[96:99]
	v_mfma_f32_16x16x32_bf16 v[96:99], v[156:159], v[206:209], v[96:99]
	v_mfma_f32_16x16x32_bf16 v[92:95], v[160:163], v[202:205], v[92:95]
	v_mfma_f32_16x16x32_bf16 v[92:95], v[174:177], v[206:209], v[92:95]
	v_mfma_f32_16x16x32_bf16 v[80:83], v[152:155], v[216:219], v[80:83]
	v_mfma_f32_16x16x32_bf16 v[80:83], v[156:159], v[220:223], v[80:83]
	v_mfma_f32_16x16x32_bf16 v[76:79], v[160:163], v[216:219], v[76:79]
	v_mfma_f32_16x16x32_bf16 v[76:79], v[174:177], v[220:223], v[76:79]
	s_barrier
	s_mov_b32 m0, s46
	v_lshl_add_u64 v[224:225], v[194:195], 0, s[78:79]
	ds_read_b128 v[178:181], v200 offset:49152
	ds_read_b128 v[182:185], v200 offset:50176
	ds_read_b128 v[186:189], v200 offset:51200
	ds_read_b128 v[190:193], v200 offset:52224
	ds_read_b128 v[202:205], v200 offset:53248
	ds_read_b128 v[206:209], v200 offset:54272
	ds_read_b128 v[216:219], v200 offset:55296
	ds_read_b128 v[220:223], v200 offset:56320
	global_load_lds_dwordx4 v[224:225], off
	v_lshl_add_u64 v[224:225], v[194:195], 0, s[84:85]
	s_mov_b32 m0, s47
	s_nop 0
	global_load_lds_dwordx4 v[224:225], off
	v_lshl_add_u64 v[224:225], v[194:195], 0, s[56:57]
	s_mov_b32 m0, s48
	v_lshl_add_u64 v[194:195], v[194:195], 0, s[62:63]
	global_load_lds_dwordx4 v[224:225], off
	s_mov_b32 m0, s49
	s_nop 0
	global_load_lds_dwordx4 v[194:195], off
	v_lshl_add_u64 v[194:195], v[214:215], 0, s[78:79]
	s_mov_b32 m0, s38
	s_nop 0
	global_load_lds_dwordx4 v[194:195], off
	v_lshl_add_u64 v[194:195], v[214:215], 0, s[92:93]
	s_mov_b32 m0, s39
	s_nop 0
	global_load_lds_dwordx4 v[194:195], off
	s_waitcnt vmcnt(8)
	s_waitcnt lgkmcnt(0)
	s_barrier
	v_mfma_f32_16x16x32_bf16 v[56:59], v[136:139], v[178:181], v[56:59]
	v_mfma_f32_16x16x32_bf16 v[56:59], v[140:143], v[182:185], v[56:59]
	v_mfma_f32_16x16x32_bf16 v[52:55], v[144:147], v[178:181], v[52:55]
	v_mfma_f32_16x16x32_bf16 v[52:55], v[148:151], v[182:185], v[52:55]
	v_mfma_f32_16x16x32_bf16 v[40:43], v[136:139], v[186:189], v[40:43]
	v_mfma_f32_16x16x32_bf16 v[40:43], v[140:143], v[190:193], v[40:43]
	v_mfma_f32_16x16x32_bf16 v[36:39], v[144:147], v[186:189], v[36:39]
	v_mfma_f32_16x16x32_bf16 v[36:39], v[148:151], v[190:193], v[36:39]
	v_mfma_f32_16x16x32_bf16 v[24:27], v[136:139], v[202:205], v[24:27]
	v_mfma_f32_16x16x32_bf16 v[24:27], v[140:143], v[206:209], v[24:27]
	v_mfma_f32_16x16x32_bf16 v[20:23], v[144:147], v[202:205], v[20:23]
	v_mfma_f32_16x16x32_bf16 v[20:23], v[148:151], v[206:209], v[20:23]
	v_mfma_f32_16x16x32_bf16 v[8:11], v[136:139], v[216:219], v[8:11]
	v_mfma_f32_16x16x32_bf16 v[8:11], v[140:143], v[220:223], v[8:11]
	v_mfma_f32_16x16x32_bf16 v[4:7], v[144:147], v[216:219], v[4:7]
	v_mfma_f32_16x16x32_bf16 v[4:7], v[148:151], v[220:223], v[4:7]
	v_mfma_f32_16x16x32_bf16 v[64:67], v[152:155], v[178:181], v[64:67]
	v_mfma_f32_16x16x32_bf16 v[64:67], v[156:159], v[182:185], v[64:67]
	v_mfma_f32_16x16x32_bf16 v[60:63], v[160:163], v[178:181], v[60:63]
	v_mfma_f32_16x16x32_bf16 v[60:63], v[174:177], v[182:185], v[60:63]
	v_mfma_f32_16x16x32_bf16 v[48:51], v[152:155], v[186:189], v[48:51]
	v_mfma_f32_16x16x32_bf16 v[48:51], v[156:159], v[190:193], v[48:51]
	v_mfma_f32_16x16x32_bf16 v[44:47], v[160:163], v[186:189], v[44:47]
	v_mfma_f32_16x16x32_bf16 v[44:47], v[174:177], v[190:193], v[44:47]
	v_mfma_f32_16x16x32_bf16 v[32:35], v[152:155], v[202:205], v[32:35]
	v_mfma_f32_16x16x32_bf16 v[32:35], v[156:159], v[206:209], v[32:35]
	v_mfma_f32_16x16x32_bf16 v[28:31], v[160:163], v[202:205], v[28:31]
	v_mfma_f32_16x16x32_bf16 v[28:31], v[174:177], v[206:209], v[28:31]
	v_mfma_f32_16x16x32_bf16 v[16:19], v[152:155], v[216:219], v[16:19]
	v_mfma_f32_16x16x32_bf16 v[16:19], v[156:159], v[220:223], v[16:19]
	v_mfma_f32_16x16x32_bf16 v[12:15], v[160:163], v[216:219], v[12:15]
	v_mfma_f32_16x16x32_bf16 v[12:15], v[174:177], v[220:223], v[12:15]
	s_barrier
	s_add_i32 s14, s14, 2
	s_add_u32 s10, s10, 0x100
	s_addc_u32 s11, s11, 0
	s_add_u32 s12, s12, 0x100
	s_addc_u32 s13, s13, 0
	s_cmp_gt_u32 s14, 29
	s_cbranch_scc0 .LBB0_324
	s_and_b64 vcc, exec, s[18:19]
	s_cbranch_vccz .LBB0_327
	s_barrier

.LBB0_593:
	v_readlane_b32 s18, v253, 7
	v_readlane_b32 s34, v254, 59
	s_cmp_eq_u32 s29, 0
	v_readlane_b32 s19, v253, 8
	v_readlane_b32 s35, v254, 60
	s_cselect_b32 s33, s35, s19
	s_cselect_b32 s34, s34, s18
	s_ashr_i32 s15, s14, 31
	s_lshl_b64 s[18:19], s[14:15], 20
	s_add_u32 s18, s34, s18
	s_addc_u32 s19, s33, s19
	s_and_b64 s[4:5], s[4:5], exec
	s_cselect_b32 s4, s19, s9
	s_cselect_b32 s5, s18, s8
	s_add_i32 s35, 0, 0x10000
	s_add_i32 s37, 0, 0x14000
	v_add_u32_e32 v116, s35, v219
	v_add_u32_e32 v117, s37, v219
	ds_read_b128 v[4:7], v116
	ds_read_b128 v[8:11], v116 offset:1024
	ds_read_b128 v[12:15], v116 offset:2048
	ds_read_b128 v[16:19], v116 offset:3072
	ds_read_b128 v[20:23], v117
	ds_read_b128 v[24:27], v117 offset:1024
	ds_read_b128 v[28:31], v117 offset:2048
	ds_read_b128 v[32:35], v117 offset:3072
	s_mov_b32 s15, 0
	v_lshl_add_u64 v[192:193], s[20:21], 0, v[196:197]
	s_mov_b64 s[38:39], 0x84080
	s_add_i32 s33, s23, 0xc000
	v_lshl_add_u64 v[68:69], v[192:193], 0, s[38:39]
	s_mov_b32 m0, s33
	s_mov_b64 s[38:39], 0xc6080
	s_add_i32 s34, s23, 0xe000
	ds_read_b128 v[36:39], v221
	ds_read_b128 v[40:43], v221 offset:1024
	ds_read_b128 v[44:47], v221 offset:2048
	ds_read_b128 v[48:51], v221 offset:3072
	ds_read_b128 v[52:55], v221 offset:4096
	ds_read_b128 v[56:59], v221 offset:5120
	ds_read_b128 v[60:63], v221 offset:6144
	ds_read_b128 v[64:67], v221 offset:7168
	global_load_lds_dwordx4 v[68:69], off
	v_lshl_add_u64 v[68:69], v[192:193], 0, s[38:39]
	s_mov_b32 m0, s34
	s_nop 0
	global_load_lds_dwordx4 v[68:69], off
	s_waitcnt vmcnt(8)
	s_waitcnt lgkmcnt(0)
	s_barrier
	v_mfma_f32_16x16x32_bf16 v[92:95], v[4:7], v[60:63], 0
	v_mfma_f32_16x16x32_bf16 v[68:71], v[4:7], v[36:39], 0
	v_mfma_f32_16x16x32_bf16 v[72:75], v[12:15], v[36:39], 0
	v_mfma_f32_16x16x32_bf16 v[76:79], v[4:7], v[44:47], 0
	v_mfma_f32_16x16x32_bf16 v[80:83], v[12:15], v[44:47], 0
	v_mfma_f32_16x16x32_bf16 v[84:87], v[4:7], v[52:55], 0
	v_mfma_f32_16x16x32_bf16 v[88:91], v[12:15], v[52:55], 0
	v_mfma_f32_16x16x32_bf16 v[100:103], v[8:11], v[64:67], v[92:95]
	v_mfma_f32_16x16x32_bf16 v[92:95], v[12:15], v[60:63], 0
	v_mfma_f32_16x16x32_bf16 v[68:71], v[8:11], v[40:43], v[68:71]
	v_mfma_f32_16x16x32_bf16 v[72:75], v[16:19], v[40:43], v[72:75]
	v_mfma_f32_16x16x32_bf16 v[76:79], v[8:11], v[48:51], v[76:79]
	v_mfma_f32_16x16x32_bf16 v[80:83], v[16:19], v[48:51], v[80:83]
	v_mfma_f32_16x16x32_bf16 v[84:87], v[8:11], v[56:59], v[84:87]
	v_mfma_f32_16x16x32_bf16 v[88:91], v[16:19], v[56:59], v[88:91]
	v_mfma_f32_16x16x32_bf16 v[104:107], v[16:19], v[64:67], v[92:95]
	v_mfma_f32_16x16x32_bf16 v[92:95], v[20:23], v[36:39], 0
	v_mfma_f32_16x16x32_bf16 v[36:39], v[28:31], v[36:39], 0
	v_mfma_f32_16x16x32_bf16 v[118:121], v[24:27], v[40:43], v[92:95]
	v_mfma_f32_16x16x32_bf16 v[36:39], v[32:35], v[40:43], v[36:39]
	v_mfma_f32_16x16x32_bf16 v[40:43], v[20:23], v[44:47], 0
	v_mfma_f32_16x16x32_bf16 v[44:47], v[28:31], v[44:47], 0
	v_mfma_f32_16x16x32_bf16 v[40:43], v[24:27], v[48:51], v[40:43]
	v_mfma_f32_16x16x32_bf16 v[44:47], v[32:35], v[48:51], v[44:47]
	v_mfma_f32_16x16x32_bf16 v[48:51], v[20:23], v[52:55], 0
	v_mfma_f32_16x16x32_bf16 v[52:55], v[28:31], v[52:55], 0
	v_mfma_f32_16x16x32_bf16 v[48:51], v[24:27], v[56:59], v[48:51]
	v_mfma_f32_16x16x32_bf16 v[52:55], v[32:35], v[56:59], v[52:55]
	v_mfma_f32_16x16x32_bf16 v[56:59], v[20:23], v[60:63], 0
	v_mfma_f32_16x16x32_bf16 v[60:63], v[28:31], v[60:63], 0
	v_mfma_f32_16x16x32_bf16 v[56:59], v[24:27], v[64:67], v[56:59]
	v_mfma_f32_16x16x32_bf16 v[60:63], v[32:35], v[64:67], v[60:63]
	s_barrier
	v_lshl_add_u64 v[250:251], s[8:9], 0, v[194:195]
	s_mov_b64 s[40:41], 0x100
	s_add_i32 s35, s35, s22
	v_lshl_add_u64 v[134:135], v[250:251], 0, s[40:41]
	s_mov_b32 m0, s35
	s_mov_b64 s[38:39], 0x40100
	s_add_i32 s36, s35, 0x2000
	ds_read_b128 v[64:67], v221 offset:16384
	ds_read_b128 v[92:95], v221 offset:17408
	ds_read_b128 v[96:99], v221 offset:18432
	ds_read_b128 v[108:111], v221 offset:19456
	ds_read_b128 v[112:115], v221 offset:20480
	ds_read_b128 v[122:125], v221 offset:21504
	ds_read_b128 v[126:129], v221 offset:22528
	ds_read_b128 v[130:133], v221 offset:23552
	global_load_lds_dwordx4 v[134:135], off
	v_lshl_add_u64 v[134:135], v[250:251], 0, s[38:39]
	s_mov_b32 m0, s36
	s_mov_b64 s[38:39], 0x80100
	s_add_i32 s37, s37, s22
	global_load_lds_dwordx4 v[134:135], off
	v_lshl_add_u64 v[134:135], v[250:251], 0, s[38:39]
	s_mov_b32 m0, s37
	s_mov_b64 s[38:39], 0xc0100
	global_load_lds_dwordx4 v[134:135], off
	v_lshl_add_u64 v[134:135], v[250:251], 0, s[38:39]
	s_add_i32 s38, s37, 0x2000
	s_mov_b32 m0, s38
	s_nop 0
	global_load_lds_dwordx4 v[134:135], off
	v_lshl_add_u64 v[134:135], v[192:193], 0, s[40:41]
	s_mov_b32 m0, s23
	s_mov_b64 s[40:41], 0x42100
	global_load_lds_dwordx4 v[134:135], off
	v_lshl_add_u64 v[134:135], v[192:193], 0, s[40:41]
	s_mov_b32 m0, s24
	s_nop 0
	global_load_lds_dwordx4 v[134:135], off
	s_waitcnt vmcnt(8)
	s_waitcnt lgkmcnt(0)
	s_barrier
	v_mfma_f32_16x16x32_bf16 v[134:137], v[4:7], v[64:67], 0
	v_mfma_f32_16x16x32_bf16 v[144:147], v[4:7], v[96:99], 0
	v_mfma_f32_16x16x32_bf16 v[152:155], v[4:7], v[112:115], 0
	v_mfma_f32_16x16x32_bf16 v[4:7], v[4:7], v[126:129], 0
	v_mfma_f32_16x16x32_bf16 v[136:139], v[8:11], v[92:95], v[134:137]
	v_mfma_f32_16x16x32_bf16 v[144:147], v[8:11], v[108:111], v[144:147]
	v_mfma_f32_16x16x32_bf16 v[152:155], v[8:11], v[122:125], v[152:155]
	v_mfma_f32_16x16x32_bf16 v[4:7], v[8:11], v[130:133], v[4:7]
	v_mfma_f32_16x16x32_bf16 v[8:11], v[12:15], v[126:129], 0
	v_mfma_f32_16x16x32_bf16 v[140:143], v[12:15], v[64:67], 0
	v_mfma_f32_16x16x32_bf16 v[148:151], v[12:15], v[96:99], 0
	v_mfma_f32_16x16x32_bf16 v[156:159], v[12:15], v[112:115], 0
	v_mfma_f32_16x16x32_bf16 v[8:11], v[16:19], v[130:133], v[8:11]
	v_mfma_f32_16x16x32_bf16 v[140:143], v[16:19], v[92:95], v[140:143]
	v_mfma_f32_16x16x32_bf16 v[148:151], v[16:19], v[108:111], v[148:151]
	v_mfma_f32_16x16x32_bf16 v[156:159], v[16:19], v[122:125], v[156:159]
	v_mfma_f32_16x16x32_bf16 v[12:15], v[20:23], v[64:67], 0
	v_mfma_f32_16x16x32_bf16 v[160:163], v[24:27], v[92:95], v[12:15]
	v_mfma_f32_16x16x32_bf16 v[12:15], v[28:31], v[64:67], 0
	v_mfma_f32_16x16x32_bf16 v[164:167], v[32:35], v[92:95], v[12:15]
	v_mfma_f32_16x16x32_bf16 v[12:15], v[20:23], v[96:99], 0
	v_mfma_f32_16x16x32_bf16 v[168:171], v[24:27], v[108:111], v[12:15]
	v_mfma_f32_16x16x32_bf16 v[12:15], v[28:31], v[96:99], 0
	v_mfma_f32_16x16x32_bf16 v[172:175], v[32:35], v[108:111], v[12:15]
	v_mfma_f32_16x16x32_bf16 v[12:15], v[20:23], v[112:115], 0
	v_mfma_f32_16x16x32_bf16 v[176:179], v[24:27], v[122:125], v[12:15]
	v_mfma_f32_16x16x32_bf16 v[12:15], v[28:31], v[112:115], 0
	v_mfma_f32_16x16x32_bf16 v[180:183], v[32:35], v[122:125], v[12:15]
	v_mfma_f32_16x16x32_bf16 v[12:15], v[20:23], v[126:129], 0
	v_mfma_f32_16x16x32_bf16 v[184:187], v[24:27], v[130:133], v[12:15]
	v_mfma_f32_16x16x32_bf16 v[12:15], v[28:31], v[126:129], 0
	v_mfma_f32_16x16x32_bf16 v[188:191], v[32:35], v[130:133], v[12:15]
	s_barrier
	s_add_i32 s39, 0, 0x18000
	s_add_i32 s41, 0, 0x1c000
	v_add_u32_e32 v134, s39, v219
	v_add_u32_e32 v135, s41, v219
	s_nop 0
	ds_read_b128 v[12:15], v134
	ds_read_b128 v[16:19], v134 offset:1024
	ds_read_b128 v[20:23], v134 offset:2048
	ds_read_b128 v[24:27], v134 offset:3072
	ds_read_b128 v[202:205], v135
	ds_read_b128 v[206:209], v135 offset:1024
	ds_read_b128 v[222:225], v135 offset:2048
	ds_read_b128 v[226:229], v135 offset:3072
	s_mov_b64 s[42:43], 0x84100
	s_mov_b32 m0, s25
	v_lshl_add_u64 v[92:93], v[192:193], 0, s[42:43]
	s_mov_b64 s[42:43], 0xc6100
	ds_read_b128 v[28:31], v221 offset:32768
	ds_read_b128 v[32:35], v221 offset:33792
	ds_read_b128 v[64:67], v221 offset:34816
	ds_read_b128 v[230:233], v221 offset:35840
	ds_read_b128 v[234:237], v221 offset:36864
	ds_read_b128 v[238:241], v221 offset:37888
	ds_read_b128 v[242:245], v221 offset:38912
	ds_read_b128 v[246:249], v221 offset:39936
	global_load_lds_dwordx4 v[92:93], off
	v_lshl_add_u64 v[92:93], v[192:193], 0, s[42:43]
	s_mov_b32 m0, s26
	s_nop 0
	global_load_lds_dwordx4 v[92:93], off
	s_waitcnt vmcnt(8)
	s_waitcnt lgkmcnt(0)
	s_barrier
	v_mfma_f32_16x16x32_bf16 v[68:71], v[12:15], v[28:31], v[68:71]
	v_mfma_f32_16x16x32_bf16 v[130:133], v[16:19], v[32:35], v[68:71]
	v_mfma_f32_16x16x32_bf16 v[68:71], v[20:23], v[28:31], v[72:75]
	v_mfma_f32_16x16x32_bf16 v[126:129], v[24:27], v[32:35], v[68:71]
	v_mfma_f32_16x16x32_bf16 v[68:71], v[12:15], v[64:67], v[76:79]
	v_mfma_f32_16x16x32_bf16 v[112:115], v[16:19], v[230:233], v[68:71]
	v_mfma_f32_16x16x32_bf16 v[68:71], v[20:23], v[64:67], v[80:83]
	v_mfma_f32_16x16x32_bf16 v[108:111], v[24:27], v[230:233], v[68:71]
	v_mfma_f32_16x16x32_bf16 v[68:71], v[12:15], v[234:237], v[84:87]
	v_mfma_f32_16x16x32_bf16 v[96:99], v[16:19], v[238:241], v[68:71]
	v_mfma_f32_16x16x32_bf16 v[68:71], v[20:23], v[234:237], v[88:91]
	v_mfma_f32_16x16x32_bf16 v[92:95], v[24:27], v[238:241], v[68:71]
	v_mfma_f32_16x16x32_bf16 v[68:71], v[12:15], v[242:245], v[100:103]
	v_mfma_f32_16x16x32_bf16 v[80:83], v[16:19], v[246:249], v[68:71]
	v_mfma_f32_16x16x32_bf16 v[68:71], v[20:23], v[242:245], v[104:107]
	v_mfma_f32_16x16x32_bf16 v[76:79], v[24:27], v[246:249], v[68:71]
	v_mfma_f32_16x16x32_bf16 v[68:71], v[202:205], v[28:31], v[118:121]
	v_mfma_f32_16x16x32_bf16 v[28:31], v[222:225], v[28:31], v[36:39]
	v_mfma_f32_16x16x32_bf16 v[118:121], v[226:229], v[32:35], v[28:31]
	v_mfma_f32_16x16x32_bf16 v[28:31], v[202:205], v[64:67], v[40:43]
	v_mfma_f32_16x16x32_bf16 v[104:107], v[206:209], v[230:233], v[28:31]
	v_mfma_f32_16x16x32_bf16 v[28:31], v[222:225], v[64:67], v[44:47]
	v_mfma_f32_16x16x32_bf16 v[100:103], v[226:229], v[230:233], v[28:31]
	v_mfma_f32_16x16x32_bf16 v[28:31], v[202:205], v[234:237], v[48:51]
	v_mfma_f32_16x16x32_bf16 v[88:91], v[206:209], v[238:241], v[28:31]
	v_mfma_f32_16x16x32_bf16 v[28:31], v[222:225], v[234:237], v[52:55]
	v_mfma_f32_16x16x32_bf16 v[84:87], v[226:229], v[238:241], v[28:31]
	v_mfma_f32_16x16x32_bf16 v[28:31], v[202:205], v[242:245], v[56:59]
	v_mfma_f32_16x16x32_bf16 v[72:75], v[206:209], v[246:249], v[28:31]
	v_mfma_f32_16x16x32_bf16 v[28:31], v[222:225], v[242:245], v[60:63]
	v_mfma_f32_16x16x32_bf16 v[122:125], v[206:209], v[32:35], v[68:71]
	v_mfma_f32_16x16x32_bf16 v[68:71], v[226:229], v[246:249], v[28:31]
	s_barrier
; #define PG8_MMA(ai, bj, At, Bt) do { __builtin_amdgcn_s_setprio(1); _Pragma("unroll") for (int m = 0; m < 4; ++m) _Pragma("unroll") for (int n = 0; n < 2; ++n) _Pragma("unroll") for (int k = 0; k < 2; ++k) \
;         acc[ai][bj][m][n] = __builtin_amdgcn_mfma_f32_16x16x32_bf16(Bt[n][k], At[m][k], acc[ai][bj][m][n], 0, 0, 0); __builtin_amdgcn_s_setprio(0); } while (0)
; #define PG8_WAIT_V(n) asm volatile("s_waitcnt vmcnt(" #n ")" ::: "memory")
; #define PG8_TRIP_HEAD(T) const int t = (T); const bool last = (t == nt - 2); \
;             const char* a1 = cA + (size_t)(t + 1) * kstep; \
;             const char* a2 = last ? nA : cA + (size_t)(t + 2) * kstep; const char* b2 = last ? nB : cB + (size_t)(t + 2) * kstep; \
;             const char* a3 = a2 + kstep; const char* b3 = b2 + kstep; \
;             if (last && has_next) S.a_ready(nxt);
; template <class Epi, class Sched, bool ALIGN_EPI = false, bool SP2 = false>
; __device__ __forceinline__ void gemm_phase(PG8_LAS unsigned char* lds, const Gemm g, const Sched& S, const Epi& E) {
;     ...
;         if constexpr (SP2) {
;             { PG8_TRIP_HEAD(0) PG8_TRIP_SP2(asm volatile("s_waitcnt vmcnt(%0)" :: "n"(8 + Epi::NST) : "memory"), PG8_MMAZ) }
;             for (int tt = 2; tt < nt; tt += 2) { PG8_TRIP_HEAD(tt) PG8_TRIP_SP2(PG8_WAIT_V(8), PG8_MMA) }
	s_mov_b64 s[44:45], 0x180
	s_add_i32 s39, s39, s22
	s_nop 1
	v_lshl_add_u64 v[28:29], v[250:251], 0, s[44:45]
	s_mov_b32 m0, s39
	s_mov_b64 s[42:43], 0x40180
	s_add_i32 s40, s39, 0x2000
	ds_read_b128 v[36:39], v221 offset:49152
	ds_read_b128 v[40:43], v221 offset:50176
	ds_read_b128 v[230:233], v221 offset:51200
	ds_read_b128 v[234:237], v221 offset:52224
	ds_read_b128 v[238:241], v221 offset:53248
	ds_read_b128 v[242:245], v221 offset:54272
	ds_read_b128 v[246:249], v221 offset:55296
	ds_read_b128 v[214:217], v221 offset:56320
	global_load_lds_dwordx4 v[28:29], off
	v_lshl_add_u64 v[28:29], v[250:251], 0, s[42:43]
	s_mov_b32 m0, s40
	s_mov_b64 s[42:43], 0x80180
	s_add_i32 s41, s41, s22
	global_load_lds_dwordx4 v[28:29], off
	v_lshl_add_u64 v[28:29], v[250:251], 0, s[42:43]
	s_mov_b32 m0, s41
	s_mov_b64 s[42:43], 0xc0180
	global_load_lds_dwordx4 v[28:29], off
	v_lshl_add_u64 v[28:29], v[250:251], 0, s[42:43]
	s_add_i32 s42, s41, 0x2000
	s_mov_b32 m0, s42
	s_nop 0
	global_load_lds_dwordx4 v[28:29], off
	v_lshl_add_u64 v[28:29], v[192:193], 0, s[44:45]
	s_mov_b32 m0, s27
	s_mov_b64 s[44:45], 0x42180
	global_load_lds_dwordx4 v[28:29], off
	v_lshl_add_u64 v[28:29], v[192:193], 0, s[44:45]
	s_mov_b32 m0, s28
	s_nop 0
	global_load_lds_dwordx4 v[28:29], off
	s_waitcnt vmcnt(8)
	s_waitcnt lgkmcnt(0)
	s_barrier
	v_mfma_f32_16x16x32_bf16 v[28:31], v[12:15], v[36:39], v[136:139]
	v_mfma_f32_16x16x32_bf16 v[64:67], v[16:19], v[40:43], v[28:31]
	v_mfma_f32_16x16x32_bf16 v[28:31], v[20:23], v[36:39], v[140:143]
	v_mfma_f32_16x16x32_bf16 v[60:63], v[24:27], v[40:43], v[28:31]
	v_mfma_f32_16x16x32_bf16 v[28:31], v[12:15], v[230:233], v[144:147]
	v_mfma_f32_16x16x32_bf16 v[48:51], v[16:19], v[234:237], v[28:31]
	v_mfma_f32_16x16x32_bf16 v[28:31], v[20:23], v[230:233], v[148:151]
	v_mfma_f32_16x16x32_bf16 v[44:47], v[24:27], v[234:237], v[28:31]
	v_mfma_f32_16x16x32_bf16 v[28:31], v[12:15], v[238:241], v[152:155]
	v_mfma_f32_16x16x32_bf16 v[4:7], v[12:15], v[246:249], v[4:7]
	v_mfma_f32_16x16x32_bf16 v[32:35], v[16:19], v[242:245], v[28:31]
	v_mfma_f32_16x16x32_bf16 v[28:31], v[20:23], v[238:241], v[156:159]
	v_mfma_f32_16x16x32_bf16 v[16:19], v[16:19], v[214:217], v[4:7]
	v_mfma_f32_16x16x32_bf16 v[4:7], v[20:23], v[246:249], v[8:11]
	v_mfma_f32_16x16x32_bf16 v[28:31], v[24:27], v[242:245], v[28:31]
	v_mfma_f32_16x16x32_bf16 v[12:15], v[24:27], v[214:217], v[4:7]
	v_mfma_f32_16x16x32_bf16 v[4:7], v[202:205], v[36:39], v[160:163]
	v_mfma_f32_16x16x32_bf16 v[56:59], v[206:209], v[40:43], v[4:7]
	v_mfma_f32_16x16x32_bf16 v[4:7], v[222:225], v[36:39], v[164:167]
	v_mfma_f32_16x16x32_bf16 v[52:55], v[226:229], v[40:43], v[4:7]
	v_mfma_f32_16x16x32_bf16 v[4:7], v[202:205], v[230:233], v[168:171]
	v_mfma_f32_16x16x32_bf16 v[40:43], v[206:209], v[234:237], v[4:7]
	v_mfma_f32_16x16x32_bf16 v[4:7], v[222:225], v[230:233], v[172:175]
	v_mfma_f32_16x16x32_bf16 v[36:39], v[226:229], v[234:237], v[4:7]
	v_mfma_f32_16x16x32_bf16 v[4:7], v[202:205], v[238:241], v[176:179]
	v_mfma_f32_16x16x32_bf16 v[24:27], v[206:209], v[242:245], v[4:7]
	v_mfma_f32_16x16x32_bf16 v[4:7], v[222:225], v[238:241], v[180:183]
	v_mfma_f32_16x16x32_bf16 v[20:23], v[226:229], v[242:245], v[4:7]
	v_mfma_f32_16x16x32_bf16 v[4:7], v[202:205], v[246:249], v[184:187]
	v_mfma_f32_16x16x32_bf16 v[8:11], v[206:209], v[214:217], v[4:7]
	v_mfma_f32_16x16x32_bf16 v[4:7], v[222:225], v[246:249], v[188:191]
	v_mfma_f32_16x16x32_bf16 v[4:7], v[226:229], v[214:217], v[4:7]
	s_barrier
	s_add_u32 s20, s20, 0x84180
	s_addc_u32 s21, s21, 0
	s_add_u32 s8, s8, 0x200
	s_addc_u32 s9, s9, 0
	s_mov_b64 s[48:49], 0x80000
	s_mov_b64 s[50:51], 0x80080
	s_mov_b64 s[52:53], 0xc0000
	s_mov_b64 s[54:55], 0xc0080
	s_mov_b64 s[56:57], 0xc6000
.LBB0_594:
	ds_read_b128 v[136:139], v116
	ds_read_b128 v[140:143], v116 offset:1024
	ds_read_b128 v[144:147], v116 offset:2048
	ds_read_b128 v[148:151], v116 offset:3072
	ds_read_b128 v[152:155], v117
	ds_read_b128 v[156:159], v117 offset:1024
	ds_read_b128 v[160:163], v117 offset:2048
	ds_read_b128 v[164:167], v117 offset:3072
	s_add_u32 s43, s20, 0xfff7c080
	s_addc_u32 s44, s21, -1
	s_cmp_eq_u32 s15, 28
	s_cselect_b32 s45, s17, s44
	s_cselect_b32 s44, s16, s43
	s_cselect_b32 s47, s4, s9
	s_cselect_b32 s46, s5, s8
	s_mov_b32 m0, s33
	v_lshl_add_u64 v[192:193], s[20:21], 0, v[200:201]
	ds_read_b128 v[168:171], v221
	ds_read_b128 v[172:175], v221 offset:1024
	ds_read_b128 v[176:179], v221 offset:2048
	ds_read_b128 v[180:183], v221 offset:3072
	ds_read_b128 v[184:187], v221 offset:4096
	ds_read_b128 v[188:191], v221 offset:5120
	ds_read_b128 v[202:205], v221 offset:6144
	ds_read_b128 v[206:209], v221 offset:7168
	global_load_lds_dwordx4 v[192:193], off
	v_lshl_add_u64 v[192:193], v[192:193], 0, s[96:97]
	s_mov_b32 m0, s34
	s_nop 0
	global_load_lds_dwordx4 v[192:193], off
	s_waitcnt vmcnt(8)
	s_waitcnt lgkmcnt(0)
	s_barrier
	v_mfma_f32_16x16x32_bf16 v[130:133], v[136:139], v[168:171], v[130:133]
	v_mfma_f32_16x16x32_bf16 v[130:133], v[140:143], v[172:175], v[130:133]
	v_mfma_f32_16x16x32_bf16 v[126:129], v[144:147], v[168:171], v[126:129]
	v_mfma_f32_16x16x32_bf16 v[126:129], v[148:151], v[172:175], v[126:129]
	v_mfma_f32_16x16x32_bf16 v[112:115], v[136:139], v[176:179], v[112:115]
	v_mfma_f32_16x16x32_bf16 v[112:115], v[140:143], v[180:183], v[112:115]
	v_mfma_f32_16x16x32_bf16 v[108:111], v[144:147], v[176:179], v[108:111]
	v_mfma_f32_16x16x32_bf16 v[108:111], v[148:151], v[180:183], v[108:111]
	v_mfma_f32_16x16x32_bf16 v[96:99], v[136:139], v[184:187], v[96:99]
	v_mfma_f32_16x16x32_bf16 v[96:99], v[140:143], v[188:191], v[96:99]
	v_mfma_f32_16x16x32_bf16 v[92:95], v[144:147], v[184:187], v[92:95]
	v_mfma_f32_16x16x32_bf16 v[92:95], v[148:151], v[188:191], v[92:95]
	v_mfma_f32_16x16x32_bf16 v[80:83], v[136:139], v[202:205], v[80:83]
	v_mfma_f32_16x16x32_bf16 v[80:83], v[140:143], v[206:209], v[80:83]
	v_mfma_f32_16x16x32_bf16 v[76:79], v[144:147], v[202:205], v[76:79]
	v_mfma_f32_16x16x32_bf16 v[76:79], v[148:151], v[206:209], v[76:79]
	v_mfma_f32_16x16x32_bf16 v[122:125], v[152:155], v[168:171], v[122:125]
	v_mfma_f32_16x16x32_bf16 v[122:125], v[156:159], v[172:175], v[122:125]
	v_mfma_f32_16x16x32_bf16 v[118:121], v[160:163], v[168:171], v[118:121]
	v_mfma_f32_16x16x32_bf16 v[118:121], v[164:167], v[172:175], v[118:121]
	v_mfma_f32_16x16x32_bf16 v[104:107], v[152:155], v[176:179], v[104:107]
	v_mfma_f32_16x16x32_bf16 v[104:107], v[156:159], v[180:183], v[104:107]
	v_mfma_f32_16x16x32_bf16 v[100:103], v[160:163], v[176:179], v[100:103]
	v_mfma_f32_16x16x32_bf16 v[100:103], v[164:167], v[180:183], v[100:103]
	v_mfma_f32_16x16x32_bf16 v[88:91], v[152:155], v[184:187], v[88:91]
	v_mfma_f32_16x16x32_bf16 v[88:91], v[156:159], v[188:191], v[88:91]
	v_mfma_f32_16x16x32_bf16 v[84:87], v[160:163], v[184:187], v[84:87]
	v_mfma_f32_16x16x32_bf16 v[84:87], v[164:167], v[188:191], v[84:87]
	v_mfma_f32_16x16x32_bf16 v[72:75], v[152:155], v[202:205], v[72:75]
	v_mfma_f32_16x16x32_bf16 v[72:75], v[156:159], v[206:209], v[72:75]
	v_mfma_f32_16x16x32_bf16 v[68:71], v[160:163], v[202:205], v[68:71]
	v_mfma_f32_16x16x32_bf16 v[68:71], v[164:167], v[206:209], v[68:71]
	s_barrier
	s_mov_b32 m0, s35
	v_lshl_add_u64 v[192:193], s[46:47], 0, v[194:195]
	ds_read_b128 v[168:171], v221 offset:16384
	ds_read_b128 v[172:175], v221 offset:17408
	ds_read_b128 v[176:179], v221 offset:18432
	ds_read_b128 v[180:183], v221 offset:19456
	ds_read_b128 v[184:187], v221 offset:20480
	ds_read_b128 v[188:191], v221 offset:21504
	ds_read_b128 v[202:205], v221 offset:22528
	ds_read_b128 v[206:209], v221 offset:23552
	global_load_lds_dwordx4 v[192:193], off
	v_lshl_add_u64 v[214:215], v[192:193], 0, s[90:91]
	s_mov_b32 m0, s36
	s_nop 0
	global_load_lds_dwordx4 v[214:215], off
	v_lshl_add_u64 v[214:215], v[192:193], 0, s[48:49]
	s_mov_b32 m0, s37
	s_nop 0
	global_load_lds_dwordx4 v[214:215], off
	v_lshl_add_u64 v[214:215], v[192:193], 0, s[52:53]
	s_mov_b32 m0, s38
	s_nop 0
	global_load_lds_dwordx4 v[214:215], off
	v_lshl_add_u64 v[214:215], s[44:45], 0, v[196:197]
	s_mov_b32 m0, s23
	v_lshl_add_u64 v[216:217], v[214:215], 0, s[96:97]
	global_load_lds_dwordx4 v[214:215], off
	s_mov_b32 m0, s24
	s_nop 0
	global_load_lds_dwordx4 v[216:217], off
	s_waitcnt vmcnt(8)
	s_waitcnt lgkmcnt(0)
	s_barrier
	v_mfma_f32_16x16x32_bf16 v[64:67], v[136:139], v[168:171], v[64:67]
	v_mfma_f32_16x16x32_bf16 v[64:67], v[140:143], v[172:175], v[64:67]
	v_mfma_f32_16x16x32_bf16 v[60:63], v[144:147], v[168:171], v[60:63]
	v_mfma_f32_16x16x32_bf16 v[60:63], v[148:151], v[172:175], v[60:63]
	v_mfma_f32_16x16x32_bf16 v[48:51], v[136:139], v[176:179], v[48:51]
	v_mfma_f32_16x16x32_bf16 v[48:51], v[140:143], v[180:183], v[48:51]
	v_mfma_f32_16x16x32_bf16 v[44:47], v[144:147], v[176:179], v[44:47]
	v_mfma_f32_16x16x32_bf16 v[44:47], v[148:151], v[180:183], v[44:47]
	v_mfma_f32_16x16x32_bf16 v[32:35], v[136:139], v[184:187], v[32:35]
	v_mfma_f32_16x16x32_bf16 v[32:35], v[140:143], v[188:191], v[32:35]
	v_mfma_f32_16x16x32_bf16 v[28:31], v[144:147], v[184:187], v[28:31]
	v_mfma_f32_16x16x32_bf16 v[28:31], v[148:151], v[188:191], v[28:31]
	v_mfma_f32_16x16x32_bf16 v[16:19], v[136:139], v[202:205], v[16:19]
	v_mfma_f32_16x16x32_bf16 v[16:19], v[140:143], v[206:209], v[16:19]
	v_mfma_f32_16x16x32_bf16 v[12:15], v[144:147], v[202:205], v[12:15]
	v_mfma_f32_16x16x32_bf16 v[12:15], v[148:151], v[206:209], v[12:15]
	v_mfma_f32_16x16x32_bf16 v[56:59], v[152:155], v[168:171], v[56:59]
	v_mfma_f32_16x16x32_bf16 v[56:59], v[156:159], v[172:175], v[56:59]
	v_mfma_f32_16x16x32_bf16 v[52:55], v[160:163], v[168:171], v[52:55]
	v_mfma_f32_16x16x32_bf16 v[52:55], v[164:167], v[172:175], v[52:55]
	v_mfma_f32_16x16x32_bf16 v[40:43], v[152:155], v[176:179], v[40:43]
	v_mfma_f32_16x16x32_bf16 v[40:43], v[156:159], v[180:183], v[40:43]
	v_mfma_f32_16x16x32_bf16 v[36:39], v[160:163], v[176:179], v[36:39]
	v_mfma_f32_16x16x32_bf16 v[36:39], v[164:167], v[180:183], v[36:39]
	v_mfma_f32_16x16x32_bf16 v[24:27], v[152:155], v[184:187], v[24:27]
	v_mfma_f32_16x16x32_bf16 v[24:27], v[156:159], v[188:191], v[24:27]
	v_mfma_f32_16x16x32_bf16 v[20:23], v[160:163], v[184:187], v[20:23]
	v_mfma_f32_16x16x32_bf16 v[20:23], v[164:167], v[188:191], v[20:23]
	v_mfma_f32_16x16x32_bf16 v[8:11], v[152:155], v[202:205], v[8:11]
	v_mfma_f32_16x16x32_bf16 v[8:11], v[156:159], v[206:209], v[8:11]
	v_mfma_f32_16x16x32_bf16 v[4:7], v[160:163], v[202:205], v[4:7]
	v_mfma_f32_16x16x32_bf16 v[4:7], v[164:167], v[206:209], v[4:7]
	s_barrier
; #define PG8_MMA(ai, bj, At, Bt) do { __builtin_amdgcn_s_setprio(1); _Pragma("unroll") for (int m = 0; m < 4; ++m) _Pragma("unroll") for (int n = 0; n < 2; ++n) _Pragma("unroll") for (int k = 0; k < 2; ++k) \
;         acc[ai][bj][m][n] = __builtin_amdgcn_mfma_f32_16x16x32_bf16(Bt[n][k], At[m][k], acc[ai][bj][m][n], 0, 0, 0); __builtin_amdgcn_s_setprio(0); } while (0)
; #define PG8_WAIT_V(n) asm volatile("s_waitcnt vmcnt(" #n ")" ::: "memory")
; #define PG8_TRIP_HEAD(T) const int t = (T); const bool last = (t == nt - 2); \
;             const char* a1 = cA + (size_t)(t + 1) * kstep; \
;             const char* a2 = last ? nA : cA + (size_t)(t + 2) * kstep; const char* b2 = last ? nB : cB + (size_t)(t + 2) * kstep; \
;             const char* a3 = a2 + kstep; const char* b3 = b2 + kstep; \
;             if (last && has_next) S.a_ready(nxt);
; template <class Epi, class Sched, bool ALIGN_EPI = false, bool SP2 = false>
; __device__ __forceinline__ void gemm_phase(PG8_LAS unsigned char* lds, const Gemm g, const Sched& S, const Epi& E) {
;     ...
;         if constexpr (SP2) {
;             { PG8_TRIP_HEAD(0) PG8_TRIP_SP2(asm volatile("s_waitcnt vmcnt(%0)" :: "n"(8 + Epi::NST) : "memory"), PG8_MMAZ) }
;             for (int tt = 2; tt < nt; tt += 2) { PG8_TRIP_HEAD(tt) PG8_TRIP_SP2(PG8_WAIT_V(8), PG8_MMA) }
	ds_read_b128 v[136:139], v134
	ds_read_b128 v[140:143], v134 offset:1024
	ds_read_b128 v[144:147], v134 offset:2048
	ds_read_b128 v[148:151], v134 offset:3072
	ds_read_b128 v[152:155], v135
	ds_read_b128 v[156:159], v135 offset:1024
	ds_read_b128 v[160:163], v135 offset:2048
	ds_read_b128 v[164:167], v135 offset:3072
	s_mov_b32 m0, s25
	v_lshl_add_u64 v[216:217], v[214:215], 0, s[82:83]
	ds_read_b128 v[168:171], v221 offset:32768
	ds_read_b128 v[172:175], v221 offset:33792
	ds_read_b128 v[176:179], v221 offset:34816
	ds_read_b128 v[180:183], v221 offset:35840
	ds_read_b128 v[184:187], v221 offset:36864
	ds_read_b128 v[188:191], v221 offset:37888
	ds_read_b128 v[202:205], v221 offset:38912
	ds_read_b128 v[206:209], v221 offset:39936
	global_load_lds_dwordx4 v[216:217], off
	v_lshl_add_u64 v[216:217], v[214:215], 0, s[56:57]
	s_mov_b32 m0, s26
	s_nop 0
	global_load_lds_dwordx4 v[216:217], off
	s_waitcnt vmcnt(8)
	s_waitcnt lgkmcnt(0)
	s_barrier
	v_mfma_f32_16x16x32_bf16 v[130:133], v[136:139], v[168:171], v[130:133]
	v_mfma_f32_16x16x32_bf16 v[130:133], v[140:143], v[172:175], v[130:133]
	v_mfma_f32_16x16x32_bf16 v[126:129], v[144:147], v[168:171], v[126:129]
	v_mfma_f32_16x16x32_bf16 v[126:129], v[148:151], v[172:175], v[126:129]
	v_mfma_f32_16x16x32_bf16 v[112:115], v[136:139], v[176:179], v[112:115]
	v_mfma_f32_16x16x32_bf16 v[112:115], v[140:143], v[180:183], v[112:115]
	v_mfma_f32_16x16x32_bf16 v[108:111], v[144:147], v[176:179], v[108:111]
	v_mfma_f32_16x16x32_bf16 v[108:111], v[148:151], v[180:183], v[108:111]
	v_mfma_f32_16x16x32_bf16 v[96:99], v[136:139], v[184:187], v[96:99]
	v_mfma_f32_16x16x32_bf16 v[96:99], v[140:143], v[188:191], v[96:99]
	v_mfma_f32_16x16x32_bf16 v[92:95], v[144:147], v[184:187], v[92:95]
	v_mfma_f32_16x16x32_bf16 v[92:95], v[148:151], v[188:191], v[92:95]
	v_mfma_f32_16x16x32_bf16 v[80:83], v[136:139], v[202:205], v[80:83]
	v_mfma_f32_16x16x32_bf16 v[80:83], v[140:143], v[206:209], v[80:83]
	v_mfma_f32_16x16x32_bf16 v[76:79], v[144:147], v[202:205], v[76:79]
	v_mfma_f32_16x16x32_bf16 v[76:79], v[148:151], v[206:209], v[76:79]
	v_mfma_f32_16x16x32_bf16 v[122:125], v[152:155], v[168:171], v[122:125]
	v_mfma_f32_16x16x32_bf16 v[122:125], v[156:159], v[172:175], v[122:125]
	v_mfma_f32_16x16x32_bf16 v[118:121], v[160:163], v[168:171], v[118:121]
	v_mfma_f32_16x16x32_bf16 v[118:121], v[164:167], v[172:175], v[118:121]
	v_mfma_f32_16x16x32_bf16 v[104:107], v[152:155], v[176:179], v[104:107]
	v_mfma_f32_16x16x32_bf16 v[104:107], v[156:159], v[180:183], v[104:107]
	v_mfma_f32_16x16x32_bf16 v[100:103], v[160:163], v[176:179], v[100:103]
	v_mfma_f32_16x16x32_bf16 v[100:103], v[164:167], v[180:183], v[100:103]
	v_mfma_f32_16x16x32_bf16 v[88:91], v[152:155], v[184:187], v[88:91]
	v_mfma_f32_16x16x32_bf16 v[88:91], v[156:159], v[188:191], v[88:91]
	v_mfma_f32_16x16x32_bf16 v[84:87], v[160:163], v[184:187], v[84:87]
	v_mfma_f32_16x16x32_bf16 v[84:87], v[164:167], v[188:191], v[84:87]
	v_mfma_f32_16x16x32_bf16 v[72:75], v[152:155], v[202:205], v[72:75]
	v_mfma_f32_16x16x32_bf16 v[72:75], v[156:159], v[206:209], v[72:75]
	v_mfma_f32_16x16x32_bf16 v[68:71], v[160:163], v[202:205], v[68:71]
	v_mfma_f32_16x16x32_bf16 v[68:71], v[164:167], v[206:209], v[68:71]
	s_barrier
	s_mov_b32 m0, s39
	v_lshl_add_u64 v[216:217], v[192:193], 0, s[78:79]
	ds_read_b128 v[168:171], v221 offset:49152
	ds_read_b128 v[172:175], v221 offset:50176
	ds_read_b128 v[176:179], v221 offset:51200
	ds_read_b128 v[180:183], v221 offset:52224
	ds_read_b128 v[184:187], v221 offset:53248
	ds_read_b128 v[188:191], v221 offset:54272
	ds_read_b128 v[202:205], v221 offset:55296
	ds_read_b128 v[206:209], v221 offset:56320
	global_load_lds_dwordx4 v[216:217], off
	v_lshl_add_u64 v[216:217], v[192:193], 0, s[84:85]
	s_mov_b32 m0, s40
	s_nop 0
	global_load_lds_dwordx4 v[216:217], off
	v_lshl_add_u64 v[216:217], v[192:193], 0, s[50:51]
	s_mov_b32 m0, s41
	v_lshl_add_u64 v[192:193], v[192:193], 0, s[54:55]
	global_load_lds_dwordx4 v[216:217], off
	s_mov_b32 m0, s42
	s_nop 0
	global_load_lds_dwordx4 v[192:193], off
	v_lshl_add_u64 v[192:193], v[214:215], 0, s[78:79]
	s_mov_b32 m0, s27
	s_nop 0
	global_load_lds_dwordx4 v[192:193], off
	v_lshl_add_u64 v[192:193], v[214:215], 0, s[92:93]
	s_mov_b32 m0, s28
	s_nop 0
	global_load_lds_dwordx4 v[192:193], off
	s_waitcnt vmcnt(8)
	s_waitcnt lgkmcnt(0)
	s_barrier
	v_mfma_f32_16x16x32_bf16 v[64:67], v[136:139], v[168:171], v[64:67]
	v_mfma_f32_16x16x32_bf16 v[64:67], v[140:143], v[172:175], v[64:67]
	v_mfma_f32_16x16x32_bf16 v[60:63], v[144:147], v[168:171], v[60:63]
	v_mfma_f32_16x16x32_bf16 v[60:63], v[148:151], v[172:175], v[60:63]
	v_mfma_f32_16x16x32_bf16 v[48:51], v[136:139], v[176:179], v[48:51]
	v_mfma_f32_16x16x32_bf16 v[48:51], v[140:143], v[180:183], v[48:51]
	v_mfma_f32_16x16x32_bf16 v[44:47], v[144:147], v[176:179], v[44:47]
	v_mfma_f32_16x16x32_bf16 v[44:47], v[148:151], v[180:183], v[44:47]
	v_mfma_f32_16x16x32_bf16 v[32:35], v[136:139], v[184:187], v[32:35]
	v_mfma_f32_16x16x32_bf16 v[32:35], v[140:143], v[188:191], v[32:35]
	v_mfma_f32_16x16x32_bf16 v[28:31], v[144:147], v[184:187], v[28:31]
	v_mfma_f32_16x16x32_bf16 v[28:31], v[148:151], v[188:191], v[28:31]
	v_mfma_f32_16x16x32_bf16 v[16:19], v[136:139], v[202:205], v[16:19]
	v_mfma_f32_16x16x32_bf16 v[16:19], v[140:143], v[206:209], v[16:19]
	v_mfma_f32_16x16x32_bf16 v[12:15], v[144:147], v[202:205], v[12:15]
	v_mfma_f32_16x16x32_bf16 v[12:15], v[148:151], v[206:209], v[12:15]
	v_mfma_f32_16x16x32_bf16 v[56:59], v[152:155], v[168:171], v[56:59]
	v_mfma_f32_16x16x32_bf16 v[56:59], v[156:159], v[172:175], v[56:59]
	v_mfma_f32_16x16x32_bf16 v[52:55], v[160:163], v[168:171], v[52:55]
	v_mfma_f32_16x16x32_bf16 v[52:55], v[164:167], v[172:175], v[52:55]
	v_mfma_f32_16x16x32_bf16 v[40:43], v[152:155], v[176:179], v[40:43]
	v_mfma_f32_16x16x32_bf16 v[40:43], v[156:159], v[180:183], v[40:43]
	v_mfma_f32_16x16x32_bf16 v[36:39], v[160:163], v[176:179], v[36:39]
	v_mfma_f32_16x16x32_bf16 v[36:39], v[164:167], v[180:183], v[36:39]
	v_mfma_f32_16x16x32_bf16 v[24:27], v[152:155], v[184:187], v[24:27]
	v_mfma_f32_16x16x32_bf16 v[24:27], v[156:159], v[188:191], v[24:27]
	v_mfma_f32_16x16x32_bf16 v[20:23], v[160:163], v[184:187], v[20:23]
	v_mfma_f32_16x16x32_bf16 v[20:23], v[164:167], v[188:191], v[20:23]
	v_mfma_f32_16x16x32_bf16 v[8:11], v[152:155], v[202:205], v[8:11]
	v_mfma_f32_16x16x32_bf16 v[8:11], v[156:159], v[206:209], v[8:11]
	v_mfma_f32_16x16x32_bf16 v[4:7], v[160:163], v[202:205], v[4:7]
	v_mfma_f32_16x16x32_bf16 v[4:7], v[164:167], v[206:209], v[4:7]
	s_barrier
	s_add_i32 s15, s15, 2
	s_add_u32 s20, s20, 0x100
	s_addc_u32 s21, s21, 0
	s_add_u32 s8, s8, 0x100
	s_addc_u32 s9, s9, 0
	s_cmp_gt_u32 s15, 29
	s_cbranch_scc0 .LBB0_594
	s_and_b64 vcc, exec, s[12:13]
	s_cbranch_vccz .LBB0_597
	s_barrier

.LBB0_699:
	s_ashr_i32 s19, s18, 31
	s_lshl_b64 s[4:5], s[18:19], 20
	v_readlane_b32 s22, v254, 33
	v_readlane_b32 s23, v254, 34
	s_add_u32 s22, s22, s4
	s_addc_u32 s23, s23, s5
	s_add_i32 s33, 0, 0x10000
	s_add_i32 s41, 0, 0x14000
	v_add_u32_e32 v116, s33, v176
	v_add_u32_e32 v117, s41, v176
	ds_read_b128 v[4:7], v116
	ds_read_b128 v[8:11], v116 offset:1024
	ds_read_b128 v[12:15], v116 offset:2048
	ds_read_b128 v[16:19], v116 offset:3072
	ds_read_b128 v[20:23], v117
	ds_read_b128 v[24:27], v117 offset:1024
	ds_read_b128 v[28:31], v117 offset:2048
	ds_read_b128 v[32:35], v117 offset:3072
	s_and_b64 s[4:5], s[10:11], exec
	s_cselect_b32 s3, s23, s25
	s_cselect_b32 s4, s22, s24
	v_lshl_add_u64 v[208:209], s[26:27], 0, v[162:163]
	s_mov_b64 s[10:11], 0x84080
	s_add_i32 s5, s29, 0xc000
	v_lshl_add_u64 v[68:69], v[208:209], 0, s[10:11]
	s_mov_b32 m0, s5
	s_mov_b64 s[10:11], 0xc6080
	s_add_i32 s19, s29, 0xe000
	ds_read_b128 v[36:39], v178
	ds_read_b128 v[40:43], v178 offset:1024
	ds_read_b128 v[44:47], v178 offset:2048
	ds_read_b128 v[48:51], v178 offset:3072
	ds_read_b128 v[52:55], v178 offset:4096
	ds_read_b128 v[56:59], v178 offset:5120
	ds_read_b128 v[60:63], v178 offset:6144
	ds_read_b128 v[64:67], v178 offset:7168
	global_load_lds_dwordx4 v[68:69], off
	v_lshl_add_u64 v[68:69], v[208:209], 0, s[10:11]
	s_mov_b32 m0, s19
	s_nop 0
	global_load_lds_dwordx4 v[68:69], off
	s_waitcnt vmcnt(16)
	s_waitcnt lgkmcnt(0)
	s_barrier
	v_mfma_f32_16x16x32_bf16 v[92:95], v[4:7], v[60:63], 0
	v_mfma_f32_16x16x32_bf16 v[68:71], v[4:7], v[36:39], 0
	v_mfma_f32_16x16x32_bf16 v[72:75], v[12:15], v[36:39], 0
	v_mfma_f32_16x16x32_bf16 v[76:79], v[4:7], v[44:47], 0
	v_mfma_f32_16x16x32_bf16 v[80:83], v[12:15], v[44:47], 0
	v_mfma_f32_16x16x32_bf16 v[84:87], v[4:7], v[52:55], 0
	v_mfma_f32_16x16x32_bf16 v[88:91], v[12:15], v[52:55], 0
	v_mfma_f32_16x16x32_bf16 v[100:103], v[8:11], v[64:67], v[92:95]
	v_mfma_f32_16x16x32_bf16 v[92:95], v[12:15], v[60:63], 0
	v_mfma_f32_16x16x32_bf16 v[68:71], v[8:11], v[40:43], v[68:71]
	v_mfma_f32_16x16x32_bf16 v[72:75], v[16:19], v[40:43], v[72:75]
	v_mfma_f32_16x16x32_bf16 v[76:79], v[8:11], v[48:51], v[76:79]
	v_mfma_f32_16x16x32_bf16 v[80:83], v[16:19], v[48:51], v[80:83]
	v_mfma_f32_16x16x32_bf16 v[84:87], v[8:11], v[56:59], v[84:87]
	v_mfma_f32_16x16x32_bf16 v[88:91], v[16:19], v[56:59], v[88:91]
	v_mfma_f32_16x16x32_bf16 v[104:107], v[16:19], v[64:67], v[92:95]
	v_mfma_f32_16x16x32_bf16 v[92:95], v[20:23], v[36:39], 0
	v_mfma_f32_16x16x32_bf16 v[36:39], v[28:31], v[36:39], 0
	v_mfma_f32_16x16x32_bf16 v[120:123], v[24:27], v[40:43], v[92:95]
	v_mfma_f32_16x16x32_bf16 v[36:39], v[32:35], v[40:43], v[36:39]
	v_mfma_f32_16x16x32_bf16 v[40:43], v[20:23], v[44:47], 0
	v_mfma_f32_16x16x32_bf16 v[44:47], v[28:31], v[44:47], 0
	v_mfma_f32_16x16x32_bf16 v[40:43], v[24:27], v[48:51], v[40:43]
	v_mfma_f32_16x16x32_bf16 v[44:47], v[32:35], v[48:51], v[44:47]
	v_mfma_f32_16x16x32_bf16 v[48:51], v[20:23], v[52:55], 0
	v_mfma_f32_16x16x32_bf16 v[52:55], v[28:31], v[52:55], 0
	v_mfma_f32_16x16x32_bf16 v[48:51], v[24:27], v[56:59], v[48:51]
	v_mfma_f32_16x16x32_bf16 v[52:55], v[32:35], v[56:59], v[52:55]
	v_mfma_f32_16x16x32_bf16 v[56:59], v[20:23], v[60:63], 0
	v_mfma_f32_16x16x32_bf16 v[60:63], v[28:31], v[60:63], 0
	v_mfma_f32_16x16x32_bf16 v[56:59], v[24:27], v[64:67], v[56:59]
	v_mfma_f32_16x16x32_bf16 v[60:63], v[32:35], v[64:67], v[60:63]
	s_barrier
	v_lshl_add_u64 v[250:251], s[24:25], 0, v[160:161]
	s_mov_b64 s[10:11], 0x100
	s_add_i32 s33, s33, s28
	v_lshl_add_u64 v[118:119], v[250:251], 0, s[10:11]
	s_mov_b32 m0, s33
	s_mov_b64 s[42:43], 0x40100
	s_add_i32 s40, s33, 0x2000
	ds_read_b128 v[64:67], v178 offset:16384
	ds_read_b128 v[92:95], v178 offset:17408
	ds_read_b128 v[96:99], v178 offset:18432
	ds_read_b128 v[108:111], v178 offset:19456
	ds_read_b128 v[112:115], v178 offset:20480
	ds_read_b128 v[124:127], v178 offset:21504
	ds_read_b128 v[128:131], v178 offset:22528
	ds_read_b128 v[132:135], v178 offset:23552
	global_load_lds_dwordx4 v[118:119], off
	v_lshl_add_u64 v[118:119], v[250:251], 0, s[42:43]
	s_mov_b32 m0, s40
	s_mov_b64 s[42:43], 0x80100
	s_add_i32 s41, s41, s28
	global_load_lds_dwordx4 v[118:119], off
	v_lshl_add_u64 v[118:119], v[250:251], 0, s[42:43]
	s_mov_b32 m0, s41
	s_mov_b64 s[42:43], 0xc0100
	global_load_lds_dwordx4 v[118:119], off
	v_lshl_add_u64 v[118:119], v[250:251], 0, s[42:43]
	s_add_i32 s42, s41, 0x2000
	s_mov_b32 m0, s42
	s_nop 0
	global_load_lds_dwordx4 v[118:119], off
	v_lshl_add_u64 v[118:119], v[208:209], 0, s[10:11]
	s_mov_b32 m0, s29
	s_mov_b64 s[10:11], 0x42100
	global_load_lds_dwordx4 v[118:119], off
	v_lshl_add_u64 v[118:119], v[208:209], 0, s[10:11]
	s_mov_b32 m0, s30
	s_nop 0
	global_load_lds_dwordx4 v[118:119], off
	s_waitcnt vmcnt(16)
	s_waitcnt lgkmcnt(0)
	s_barrier
	v_mfma_f32_16x16x32_bf16 v[136:139], v[4:7], v[64:67], 0
	v_mfma_f32_16x16x32_bf16 v[144:147], v[8:11], v[92:95], v[136:139]
	v_mfma_f32_16x16x32_bf16 v[136:139], v[12:15], v[64:67], 0
	v_mfma_f32_16x16x32_bf16 v[148:151], v[16:19], v[92:95], v[136:139]
	v_mfma_f32_16x16x32_bf16 v[136:139], v[4:7], v[96:99], 0
	v_mfma_f32_16x16x32_bf16 v[152:155], v[8:11], v[108:111], v[136:139]
	v_mfma_f32_16x16x32_bf16 v[136:139], v[12:15], v[96:99], 0
	v_mfma_f32_16x16x32_bf16 v[156:159], v[16:19], v[108:111], v[136:139]
	v_mfma_f32_16x16x32_bf16 v[136:139], v[4:7], v[112:115], 0
	v_mfma_f32_16x16x32_bf16 v[4:7], v[4:7], v[128:131], 0
	v_mfma_f32_16x16x32_bf16 v[166:169], v[8:11], v[124:127], v[136:139]
	v_mfma_f32_16x16x32_bf16 v[4:7], v[8:11], v[132:135], v[4:7]
	v_mfma_f32_16x16x32_bf16 v[8:11], v[12:15], v[128:131], 0
	v_mfma_f32_16x16x32_bf16 v[136:139], v[12:15], v[112:115], 0
	v_mfma_f32_16x16x32_bf16 v[8:11], v[16:19], v[132:135], v[8:11]
	v_mfma_f32_16x16x32_bf16 v[170:173], v[16:19], v[124:127], v[136:139]
	v_mfma_f32_16x16x32_bf16 v[12:15], v[20:23], v[64:67], 0
	v_mfma_f32_16x16x32_bf16 v[180:183], v[24:27], v[92:95], v[12:15]
	v_mfma_f32_16x16x32_bf16 v[12:15], v[28:31], v[64:67], 0
	v_mfma_f32_16x16x32_bf16 v[184:187], v[32:35], v[92:95], v[12:15]
	v_mfma_f32_16x16x32_bf16 v[12:15], v[20:23], v[96:99], 0
	v_mfma_f32_16x16x32_bf16 v[188:191], v[24:27], v[108:111], v[12:15]
	v_mfma_f32_16x16x32_bf16 v[12:15], v[28:31], v[96:99], 0
	v_mfma_f32_16x16x32_bf16 v[192:195], v[32:35], v[108:111], v[12:15]
	v_mfma_f32_16x16x32_bf16 v[12:15], v[20:23], v[112:115], 0
	v_mfma_f32_16x16x32_bf16 v[196:199], v[24:27], v[124:127], v[12:15]
	v_mfma_f32_16x16x32_bf16 v[12:15], v[28:31], v[112:115], 0
	v_mfma_f32_16x16x32_bf16 v[200:203], v[32:35], v[124:127], v[12:15]
	v_mfma_f32_16x16x32_bf16 v[12:15], v[20:23], v[128:131], 0
	v_mfma_f32_16x16x32_bf16 v[204:207], v[24:27], v[132:135], v[12:15]
	v_mfma_f32_16x16x32_bf16 v[12:15], v[28:31], v[128:131], 0
	v_mfma_f32_16x16x32_bf16 v[132:135], v[32:35], v[132:135], v[12:15]
	s_barrier
	s_add_i32 s43, 0, 0x18000
	s_add_i32 s45, 0, 0x1c000
	v_add_u32_e32 v118, s43, v176
	v_add_u32_e32 v119, s45, v176
	s_nop 0
	ds_read_b128 v[12:15], v118
	ds_read_b128 v[16:19], v118 offset:1024
	ds_read_b128 v[20:23], v118 offset:2048
	ds_read_b128 v[24:27], v118 offset:3072
	ds_read_b128 v[214:217], v119
	ds_read_b128 v[218:221], v119 offset:1024
	ds_read_b128 v[222:225], v119 offset:2048
	ds_read_b128 v[226:229], v119 offset:3072
	s_mov_b64 s[10:11], 0x84100
	s_mov_b32 m0, s31
	v_lshl_add_u64 v[92:93], v[208:209], 0, s[10:11]
	s_mov_b64 s[10:11], 0xc6100
	ds_read_b128 v[28:31], v178 offset:32768
	ds_read_b128 v[32:35], v178 offset:33792
	ds_read_b128 v[64:67], v178 offset:34816
	ds_read_b128 v[230:233], v178 offset:35840
	ds_read_b128 v[234:237], v178 offset:36864
	ds_read_b128 v[238:241], v178 offset:37888
	ds_read_b128 v[242:245], v178 offset:38912
	ds_read_b128 v[246:249], v178 offset:39936
	global_load_lds_dwordx4 v[92:93], off
	v_lshl_add_u64 v[92:93], v[208:209], 0, s[10:11]
	s_mov_b32 m0, s34
	s_nop 0
	global_load_lds_dwordx4 v[92:93], off
	s_waitcnt vmcnt(8)
	s_waitcnt lgkmcnt(0)
	s_barrier
	v_mfma_f32_16x16x32_bf16 v[68:71], v[12:15], v[28:31], v[68:71]
	v_mfma_f32_16x16x32_bf16 v[140:143], v[16:19], v[32:35], v[68:71]
	v_mfma_f32_16x16x32_bf16 v[68:71], v[20:23], v[28:31], v[72:75]
	v_mfma_f32_16x16x32_bf16 v[136:139], v[24:27], v[32:35], v[68:71]
	v_mfma_f32_16x16x32_bf16 v[68:71], v[12:15], v[64:67], v[76:79]
	v_mfma_f32_16x16x32_bf16 v[112:115], v[16:19], v[230:233], v[68:71]
	v_mfma_f32_16x16x32_bf16 v[68:71], v[20:23], v[64:67], v[80:83]
	v_mfma_f32_16x16x32_bf16 v[108:111], v[24:27], v[230:233], v[68:71]
	v_mfma_f32_16x16x32_bf16 v[68:71], v[12:15], v[234:237], v[84:87]
	v_mfma_f32_16x16x32_bf16 v[96:99], v[16:19], v[238:241], v[68:71]
	v_mfma_f32_16x16x32_bf16 v[68:71], v[20:23], v[234:237], v[88:91]
	v_mfma_f32_16x16x32_bf16 v[92:95], v[24:27], v[238:241], v[68:71]
	v_mfma_f32_16x16x32_bf16 v[68:71], v[12:15], v[242:245], v[100:103]
	v_mfma_f32_16x16x32_bf16 v[80:83], v[16:19], v[246:249], v[68:71]
	v_mfma_f32_16x16x32_bf16 v[68:71], v[20:23], v[242:245], v[104:107]
	v_mfma_f32_16x16x32_bf16 v[76:79], v[24:27], v[246:249], v[68:71]
	v_mfma_f32_16x16x32_bf16 v[68:71], v[214:217], v[28:31], v[120:123]
	v_mfma_f32_16x16x32_bf16 v[28:31], v[222:225], v[28:31], v[36:39]
	v_mfma_f32_16x16x32_bf16 v[124:127], v[226:229], v[32:35], v[28:31]
	v_mfma_f32_16x16x32_bf16 v[28:31], v[214:217], v[64:67], v[40:43]
	v_mfma_f32_16x16x32_bf16 v[104:107], v[218:221], v[230:233], v[28:31]
	v_mfma_f32_16x16x32_bf16 v[28:31], v[222:225], v[64:67], v[44:47]
	v_mfma_f32_16x16x32_bf16 v[100:103], v[226:229], v[230:233], v[28:31]
	v_mfma_f32_16x16x32_bf16 v[28:31], v[214:217], v[234:237], v[48:51]
	v_mfma_f32_16x16x32_bf16 v[88:91], v[218:221], v[238:241], v[28:31]
	v_mfma_f32_16x16x32_bf16 v[28:31], v[222:225], v[234:237], v[52:55]
	v_mfma_f32_16x16x32_bf16 v[84:87], v[226:229], v[238:241], v[28:31]
	v_mfma_f32_16x16x32_bf16 v[28:31], v[214:217], v[242:245], v[56:59]
	v_mfma_f32_16x16x32_bf16 v[72:75], v[218:221], v[246:249], v[28:31]
	v_mfma_f32_16x16x32_bf16 v[28:31], v[222:225], v[242:245], v[60:63]
	v_mfma_f32_16x16x32_bf16 v[128:131], v[218:221], v[32:35], v[68:71]
	v_mfma_f32_16x16x32_bf16 v[68:71], v[226:229], v[246:249], v[28:31]
	s_barrier
; #define PG8_MMA(ai, bj, At, Bt) do { __builtin_amdgcn_s_setprio(1); _Pragma("unroll") for (int m = 0; m < 4; ++m) _Pragma("unroll") for (int n = 0; n < 2; ++n) _Pragma("unroll") for (int k = 0; k < 2; ++k) \
;         acc[ai][bj][m][n] = __builtin_amdgcn_mfma_f32_16x16x32_bf16(Bt[n][k], At[m][k], acc[ai][bj][m][n], 0, 0, 0); __builtin_amdgcn_s_setprio(0); } while (0)
; #define PG8_WAIT_V(n) asm volatile("s_waitcnt vmcnt(" #n ")" ::: "memory")
; #define PG8_TRIP_HEAD(T) const int t = (T); const bool last = (t == nt - 2); \
;             const char* a1 = cA + (size_t)(t + 1) * kstep; \
;             const char* a2 = last ? nA : cA + (size_t)(t + 2) * kstep; const char* b2 = last ? nB : cB + (size_t)(t + 2) * kstep; \
;             const char* a3 = a2 + kstep; const char* b3 = b2 + kstep; \
;             if (last && has_next) S.a_ready(nxt);
; template <class Epi, class Sched, bool ALIGN_EPI = false, bool SP2 = false>
; __device__ __forceinline__ void gemm_phase(PG8_LAS unsigned char* lds, const Gemm g, const Sched& S, const Epi& E) {
;     ...
;         if constexpr (SP2) {
;             { PG8_TRIP_HEAD(0) PG8_TRIP_SP2(asm volatile("s_waitcnt vmcnt(%0)" :: "n"(8 + Epi::NST) : "memory"), PG8_MMAZ) }
;             for (int tt = 2; tt < nt; tt += 2) { PG8_TRIP_HEAD(tt) PG8_TRIP_SP2(PG8_WAIT_V(8), PG8_MMA) }
	s_mov_b64 s[10:11], 0x180
	s_add_i32 s43, s43, s28
	s_nop 1
	v_lshl_add_u64 v[28:29], v[250:251], 0, s[10:11]
	s_mov_b32 m0, s43
	s_mov_b64 s[46:47], 0x40180
	s_add_i32 s44, s43, 0x2000
	ds_read_b128 v[36:39], v178 offset:49152
	ds_read_b128 v[40:43], v178 offset:50176
	ds_read_b128 v[120:123], v178 offset:51200
	ds_read_b128 v[230:233], v178 offset:52224
	ds_read_b128 v[234:237], v178 offset:53248
	ds_read_b128 v[238:241], v178 offset:54272
	ds_read_b128 v[242:245], v178 offset:55296
	ds_read_b128 v[246:249], v178 offset:56320
	global_load_lds_dwordx4 v[28:29], off
	v_lshl_add_u64 v[28:29], v[250:251], 0, s[46:47]
	s_mov_b32 m0, s44
	s_mov_b64 s[46:47], 0x80180
	s_add_i32 s45, s45, s28
	global_load_lds_dwordx4 v[28:29], off
	v_lshl_add_u64 v[28:29], v[250:251], 0, s[46:47]
	s_mov_b32 m0, s45
	s_mov_b64 s[46:47], 0xc0180
	global_load_lds_dwordx4 v[28:29], off
	v_lshl_add_u64 v[28:29], v[250:251], 0, s[46:47]
	s_add_i32 s46, s45, 0x2000
	s_mov_b32 m0, s46
	s_nop 0
	global_load_lds_dwordx4 v[28:29], off
	v_lshl_add_u64 v[28:29], v[208:209], 0, s[10:11]
	s_mov_b32 m0, s36
	s_mov_b64 s[10:11], 0x42180
	global_load_lds_dwordx4 v[28:29], off
	v_lshl_add_u64 v[28:29], v[208:209], 0, s[10:11]
	s_mov_b32 m0, s37
	s_nop 0
	global_load_lds_dwordx4 v[28:29], off
	s_waitcnt vmcnt(8)
	s_waitcnt lgkmcnt(0)
	s_barrier
	v_mfma_f32_16x16x32_bf16 v[28:31], v[12:15], v[36:39], v[144:147]
	v_mfma_f32_16x16x32_bf16 v[56:59], v[16:19], v[40:43], v[28:31]
	v_mfma_f32_16x16x32_bf16 v[28:31], v[20:23], v[36:39], v[148:151]
	v_mfma_f32_16x16x32_bf16 v[52:55], v[24:27], v[40:43], v[28:31]
	v_mfma_f32_16x16x32_bf16 v[28:31], v[12:15], v[120:123], v[152:155]
	v_mfma_f32_16x16x32_bf16 v[48:51], v[16:19], v[230:233], v[28:31]
	v_mfma_f32_16x16x32_bf16 v[28:31], v[20:23], v[120:123], v[156:159]
	v_mfma_f32_16x16x32_bf16 v[44:47], v[24:27], v[230:233], v[28:31]
	v_mfma_f32_16x16x32_bf16 v[28:31], v[12:15], v[234:237], v[166:169]
	v_mfma_f32_16x16x32_bf16 v[4:7], v[12:15], v[242:245], v[4:7]
	v_mfma_f32_16x16x32_bf16 v[32:35], v[16:19], v[238:241], v[28:31]
	v_mfma_f32_16x16x32_bf16 v[28:31], v[20:23], v[234:237], v[170:173]
	v_mfma_f32_16x16x32_bf16 v[16:19], v[16:19], v[246:249], v[4:7]
	v_mfma_f32_16x16x32_bf16 v[4:7], v[20:23], v[242:245], v[8:11]
	v_mfma_f32_16x16x32_bf16 v[28:31], v[24:27], v[238:241], v[28:31]
	v_mfma_f32_16x16x32_bf16 v[12:15], v[24:27], v[246:249], v[4:7]
	v_mfma_f32_16x16x32_bf16 v[4:7], v[214:217], v[36:39], v[180:183]
	v_mfma_f32_16x16x32_bf16 v[64:67], v[218:221], v[40:43], v[4:7]
	v_mfma_f32_16x16x32_bf16 v[4:7], v[222:225], v[36:39], v[184:187]
	v_mfma_f32_16x16x32_bf16 v[60:63], v[226:229], v[40:43], v[4:7]
	v_mfma_f32_16x16x32_bf16 v[4:7], v[214:217], v[120:123], v[188:191]
	v_mfma_f32_16x16x32_bf16 v[40:43], v[218:221], v[230:233], v[4:7]
	v_mfma_f32_16x16x32_bf16 v[4:7], v[222:225], v[120:123], v[192:195]
	v_mfma_f32_16x16x32_bf16 v[36:39], v[226:229], v[230:233], v[4:7]
	v_mfma_f32_16x16x32_bf16 v[4:7], v[214:217], v[234:237], v[196:199]
	v_mfma_f32_16x16x32_bf16 v[24:27], v[218:221], v[238:241], v[4:7]
	v_mfma_f32_16x16x32_bf16 v[4:7], v[222:225], v[234:237], v[200:203]
	v_mfma_f32_16x16x32_bf16 v[20:23], v[226:229], v[238:241], v[4:7]
	v_mfma_f32_16x16x32_bf16 v[4:7], v[214:217], v[242:245], v[204:207]
	v_mfma_f32_16x16x32_bf16 v[8:11], v[218:221], v[246:249], v[4:7]
	v_mfma_f32_16x16x32_bf16 v[4:7], v[222:225], v[242:245], v[132:135]
	v_mfma_f32_16x16x32_bf16 v[4:7], v[226:229], v[246:249], v[4:7]
	s_barrier
	s_add_u32 s10, s26, 0x84180
	s_addc_u32 s11, s27, 0
	s_add_u32 s24, s24, 0x200
	s_addc_u32 s25, s25, 0
	s_mov_b32 s26, 0
	s_mov_b64 s[52:53], 0x80000
	s_mov_b64 s[54:55], 0x80080
	s_mov_b64 s[56:57], 0xc0000
	s_mov_b64 s[60:61], 0xc0080
	s_mov_b64 s[62:63], 0xc6000
.LBB0_700:
	ds_read_b128 v[120:123], v116
	ds_read_b128 v[132:135], v116 offset:1024
	ds_read_b128 v[144:147], v116 offset:2048
	ds_read_b128 v[148:151], v116 offset:3072
	ds_read_b128 v[152:155], v117
	ds_read_b128 v[156:159], v117 offset:1024
	ds_read_b128 v[166:169], v117 offset:2048
	ds_read_b128 v[170:173], v117 offset:3072
	s_add_u32 s27, s10, 0xfff7c080
	s_addc_u32 s47, s11, -1
	s_cmp_eq_u32 s26, 28
	s_cselect_b32 s49, s21, s47
	s_cselect_b32 s48, s20, s27
	s_cselect_b32 s51, s3, s25
	s_cselect_b32 s50, s4, s24
	s_mov_b32 m0, s5
	v_lshl_add_u64 v[208:209], s[10:11], 0, v[164:165]
	ds_read_b128 v[180:183], v178
	ds_read_b128 v[184:187], v178 offset:1024
	ds_read_b128 v[188:191], v178 offset:2048
	ds_read_b128 v[192:195], v178 offset:3072
	ds_read_b128 v[196:199], v178 offset:4096
	ds_read_b128 v[200:203], v178 offset:5120
	ds_read_b128 v[204:207], v178 offset:6144
	ds_read_b128 v[214:217], v178 offset:7168
	global_load_lds_dwordx4 v[208:209], off
	v_lshl_add_u64 v[208:209], v[208:209], 0, s[96:97]
	s_mov_b32 m0, s19
	s_nop 0
	global_load_lds_dwordx4 v[208:209], off
	s_waitcnt vmcnt(8)
	s_waitcnt lgkmcnt(0)
	s_barrier
	v_mfma_f32_16x16x32_bf16 v[140:143], v[120:123], v[180:183], v[140:143]
	v_mfma_f32_16x16x32_bf16 v[140:143], v[132:135], v[184:187], v[140:143]
	v_mfma_f32_16x16x32_bf16 v[136:139], v[144:147], v[180:183], v[136:139]
	v_mfma_f32_16x16x32_bf16 v[136:139], v[148:151], v[184:187], v[136:139]
	v_mfma_f32_16x16x32_bf16 v[112:115], v[120:123], v[188:191], v[112:115]
	v_mfma_f32_16x16x32_bf16 v[112:115], v[132:135], v[192:195], v[112:115]
	v_mfma_f32_16x16x32_bf16 v[108:111], v[144:147], v[188:191], v[108:111]
	v_mfma_f32_16x16x32_bf16 v[108:111], v[148:151], v[192:195], v[108:111]
	v_mfma_f32_16x16x32_bf16 v[96:99], v[120:123], v[196:199], v[96:99]
	v_mfma_f32_16x16x32_bf16 v[96:99], v[132:135], v[200:203], v[96:99]
	v_mfma_f32_16x16x32_bf16 v[92:95], v[144:147], v[196:199], v[92:95]
	v_mfma_f32_16x16x32_bf16 v[92:95], v[148:151], v[200:203], v[92:95]
	v_mfma_f32_16x16x32_bf16 v[80:83], v[120:123], v[204:207], v[80:83]
	v_mfma_f32_16x16x32_bf16 v[80:83], v[132:135], v[214:217], v[80:83]
	v_mfma_f32_16x16x32_bf16 v[76:79], v[144:147], v[204:207], v[76:79]
	v_mfma_f32_16x16x32_bf16 v[76:79], v[148:151], v[214:217], v[76:79]
	v_mfma_f32_16x16x32_bf16 v[128:131], v[152:155], v[180:183], v[128:131]
	v_mfma_f32_16x16x32_bf16 v[128:131], v[156:159], v[184:187], v[128:131]
	v_mfma_f32_16x16x32_bf16 v[124:127], v[166:169], v[180:183], v[124:127]
	v_mfma_f32_16x16x32_bf16 v[124:127], v[170:173], v[184:187], v[124:127]
	v_mfma_f32_16x16x32_bf16 v[104:107], v[152:155], v[188:191], v[104:107]
	v_mfma_f32_16x16x32_bf16 v[104:107], v[156:159], v[192:195], v[104:107]
	v_mfma_f32_16x16x32_bf16 v[100:103], v[166:169], v[188:191], v[100:103]
	v_mfma_f32_16x16x32_bf16 v[100:103], v[170:173], v[192:195], v[100:103]
	v_mfma_f32_16x16x32_bf16 v[88:91], v[152:155], v[196:199], v[88:91]
	v_mfma_f32_16x16x32_bf16 v[88:91], v[156:159], v[200:203], v[88:91]
	v_mfma_f32_16x16x32_bf16 v[84:87], v[166:169], v[196:199], v[84:87]
	v_mfma_f32_16x16x32_bf16 v[84:87], v[170:173], v[200:203], v[84:87]
	v_mfma_f32_16x16x32_bf16 v[72:75], v[152:155], v[204:207], v[72:75]
	v_mfma_f32_16x16x32_bf16 v[72:75], v[156:159], v[214:217], v[72:75]
	v_mfma_f32_16x16x32_bf16 v[68:71], v[166:169], v[204:207], v[68:71]
	v_mfma_f32_16x16x32_bf16 v[68:71], v[170:173], v[214:217], v[68:71]
	s_barrier
	s_mov_b32 m0, s33
	v_lshl_add_u64 v[208:209], s[50:51], 0, v[160:161]
	ds_read_b128 v[180:183], v178 offset:16384
	ds_read_b128 v[184:187], v178 offset:17408
	ds_read_b128 v[188:191], v178 offset:18432
	ds_read_b128 v[192:195], v178 offset:19456
	ds_read_b128 v[196:199], v178 offset:20480
	ds_read_b128 v[200:203], v178 offset:21504
	ds_read_b128 v[204:207], v178 offset:22528
	ds_read_b128 v[214:217], v178 offset:23552
	global_load_lds_dwordx4 v[208:209], off
	v_lshl_add_u64 v[218:219], v[208:209], 0, s[90:91]
	s_mov_b32 m0, s40
	s_nop 0
	global_load_lds_dwordx4 v[218:219], off
	v_lshl_add_u64 v[218:219], v[208:209], 0, s[52:53]
	s_mov_b32 m0, s41
	s_nop 0
	global_load_lds_dwordx4 v[218:219], off
	v_lshl_add_u64 v[218:219], v[208:209], 0, s[56:57]
	s_mov_b32 m0, s42
	s_nop 0
	global_load_lds_dwordx4 v[218:219], off
	v_lshl_add_u64 v[218:219], s[48:49], 0, v[162:163]
	s_mov_b32 m0, s29
	v_lshl_add_u64 v[220:221], v[218:219], 0, s[96:97]
	global_load_lds_dwordx4 v[218:219], off
	s_mov_b32 m0, s30
	s_nop 0
	global_load_lds_dwordx4 v[220:221], off
	s_waitcnt vmcnt(8)
	s_waitcnt lgkmcnt(0)
	s_barrier
	v_mfma_f32_16x16x32_bf16 v[56:59], v[120:123], v[180:183], v[56:59]
	v_mfma_f32_16x16x32_bf16 v[56:59], v[132:135], v[184:187], v[56:59]
	v_mfma_f32_16x16x32_bf16 v[52:55], v[144:147], v[180:183], v[52:55]
	v_mfma_f32_16x16x32_bf16 v[52:55], v[148:151], v[184:187], v[52:55]
	v_mfma_f32_16x16x32_bf16 v[48:51], v[120:123], v[188:191], v[48:51]
	v_mfma_f32_16x16x32_bf16 v[48:51], v[132:135], v[192:195], v[48:51]
	v_mfma_f32_16x16x32_bf16 v[44:47], v[144:147], v[188:191], v[44:47]
	v_mfma_f32_16x16x32_bf16 v[44:47], v[148:151], v[192:195], v[44:47]
	v_mfma_f32_16x16x32_bf16 v[32:35], v[120:123], v[196:199], v[32:35]
	v_mfma_f32_16x16x32_bf16 v[32:35], v[132:135], v[200:203], v[32:35]
	v_mfma_f32_16x16x32_bf16 v[28:31], v[144:147], v[196:199], v[28:31]
	v_mfma_f32_16x16x32_bf16 v[28:31], v[148:151], v[200:203], v[28:31]
	v_mfma_f32_16x16x32_bf16 v[16:19], v[120:123], v[204:207], v[16:19]
	v_mfma_f32_16x16x32_bf16 v[16:19], v[132:135], v[214:217], v[16:19]
	v_mfma_f32_16x16x32_bf16 v[12:15], v[144:147], v[204:207], v[12:15]
	v_mfma_f32_16x16x32_bf16 v[12:15], v[148:151], v[214:217], v[12:15]
	v_mfma_f32_16x16x32_bf16 v[64:67], v[152:155], v[180:183], v[64:67]
	v_mfma_f32_16x16x32_bf16 v[64:67], v[156:159], v[184:187], v[64:67]
	v_mfma_f32_16x16x32_bf16 v[60:63], v[166:169], v[180:183], v[60:63]
	v_mfma_f32_16x16x32_bf16 v[60:63], v[170:173], v[184:187], v[60:63]
	v_mfma_f32_16x16x32_bf16 v[40:43], v[152:155], v[188:191], v[40:43]
	v_mfma_f32_16x16x32_bf16 v[40:43], v[156:159], v[192:195], v[40:43]
	v_mfma_f32_16x16x32_bf16 v[36:39], v[166:169], v[188:191], v[36:39]
	v_mfma_f32_16x16x32_bf16 v[36:39], v[170:173], v[192:195], v[36:39]
	v_mfma_f32_16x16x32_bf16 v[24:27], v[152:155], v[196:199], v[24:27]
	v_mfma_f32_16x16x32_bf16 v[24:27], v[156:159], v[200:203], v[24:27]
	v_mfma_f32_16x16x32_bf16 v[20:23], v[166:169], v[196:199], v[20:23]
	v_mfma_f32_16x16x32_bf16 v[20:23], v[170:173], v[200:203], v[20:23]
	v_mfma_f32_16x16x32_bf16 v[8:11], v[152:155], v[204:207], v[8:11]
	v_mfma_f32_16x16x32_bf16 v[8:11], v[156:159], v[214:217], v[8:11]
	v_mfma_f32_16x16x32_bf16 v[4:7], v[166:169], v[204:207], v[4:7]
	v_mfma_f32_16x16x32_bf16 v[4:7], v[170:173], v[214:217], v[4:7]
	s_barrier
; #define PG8_MMA(ai, bj, At, Bt) do { __builtin_amdgcn_s_setprio(1); _Pragma("unroll") for (int m = 0; m < 4; ++m) _Pragma("unroll") for (int n = 0; n < 2; ++n) _Pragma("unroll") for (int k = 0; k < 2; ++k) \
;         acc[ai][bj][m][n] = __builtin_amdgcn_mfma_f32_16x16x32_bf16(Bt[n][k], At[m][k], acc[ai][bj][m][n], 0, 0, 0); __builtin_amdgcn_s_setprio(0); } while (0)
; #define PG8_WAIT_V(n) asm volatile("s_waitcnt vmcnt(" #n ")" ::: "memory")
; #define PG8_TRIP_HEAD(T) const int t = (T); const bool last = (t == nt - 2); \
;             const char* a1 = cA + (size_t)(t + 1) * kstep; \
;             const char* a2 = last ? nA : cA + (size_t)(t + 2) * kstep; const char* b2 = last ? nB : cB + (size_t)(t + 2) * kstep; \
;             const char* a3 = a2 + kstep; const char* b3 = b2 + kstep; \
;             if (last && has_next) S.a_ready(nxt);
; template <class Epi, class Sched, bool ALIGN_EPI = false, bool SP2 = false>
; __device__ __forceinline__ void gemm_phase(PG8_LAS unsigned char* lds, const Gemm g, const Sched& S, const Epi& E) {
;     ...
;         if constexpr (SP2) {
;             { PG8_TRIP_HEAD(0) PG8_TRIP_SP2(asm volatile("s_waitcnt vmcnt(%0)" :: "n"(8 + Epi::NST) : "memory"), PG8_MMAZ) }
;             for (int tt = 2; tt < nt; tt += 2) { PG8_TRIP_HEAD(tt) PG8_TRIP_SP2(PG8_WAIT_V(8), PG8_MMA) }
	ds_read_b128 v[120:123], v118
	ds_read_b128 v[132:135], v118 offset:1024
	ds_read_b128 v[144:147], v118 offset:2048
	ds_read_b128 v[148:151], v118 offset:3072
	ds_read_b128 v[152:155], v119
	ds_read_b128 v[156:159], v119 offset:1024
	ds_read_b128 v[166:169], v119 offset:2048
	ds_read_b128 v[170:173], v119 offset:3072
	s_mov_b32 m0, s31
	v_lshl_add_u64 v[220:221], v[218:219], 0, s[82:83]
	ds_read_b128 v[180:183], v178 offset:32768
	ds_read_b128 v[184:187], v178 offset:33792
	ds_read_b128 v[188:191], v178 offset:34816
	ds_read_b128 v[192:195], v178 offset:35840
	ds_read_b128 v[196:199], v178 offset:36864
	ds_read_b128 v[200:203], v178 offset:37888
	ds_read_b128 v[204:207], v178 offset:38912
	ds_read_b128 v[214:217], v178 offset:39936
	global_load_lds_dwordx4 v[220:221], off
	v_lshl_add_u64 v[220:221], v[218:219], 0, s[62:63]
	s_mov_b32 m0, s34
	s_nop 0
	global_load_lds_dwordx4 v[220:221], off
	s_waitcnt vmcnt(8)
	s_waitcnt lgkmcnt(0)
	s_barrier
	v_mfma_f32_16x16x32_bf16 v[140:143], v[120:123], v[180:183], v[140:143]
	v_mfma_f32_16x16x32_bf16 v[140:143], v[132:135], v[184:187], v[140:143]
	v_mfma_f32_16x16x32_bf16 v[136:139], v[144:147], v[180:183], v[136:139]
	v_mfma_f32_16x16x32_bf16 v[136:139], v[148:151], v[184:187], v[136:139]
	v_mfma_f32_16x16x32_bf16 v[112:115], v[120:123], v[188:191], v[112:115]
	v_mfma_f32_16x16x32_bf16 v[112:115], v[132:135], v[192:195], v[112:115]
	v_mfma_f32_16x16x32_bf16 v[108:111], v[144:147], v[188:191], v[108:111]
	v_mfma_f32_16x16x32_bf16 v[108:111], v[148:151], v[192:195], v[108:111]
	v_mfma_f32_16x16x32_bf16 v[96:99], v[120:123], v[196:199], v[96:99]
	v_mfma_f32_16x16x32_bf16 v[96:99], v[132:135], v[200:203], v[96:99]
	v_mfma_f32_16x16x32_bf16 v[92:95], v[144:147], v[196:199], v[92:95]
	v_mfma_f32_16x16x32_bf16 v[92:95], v[148:151], v[200:203], v[92:95]
	v_mfma_f32_16x16x32_bf16 v[80:83], v[120:123], v[204:207], v[80:83]
	v_mfma_f32_16x16x32_bf16 v[80:83], v[132:135], v[214:217], v[80:83]
	v_mfma_f32_16x16x32_bf16 v[76:79], v[144:147], v[204:207], v[76:79]
	v_mfma_f32_16x16x32_bf16 v[76:79], v[148:151], v[214:217], v[76:79]
	v_mfma_f32_16x16x32_bf16 v[128:131], v[152:155], v[180:183], v[128:131]
	v_mfma_f32_16x16x32_bf16 v[128:131], v[156:159], v[184:187], v[128:131]
	v_mfma_f32_16x16x32_bf16 v[124:127], v[166:169], v[180:183], v[124:127]
	v_mfma_f32_16x16x32_bf16 v[124:127], v[170:173], v[184:187], v[124:127]
	v_mfma_f32_16x16x32_bf16 v[104:107], v[152:155], v[188:191], v[104:107]
	v_mfma_f32_16x16x32_bf16 v[104:107], v[156:159], v[192:195], v[104:107]
	v_mfma_f32_16x16x32_bf16 v[100:103], v[166:169], v[188:191], v[100:103]
	v_mfma_f32_16x16x32_bf16 v[100:103], v[170:173], v[192:195], v[100:103]
	v_mfma_f32_16x16x32_bf16 v[88:91], v[152:155], v[196:199], v[88:91]
	v_mfma_f32_16x16x32_bf16 v[88:91], v[156:159], v[200:203], v[88:91]
	v_mfma_f32_16x16x32_bf16 v[84:87], v[166:169], v[196:199], v[84:87]
	v_mfma_f32_16x16x32_bf16 v[84:87], v[170:173], v[200:203], v[84:87]
	v_mfma_f32_16x16x32_bf16 v[72:75], v[152:155], v[204:207], v[72:75]
	v_mfma_f32_16x16x32_bf16 v[72:75], v[156:159], v[214:217], v[72:75]
	v_mfma_f32_16x16x32_bf16 v[68:71], v[166:169], v[204:207], v[68:71]
	v_mfma_f32_16x16x32_bf16 v[68:71], v[170:173], v[214:217], v[68:71]
	s_barrier
	s_mov_b32 m0, s43
	v_lshl_add_u64 v[220:221], v[208:209], 0, s[78:79]
	ds_read_b128 v[180:183], v178 offset:49152
	ds_read_b128 v[184:187], v178 offset:50176
	ds_read_b128 v[188:191], v178 offset:51200
	ds_read_b128 v[192:195], v178 offset:52224
	ds_read_b128 v[196:199], v178 offset:53248
	ds_read_b128 v[200:203], v178 offset:54272
	ds_read_b128 v[204:207], v178 offset:55296
	ds_read_b128 v[214:217], v178 offset:56320
	global_load_lds_dwordx4 v[220:221], off
	v_lshl_add_u64 v[220:221], v[208:209], 0, s[84:85]
	s_mov_b32 m0, s44
	s_nop 0
	global_load_lds_dwordx4 v[220:221], off
	v_lshl_add_u64 v[220:221], v[208:209], 0, s[54:55]
	s_mov_b32 m0, s45
	v_lshl_add_u64 v[208:209], v[208:209], 0, s[60:61]
	global_load_lds_dwordx4 v[220:221], off
	s_mov_b32 m0, s46
	s_nop 0
	global_load_lds_dwordx4 v[208:209], off
	v_lshl_add_u64 v[208:209], v[218:219], 0, s[78:79]
	s_mov_b32 m0, s36
	s_nop 0
	global_load_lds_dwordx4 v[208:209], off
	v_lshl_add_u64 v[208:209], v[218:219], 0, s[92:93]
	s_mov_b32 m0, s37
	s_nop 0
	global_load_lds_dwordx4 v[208:209], off
	s_waitcnt vmcnt(8)
	s_waitcnt lgkmcnt(0)
	s_barrier
	v_mfma_f32_16x16x32_bf16 v[56:59], v[120:123], v[180:183], v[56:59]
	v_mfma_f32_16x16x32_bf16 v[56:59], v[132:135], v[184:187], v[56:59]
	v_mfma_f32_16x16x32_bf16 v[52:55], v[144:147], v[180:183], v[52:55]
	v_mfma_f32_16x16x32_bf16 v[52:55], v[148:151], v[184:187], v[52:55]
	v_mfma_f32_16x16x32_bf16 v[48:51], v[120:123], v[188:191], v[48:51]
	v_mfma_f32_16x16x32_bf16 v[48:51], v[132:135], v[192:195], v[48:51]
	v_mfma_f32_16x16x32_bf16 v[44:47], v[144:147], v[188:191], v[44:47]
	v_mfma_f32_16x16x32_bf16 v[44:47], v[148:151], v[192:195], v[44:47]
	v_mfma_f32_16x16x32_bf16 v[32:35], v[120:123], v[196:199], v[32:35]
	v_mfma_f32_16x16x32_bf16 v[32:35], v[132:135], v[200:203], v[32:35]
	v_mfma_f32_16x16x32_bf16 v[28:31], v[144:147], v[196:199], v[28:31]
	v_mfma_f32_16x16x32_bf16 v[28:31], v[148:151], v[200:203], v[28:31]
	v_mfma_f32_16x16x32_bf16 v[16:19], v[120:123], v[204:207], v[16:19]
	v_mfma_f32_16x16x32_bf16 v[16:19], v[132:135], v[214:217], v[16:19]
	v_mfma_f32_16x16x32_bf16 v[12:15], v[144:147], v[204:207], v[12:15]
	v_mfma_f32_16x16x32_bf16 v[12:15], v[148:151], v[214:217], v[12:15]
	v_mfma_f32_16x16x32_bf16 v[64:67], v[152:155], v[180:183], v[64:67]
	v_mfma_f32_16x16x32_bf16 v[64:67], v[156:159], v[184:187], v[64:67]
	v_mfma_f32_16x16x32_bf16 v[60:63], v[166:169], v[180:183], v[60:63]
	v_mfma_f32_16x16x32_bf16 v[60:63], v[170:173], v[184:187], v[60:63]
	v_mfma_f32_16x16x32_bf16 v[40:43], v[152:155], v[188:191], v[40:43]
	v_mfma_f32_16x16x32_bf16 v[40:43], v[156:159], v[192:195], v[40:43]
	v_mfma_f32_16x16x32_bf16 v[36:39], v[166:169], v[188:191], v[36:39]
	v_mfma_f32_16x16x32_bf16 v[36:39], v[170:173], v[192:195], v[36:39]
	v_mfma_f32_16x16x32_bf16 v[24:27], v[152:155], v[196:199], v[24:27]
	v_mfma_f32_16x16x32_bf16 v[24:27], v[156:159], v[200:203], v[24:27]
	v_mfma_f32_16x16x32_bf16 v[20:23], v[166:169], v[196:199], v[20:23]
	v_mfma_f32_16x16x32_bf16 v[20:23], v[170:173], v[200:203], v[20:23]
	v_mfma_f32_16x16x32_bf16 v[8:11], v[152:155], v[204:207], v[8:11]
	v_mfma_f32_16x16x32_bf16 v[8:11], v[156:159], v[214:217], v[8:11]
	v_mfma_f32_16x16x32_bf16 v[4:7], v[166:169], v[204:207], v[4:7]
	v_mfma_f32_16x16x32_bf16 v[4:7], v[170:173], v[214:217], v[4:7]
	s_barrier
	s_add_i32 s26, s26, 2
	s_add_u32 s10, s10, 0x100
	s_addc_u32 s11, s11, 0
	s_add_u32 s24, s24, 0x100
	s_addc_u32 s25, s25, 0
	s_cmp_gt_u32 s26, 29
	s_cbranch_scc0 .LBB0_700
	s_and_b64 vcc, exec, s[16:17]
	s_cbranch_vccz .LBB0_703
	s_barrier
